# adds: x rows (P10) and X1B rows (P16) loaded non-temporal
# speedup vs baseline: 1.0040x; 1.0040x over previous
.LBB0_3478:
	s_add_i32 s14, s8, -7
	s_ashr_i32 s15, s14, 31
	s_lshl_b64 s[4:5], s[14:15], 11
	s_lshl_b64 s[18:19], s[14:15], 12
	s_add_u32 s16, s96, s18
	s_addc_u32 s17, s97, s19
	global_load_dwordx2 v[34:35], v234, s[16:17]
	global_load_dwordx2 v[36:37], v234, s[16:17] offset:512
	global_load_dwordx2 v[42:43], v234, s[16:17] offset:1024
	global_load_dwordx2 v[44:45], v234, s[16:17] offset:1536
	global_load_dwordx2 v[46:47], v234, s[16:17] offset:2048
	global_load_dwordx2 v[48:49], v234, s[16:17] offset:2560
	global_load_dwordx2 v[40:41], v234, s[16:17] offset:3072
	global_load_dwordx2 v[38:39], v234, s[16:17] offset:3584
	s_lshl_b64 s[14:15], s[14:15], 13
	s_add_u32 s14, s6, s14
	s_addc_u32 s15, s7, s15
	global_load_dwordx4 v[30:33], v178, s[14:15] nt
	global_load_dwordx4 v[26:29], v178, s[14:15] offset:1024 nt
	global_load_dwordx4 v[22:25], v178, s[14:15] offset:2048 nt
	global_load_dwordx4 v[18:21], v178, s[14:15] offset:3072 nt
	v_lshl_add_u64 v[2:3], s[14:15], 0, v[178:179]
	v_add_co_u32_e32 v2, vcc, s41, v2
	s_add_i32 s22, s8, -6
	s_nop 0
	v_addc_co_u32_e32 v3, vcc, 0, v3, vcc
	global_load_dwordx4 v[14:17], v[2:3], off nt
	global_load_dwordx4 v[10:13], v[2:3], off offset:1024 nt
	global_load_dwordx4 v[6:9], v[2:3], off offset:2048 nt
	s_nop 0
	global_load_dwordx4 v[2:5], v[2:3], off offset:3072 nt
	s_ashr_i32 s23, s22, 31
	s_lshl_b64 s[14:15], s[22:23], 11
	s_lshl_b64 s[16:17], s[22:23], 12
	s_add_u32 s20, s96, s16
	s_addc_u32 s21, s97, s17
	s_lshl_b64 s[22:23], s[22:23], 13
	s_add_u32 s22, s6, s22
	s_addc_u32 s23, s7, s23
	global_load_dwordx2 v[158:159], v234, s[20:21]
	global_load_dwordx4 v[134:137], v178, s[22:23] nt
	global_load_dwordx2 v[94:95], v234, s[20:21] offset:512
	v_lshlrev_b32_e32 v237, 2, v170
	s_waitcnt vmcnt(0)
	v_and_b32_e32 v85, 0xffff0000, v34
	v_and_b32_e32 v87, 0xffff0000, v35
	v_lshlrev_b32_e32 v84, 16, v34
	v_lshlrev_b32_e32 v86, 16, v35
	v_lshlrev_b32_e32 v81, 16, v37
	v_lshlrev_b32_e32 v80, 16, v36
	v_and_b32_e32 v83, 0xffff0000, v37
	v_and_b32_e32 v82, 0xffff0000, v36
	v_and_b32_e32 v75, 0xffff0000, v43
	v_lshlrev_b32_e32 v37, 16, v44
	v_and_b32_e32 v35, 0xffff0000, v44
	v_mul_f32_e32 v34, v87, v87
	v_mul_f32_e32 v36, v85, v85
	v_lshlrev_b32_e32 v70, 16, v42
	v_and_b32_e32 v71, 0xffff0000, v42
	v_lshlrev_b32_e32 v74, 16, v43
	v_lshlrev_b32_e32 v50, 16, v45
	v_and_b32_e32 v51, 0xffff0000, v45
	v_pk_mul_f32 v[42:43], v[82:83], v[82:83]
	v_mov_b32_e32 v45, v37
	v_mul_f32_e32 v44, v75, v75
	v_pk_fma_f32 v[54:55], v[86:87], v[86:87], v[34:35] op_sel_hi:[1,1,0]
	v_pk_fma_f32 v[56:57], v[84:85], v[84:85], v[36:37] op_sel_hi:[1,1,0]
	v_lshlrev_b32_e32 v52, 16, v40
	v_and_b32_e32 v53, 0xffff0000, v40
	v_mul_f32_e32 v40, v71, v71
	v_pk_fma_f32 v[42:43], v[80:81], v[80:81], v[42:43]
	v_pk_fma_f32 v[60:61], v[74:75], v[74:75], v[44:45] op_sel_hi:[1,1,0]
	v_mov_b32_e32 v36, v56
	v_mov_b32_e32 v44, v54
	v_mul_f32_e32 v63, v35, v35
	v_mul_f32_e32 v66, v50, v50
	v_mul_f32_e32 v67, v51, v51
	v_pk_fma_f32 v[58:59], v[70:71], v[70:71], v[40:41] op_sel_hi:[1,1,0]
	v_pk_add_f32 v[54:55], v[56:57], v[54:55]
	v_pk_add_f32 v[42:43], v[42:43], v[42:43] op_sel:[0,1] op_sel_hi:[1,0]
	v_pk_mul_f32 v[44:45], v[36:37], v[44:45]
	v_and_b32_e32 v79, 0xffff0000, v47
	v_and_b32_e32 v78, 0xffff0000, v46
	v_mov_b32_e32 v59, v66
	v_mov_b32_e32 v61, v67
	v_mov_b32_e32 v43, v63
	v_mov_b32_e32 v55, v45
	v_lshlrev_b32_e32 v77, 16, v47
	v_lshlrev_b32_e32 v76, 16, v46
	v_pk_mul_f32 v[46:47], v[78:79], v[78:79]
	v_pk_add_f32 v[56:57], v[58:59], v[60:61]
	v_pk_add_f32 v[42:43], v[54:55], v[42:43]
	v_pk_fma_f32 v[46:47], v[76:77], v[76:77], v[46:47]
	v_pk_add_f32 v[42:43], v[42:43], v[56:57]
	v_and_b32_e32 v73, 0xffff0000, v49
	v_and_b32_e32 v72, 0xffff0000, v48
	v_pk_add_f32 v[46:47], v[46:47], v[46:47] op_sel:[0,1] op_sel_hi:[1,0]
	v_lshlrev_b32_e32 v93, 16, v38
	v_and_b32_e32 v91, 0xffff0000, v38
	v_lshlrev_b32_e32 v88, 16, v39
	v_and_b32_e32 v89, 0xffff0000, v39
	v_pk_add_f32 v[38:39], v[42:43], v[42:43] op_sel:[0,1] op_sel_hi:[1,0]
	v_lshlrev_b32_e32 v65, 16, v49
	v_lshlrev_b32_e32 v64, 16, v48
	v_lshlrev_b32_e32 v62, 16, v41
	v_pk_mul_f32 v[48:49], v[72:73], v[72:73]
	v_and_b32_e32 v63, 0xffff0000, v41
	v_mov_b32_e32 v92, v38
	v_mov_b32_e32 v40, v46
	v_mov_b32_e32 v41, v93
	v_pk_fma_f32 v[48:49], v[64:65], v[64:65], v[48:49]
	v_pk_add_f32 v[38:39], v[38:39], v[46:47]
	v_pk_mul_f32 v[40:41], v[92:93], v[40:41]
	v_mul_f32_e32 v34, v91, v91
	v_mov_b32_e32 v39, v41
	v_pk_add_f32 v[40:41], v[48:49], v[48:49] op_sel:[0,1] op_sel_hi:[1,0]
	v_mul_f32_e32 v36, v88, v88
	v_mov_b32_e32 v41, v34
	v_mul_f32_e32 v34, v53, v53
	v_pk_add_f32 v[38:39], v[38:39], v[40:41]
	v_pk_fma_f32 v[40:41], v[52:53], v[52:53], v[34:35] op_sel_hi:[1,1,0]
	v_mul_f32_e32 v34, v63, v63
	v_mul_f32_e32 v44, v89, v89
	v_pk_fma_f32 v[42:43], v[62:63], v[62:63], v[34:35] op_sel_hi:[1,1,0]
	v_mov_b32_e32 v41, v36
	v_mov_b32_e32 v43, v44
	v_pk_add_f32 v[40:41], v[40:41], v[42:43]
	global_load_dwordx4 v[138:141], v178, s[22:23] offset:1024 nt
	global_load_dwordx2 v[168:169], v234, s[20:21] offset:1024
	global_load_dwordx4 v[66:69], v178, s[22:23] offset:2048 nt
	global_load_dwordx2 v[166:167], v234, s[20:21] offset:1536
	v_pk_add_f32 v[38:39], v[38:39], v[40:41]
	global_load_dwordx4 v[58:61], v178, s[22:23] offset:3072 nt
	global_load_dwordx2 v[96:97], v234, s[20:21] offset:2048
	v_add_f32_e32 v34, v38, v39
	ds_bpermute_b32 v36, v171, v34
	v_lshl_add_u64 v[38:39], s[22:23], 0, v[178:179]
	v_add_co_u32_e32 v38, vcc, s41, v38
	v_mov_b32_e32 v90, v93
	s_waitcnt lgkmcnt(0)
	v_add_f32_e32 v34, v34, v36
	ds_bpermute_b32 v36, v226, v34
	v_addc_co_u32_e32 v39, vcc, 0, v39, vcc
	global_load_dwordx4 v[54:57], v[38:39], off nt
	global_load_dwordx2 v[160:161], v234, s[20:21] offset:2560
	global_load_dwordx4 v[46:49], v[38:39], off offset:1024 nt
	global_load_dwordx2 v[182:183], v234, s[20:21] offset:3072
	global_load_dwordx4 v[42:45], v[38:39], off offset:2048 nt
	global_load_dwordx2 v[180:181], v234, s[20:21] offset:3584
	s_nop 0
	global_load_dwordx4 v[38:41], v[38:39], off offset:3072 nt
	s_waitcnt lgkmcnt(0)
	v_add_f32_e32 v34, v34, v36
	ds_bpermute_b32 v36, v228, v34
	ds_read_b128 v[98:101], v233
	ds_read_b128 v[102:105], v233 offset:1024
	s_add_u32 s20, s35, s18
	s_addc_u32 s21, s36, s19
	s_waitcnt lgkmcnt(2)
	v_add_f32_e32 v34, v34, v36
	ds_bpermute_b32 v36, v229, v34
	ds_read_b128 v[106:109], v233 offset:2048
	ds_read_b128 v[110:113], v233 offset:3072
	ds_read_b128 v[114:117], v233 offset:4096
	ds_read_b128 v[118:121], v233 offset:5120
	s_waitcnt lgkmcnt(4)
	v_add_f32_e32 v34, v34, v36
	ds_bpermute_b32 v36, v230, v34
	ds_read_b128 v[122:125], v233 offset:6144
	ds_read_b128 v[126:129], v233 offset:7168
	v_and_b32_e32 v207, 0xffff0000, v158
	v_and_b32_e32 v209, 0xffff0000, v159
	s_waitcnt lgkmcnt(2)
	v_add_f32_e32 v34, v34, v36
	ds_bpermute_b32 v36, v231, v34
	v_lshlrev_b32_e32 v206, 16, v158
	v_lshlrev_b32_e32 v208, 16, v159
	v_and_b32_e32 v205, 0xffff0000, v95
	v_and_b32_e32 v204, 0xffff0000, v94
	s_waitcnt lgkmcnt(0)
	v_add_f32_e32 v34, v34, v36
	v_fmamk_f32 v34, v34, 0x3a000000, v232
	v_cmp_gt_f32_e32 vcc, s43, v34
	v_mul_f32_e32 v36, 0x4b800000, v34
	v_lshlrev_b32_e32 v203, 16, v95
	v_cndmask_b32_e32 v34, v34, v36, vcc
	v_rsq_f32_e32 v34, v34
	v_lshlrev_b32_e32 v202, 16, v94
	s_add_u32 s24, s11, s18
	s_addc_u32 s25, s13, s19
	v_mul_f32_e32 v36, 0x45800000, v34
	v_cndmask_b32_e32 v36, v34, v36, vcc
	v_pk_mul_f32 v[84:85], v[36:37], v[84:85] op_sel_hi:[0,1]
	v_pk_mul_f32 v[86:87], v[36:37], v[86:87] op_sel_hi:[0,1]
	v_pk_fma_f32 v[142:143], v[98:99], v[84:85], v[30:31]
	v_pk_fma_f32 v[144:145], v[100:101], v[86:87], v[32:33]
	v_and_b32_sdwa v31, v142, v235 dst_sel:DWORD dst_unused:UNUSED_PAD src0_sel:WORD_1 src1_sel:DWORD
	v_add3_u32 v32, v142, v31, s44
	v_and_b32_sdwa v31, v145, v235 dst_sel:DWORD dst_unused:UNUSED_PAD src0_sel:WORD_1 src1_sel:DWORD
	v_and_b32_sdwa v33, v143, v235 dst_sel:DWORD dst_unused:UNUSED_PAD src0_sel:WORD_1 src1_sel:DWORD
	v_and_b32_sdwa v30, v144, v235 dst_sel:DWORD dst_unused:UNUSED_PAD src0_sel:WORD_1 src1_sel:DWORD
	v_add3_u32 v31, v145, v31, s44
	v_add3_u32 v33, v143, v33, s44
	v_add3_u32 v30, v144, v30, s44
	v_and_b32_e32 v31, 0xffff0000, v31
	v_and_b32_e32 v33, 0xffff0000, v33
	v_or_b32_sdwa v31, v31, v30 dst_sel:DWORD dst_unused:UNUSED_PAD src0_sel:DWORD src1_sel:WORD_1
	v_or_b32_sdwa v30, v33, v32 dst_sel:DWORD dst_unused:UNUSED_PAD src0_sel:DWORD src1_sel:WORD_1
	global_store_dwordx2 v234, v[30:31], s[20:21] nt
	v_mov_b32_e32 v30, v81
	v_mov_b32_e32 v81, v82
	v_mov_b32_e32 v31, v83
	v_pk_mul_f32 v[32:33], v[36:37], v[80:81] op_sel_hi:[0,1]
	v_pk_mul_f32 v[30:31], v[36:37], v[30:31] op_sel_hi:[0,1]
	v_pk_fma_f32 v[130:131], v[102:103], v[32:33], v[26:27]
	v_pk_fma_f32 v[132:133], v[104:105], v[30:31], v[28:29]
	v_and_b32_sdwa v27, v130, v235 dst_sel:DWORD dst_unused:UNUSED_PAD src0_sel:WORD_1 src1_sel:DWORD
	v_add3_u32 v28, v130, v27, s44
	v_and_b32_sdwa v27, v133, v235 dst_sel:DWORD dst_unused:UNUSED_PAD src0_sel:WORD_1 src1_sel:DWORD
	v_and_b32_sdwa v29, v131, v235 dst_sel:DWORD dst_unused:UNUSED_PAD src0_sel:WORD_1 src1_sel:DWORD
	v_and_b32_sdwa v26, v132, v235 dst_sel:DWORD dst_unused:UNUSED_PAD src0_sel:WORD_1 src1_sel:DWORD
	v_add3_u32 v27, v133, v27, s44
	v_add3_u32 v29, v131, v29, s44
	v_add3_u32 v26, v132, v26, s44
	v_and_b32_e32 v27, 0xffff0000, v27
	v_and_b32_e32 v29, 0xffff0000, v29
	v_or_b32_sdwa v27, v27, v26 dst_sel:DWORD dst_unused:UNUSED_PAD src0_sel:DWORD src1_sel:WORD_1
	v_or_b32_sdwa v26, v29, v28 dst_sel:DWORD dst_unused:UNUSED_PAD src0_sel:DWORD src1_sel:WORD_1
	v_mov_b32_e32 v28, v143
	v_mov_b32_e32 v29, v131
	global_store_dwordx2 v234, v[26:27], s[20:21] offset:512 nt
	v_mov_b32_e32 v26, v142
	v_mov_b32_e32 v27, v130
	v_pk_mul_f32 v[28:29], v[28:29], v[28:29]
	v_mov_b32_e32 v30, v145
	v_pk_fma_f32 v[26:27], v[26:27], v[26:27], v[28:29]
	v_mov_b32_e32 v28, v144
	v_mov_b32_e32 v29, v132
	v_pk_mul_f32 v[28:29], v[28:29], v[28:29]
	v_mov_b32_e32 v31, v133
	v_pk_fma_f32 v[28:29], v[30:31], v[30:31], v[28:29]
	v_pk_mul_f32 v[30:31], v[36:37], v[70:71] op_sel_hi:[0,1]
	v_pk_add_f32 v[26:27], v[26:27], v[28:29]
	v_pk_mul_f32 v[28:29], v[36:37], v[74:75] op_sel_hi:[0,1]
	v_pk_fma_f32 v[146:147], v[106:107], v[30:31], v[22:23]
	v_pk_fma_f32 v[148:149], v[108:109], v[28:29], v[24:25]
	v_and_b32_sdwa v23, v146, v235 dst_sel:DWORD dst_unused:UNUSED_PAD src0_sel:WORD_1 src1_sel:DWORD
	v_add3_u32 v24, v146, v23, s44
	v_and_b32_sdwa v23, v149, v235 dst_sel:DWORD dst_unused:UNUSED_PAD src0_sel:WORD_1 src1_sel:DWORD
	v_and_b32_sdwa v25, v147, v235 dst_sel:DWORD dst_unused:UNUSED_PAD src0_sel:WORD_1 src1_sel:DWORD
	v_and_b32_sdwa v22, v148, v235 dst_sel:DWORD dst_unused:UNUSED_PAD src0_sel:WORD_1 src1_sel:DWORD
	v_add3_u32 v23, v149, v23, s44
	v_add3_u32 v25, v147, v25, s44
	v_add3_u32 v22, v148, v22, s44
	v_and_b32_e32 v23, 0xffff0000, v23
	v_and_b32_e32 v25, 0xffff0000, v25
	v_or_b32_sdwa v23, v23, v22 dst_sel:DWORD dst_unused:UNUSED_PAD src0_sel:DWORD src1_sel:WORD_1
	v_or_b32_sdwa v22, v25, v24 dst_sel:DWORD dst_unused:UNUSED_PAD src0_sel:DWORD src1_sel:WORD_1
	global_store_dwordx2 v234, v[22:23], s[20:21] offset:1024 nt
	v_pk_mul_f32 v[22:23], v[148:149], v[148:149]
	v_pk_mul_f32 v[24:25], v[146:147], v[146:147]
	v_mov_b32_e32 v34, v37
	v_pk_mov_b32 v[28:29], v[24:25], v[22:23] op_sel:[1,0]
	v_mov_b32_e32 v25, v23
	v_pk_add_f32 v[22:23], v[24:25], v[28:29]
	v_pk_mul_f32 v[28:29], v[34:35], v[36:37] op_sel_hi:[1,0]
	v_pk_mul_f32 v[24:25], v[50:51], v[36:37] op_sel_hi:[1,0]
	v_pk_fma_f32 v[150:151], v[110:111], v[28:29], v[18:19]
	v_pk_fma_f32 v[152:153], v[112:113], v[24:25], v[20:21]
	v_and_b32_sdwa v19, v150, v235 dst_sel:DWORD dst_unused:UNUSED_PAD src0_sel:WORD_1 src1_sel:DWORD
	v_add3_u32 v20, v150, v19, s44
	v_and_b32_sdwa v19, v153, v235 dst_sel:DWORD dst_unused:UNUSED_PAD src0_sel:WORD_1 src1_sel:DWORD
	v_and_b32_sdwa v21, v151, v235 dst_sel:DWORD dst_unused:UNUSED_PAD src0_sel:WORD_1 src1_sel:DWORD
	v_and_b32_sdwa v18, v152, v235 dst_sel:DWORD dst_unused:UNUSED_PAD src0_sel:WORD_1 src1_sel:DWORD
	v_add3_u32 v19, v153, v19, s44
	v_add3_u32 v21, v151, v21, s44
	v_mov_b32_e32 v24, v76
	v_mov_b32_e32 v25, v78
	v_add3_u32 v18, v152, v18, s44
	v_and_b32_e32 v19, 0xffff0000, v19
	v_and_b32_e32 v21, 0xffff0000, v21
	v_pk_mul_f32 v[24:25], v[36:37], v[24:25] op_sel_hi:[0,1]
	v_mov_b32_e32 v78, v77
	v_or_b32_sdwa v19, v19, v18 dst_sel:DWORD dst_unused:UNUSED_PAD src0_sel:DWORD src1_sel:WORD_1
	v_or_b32_sdwa v18, v21, v20 dst_sel:DWORD dst_unused:UNUSED_PAD src0_sel:DWORD src1_sel:WORD_1
	v_pk_mul_f32 v[28:29], v[36:37], v[78:79] op_sel_hi:[0,1]
	v_pk_fma_f32 v[154:155], v[114:115], v[24:25], v[14:15]
	global_store_dwordx2 v234, v[18:19], s[20:21] offset:1536 nt
	v_mul_f32_e32 v18, v150, v150
	v_pk_fma_f32 v[50:51], v[116:117], v[28:29], v[16:17]
	v_and_b32_sdwa v15, v154, v235 dst_sel:DWORD dst_unused:UNUSED_PAD src0_sel:WORD_1 src1_sel:DWORD
	v_pk_fma_f32 v[18:19], v[150:151], v[150:151], v[18:19] op_sel_hi:[1,1,0]
	v_add3_u32 v16, v154, v15, s44
	v_and_b32_sdwa v15, v51, v235 dst_sel:DWORD dst_unused:UNUSED_PAD src0_sel:WORD_1 src1_sel:DWORD
	v_and_b32_sdwa v17, v155, v235 dst_sel:DWORD dst_unused:UNUSED_PAD src0_sel:WORD_1 src1_sel:DWORD
	v_mul_f32_e32 v18, v152, v152
	v_and_b32_sdwa v14, v50, v235 dst_sel:DWORD dst_unused:UNUSED_PAD src0_sel:WORD_1 src1_sel:DWORD
	v_add3_u32 v15, v51, v15, s44
	v_add3_u32 v17, v155, v17, s44
	v_pk_add_f32 v[26:27], v[26:27], v[26:27] op_sel_hi:[0,1]
	v_pk_add_f32 v[22:23], v[22:23], v[22:23] op_sel_hi:[0,1]
	v_pk_fma_f32 v[20:21], v[152:153], v[152:153], v[18:19] op_sel_hi:[1,1,0]
	v_add3_u32 v14, v50, v14, s44
	v_and_b32_e32 v15, 0xffff0000, v15
	v_and_b32_e32 v17, 0xffff0000, v17
	v_or_b32_sdwa v15, v15, v14 dst_sel:DWORD dst_unused:UNUSED_PAD src0_sel:DWORD src1_sel:WORD_1
	v_or_b32_sdwa v14, v17, v16 dst_sel:DWORD dst_unused:UNUSED_PAD src0_sel:DWORD src1_sel:WORD_1
	v_mul_f32_e32 v18, v154, v154
	v_mul_f32_e32 v20, v155, v155
	v_mul_f32_e32 v26, v50, v50
	v_mul_f32_e32 v22, v51, v51
	global_store_dwordx2 v234, v[14:15], s[20:21] offset:2048 nt
	v_pk_add_f32 v[14:15], v[18:19], v[20:21]
	v_pk_add_f32 v[16:17], v[22:23], v[26:27]
	s_waitcnt vmcnt(14)
	v_lshlrev_b32_e32 v191, 16, v166
	v_pk_add_f32 v[14:15], v[14:15], v[16:17]
	v_mov_b32_e32 v16, v65
	v_mov_b32_e32 v65, v72
	v_mov_b32_e32 v17, v73
	v_pk_mul_f32 v[18:19], v[36:37], v[64:65] op_sel_hi:[0,1]
	v_pk_mul_f32 v[16:17], v[36:37], v[16:17] op_sel_hi:[0,1]
	v_pk_fma_f32 v[162:163], v[118:119], v[18:19], v[10:11]
	v_pk_fma_f32 v[164:165], v[120:121], v[16:17], v[12:13]
	v_and_b32_sdwa v11, v162, v235 dst_sel:DWORD dst_unused:UNUSED_PAD src0_sel:WORD_1 src1_sel:DWORD
	v_add3_u32 v12, v162, v11, s44
	v_and_b32_sdwa v11, v165, v235 dst_sel:DWORD dst_unused:UNUSED_PAD src0_sel:WORD_1 src1_sel:DWORD
	v_and_b32_sdwa v13, v163, v235 dst_sel:DWORD dst_unused:UNUSED_PAD src0_sel:WORD_1 src1_sel:DWORD
	v_and_b32_sdwa v10, v164, v235 dst_sel:DWORD dst_unused:UNUSED_PAD src0_sel:WORD_1 src1_sel:DWORD
	v_add3_u32 v11, v165, v11, s44
	v_add3_u32 v13, v163, v13, s44
	v_add3_u32 v10, v164, v10, s44
	v_and_b32_e32 v11, 0xffff0000, v11
	v_and_b32_e32 v13, 0xffff0000, v13
	v_or_b32_sdwa v11, v11, v10 dst_sel:DWORD dst_unused:UNUSED_PAD src0_sel:DWORD src1_sel:WORD_1
	v_or_b32_sdwa v10, v13, v12 dst_sel:DWORD dst_unused:UNUSED_PAD src0_sel:DWORD src1_sel:WORD_1
	global_store_dwordx2 v234, v[10:11], s[20:21] offset:2560 nt
	v_pk_mul_f32 v[10:11], v[164:165], v[164:165]
	v_pk_mul_f32 v[12:13], v[162:163], v[162:163]
	v_pk_add_f32 v[14:15], v[14:15], v[14:15] op_sel_hi:[0,1]
	v_pk_mov_b32 v[16:17], v[12:13], v[10:11] op_sel:[1,0]
	v_mov_b32_e32 v13, v11
	v_pk_add_f32 v[10:11], v[12:13], v[16:17]
	v_pk_mul_f32 v[16:17], v[36:37], v[52:53] op_sel_hi:[0,1]
	v_pk_mul_f32 v[12:13], v[36:37], v[62:63] op_sel_hi:[0,1]
	v_pk_fma_f32 v[64:65], v[16:17], v[122:123], v[6:7]
	v_pk_fma_f32 v[156:157], v[12:13], v[124:125], v[8:9]
	v_and_b32_sdwa v7, v64, v235 dst_sel:DWORD dst_unused:UNUSED_PAD src0_sel:WORD_1 src1_sel:DWORD
	v_add3_u32 v8, v64, v7, s44
	v_and_b32_sdwa v7, v157, v235 dst_sel:DWORD dst_unused:UNUSED_PAD src0_sel:WORD_1 src1_sel:DWORD
	v_and_b32_sdwa v9, v65, v235 dst_sel:DWORD dst_unused:UNUSED_PAD src0_sel:WORD_1 src1_sel:DWORD
	v_and_b32_sdwa v6, v156, v235 dst_sel:DWORD dst_unused:UNUSED_PAD src0_sel:WORD_1 src1_sel:DWORD
	v_add3_u32 v7, v157, v7, s44
	v_add3_u32 v9, v65, v9, s44
	v_add3_u32 v6, v156, v6, s44
	v_and_b32_e32 v7, 0xffff0000, v7
	v_and_b32_e32 v9, 0xffff0000, v9
	v_pk_mul_f32 v[12:13], v[90:91], v[36:37] op_sel_hi:[1,0]
	v_or_b32_sdwa v7, v7, v6 dst_sel:DWORD dst_unused:UNUSED_PAD src0_sel:DWORD src1_sel:WORD_1
	v_or_b32_sdwa v6, v9, v8 dst_sel:DWORD dst_unused:UNUSED_PAD src0_sel:DWORD src1_sel:WORD_1
	v_pk_mul_f32 v[16:17], v[88:89], v[36:37] op_sel_hi:[1,0]
	v_pk_fma_f32 v[62:63], v[12:13], v[126:127], v[2:3]
	global_store_dwordx2 v234, v[6:7], s[20:21] offset:3072 nt
	v_mul_f32_e32 v6, v64, v64
	v_pk_fma_f32 v[52:53], v[16:17], v[128:129], v[4:5]
	v_and_b32_sdwa v3, v62, v235 dst_sel:DWORD dst_unused:UNUSED_PAD src0_sel:WORD_1 src1_sel:DWORD
	v_pk_fma_f32 v[6:7], v[64:65], v[64:65], v[6:7] op_sel_hi:[1,1,0]
	v_add3_u32 v4, v62, v3, s44
	v_and_b32_sdwa v3, v53, v235 dst_sel:DWORD dst_unused:UNUSED_PAD src0_sel:WORD_1 src1_sel:DWORD
	v_and_b32_sdwa v5, v63, v235 dst_sel:DWORD dst_unused:UNUSED_PAD src0_sel:WORD_1 src1_sel:DWORD
	v_mul_f32_e32 v6, v156, v156
	v_and_b32_sdwa v2, v52, v235 dst_sel:DWORD dst_unused:UNUSED_PAD src0_sel:WORD_1 src1_sel:DWORD
	v_add3_u32 v3, v53, v3, s44
	v_add3_u32 v5, v63, v5, s44
	v_pk_add_f32 v[10:11], v[10:11], v[10:11] op_sel_hi:[0,1]
	v_pk_fma_f32 v[8:9], v[156:157], v[156:157], v[6:7] op_sel_hi:[1,1,0]
	v_add3_u32 v2, v52, v2, s44
	v_and_b32_e32 v3, 0xffff0000, v3
	v_and_b32_e32 v5, 0xffff0000, v5
	v_or_b32_sdwa v3, v3, v2 dst_sel:DWORD dst_unused:UNUSED_PAD src0_sel:DWORD src1_sel:WORD_1
	v_or_b32_sdwa v2, v5, v4 dst_sel:DWORD dst_unused:UNUSED_PAD src0_sel:DWORD src1_sel:WORD_1
	v_mul_f32_e32 v6, v62, v62
	v_mul_f32_e32 v8, v63, v63
	v_mul_f32_e32 v14, v52, v52
	v_mul_f32_e32 v10, v53, v53
	global_store_dwordx2 v234, v[2:3], s[20:21] offset:3584 nt
	v_pk_add_f32 v[2:3], v[6:7], v[8:9]
	v_pk_add_f32 v[4:5], v[10:11], v[14:15]
	v_mul_f32_e32 v8, v207, v207
	v_pk_add_f32 v[2:3], v[2:3], v[4:5]
	v_mul_f32_e32 v4, v209, v209
	v_pk_fma_f32 v[4:5], v[208:209], v[208:209], v[4:5] op_sel_hi:[1,1,0]
	v_pk_mul_f32 v[6:7], v[204:205], v[204:205]
	v_pk_fma_f32 v[8:9], v[206:207], v[206:207], v[8:9] op_sel_hi:[1,1,0]
	v_pk_fma_f32 v[6:7], v[202:203], v[202:203], v[6:7]
	v_and_b32_e32 v189, 0xffff0000, v166
	v_mov_b32_e32 v190, v8
	v_mov_b32_e32 v10, v4
	v_mov_b32_e32 v11, v191
	v_mul_f32_e32 v12, v189, v189
	v_pk_add_f32 v[4:5], v[8:9], v[4:5]
	v_pk_mul_f32 v[8:9], v[190:191], v[10:11]
	v_pk_add_f32 v[6:7], v[6:7], v[6:7] op_sel:[0,1] op_sel_hi:[1,0]
	v_and_b32_e32 v199, 0xffff0000, v168
	v_and_b32_e32 v201, 0xffff0000, v169
	v_mov_b32_e32 v5, v9
	v_mov_b32_e32 v7, v12
	v_lshlrev_b32_e32 v198, 16, v168
	v_lshlrev_b32_e32 v200, 16, v169
	v_lshlrev_b32_e32 v196, 16, v167
	v_and_b32_e32 v197, 0xffff0000, v167
	v_pk_add_f32 v[4:5], v[4:5], v[6:7]
	v_mul_f32_e32 v6, v199, v199
	v_mul_f32_e32 v8, v201, v201
	v_mul_f32_e32 v13, v196, v196
	v_mul_f32_e32 v14, v197, v197
	v_pk_fma_f32 v[6:7], v[198:199], v[198:199], v[6:7] op_sel_hi:[1,1,0]
	v_pk_fma_f32 v[8:9], v[200:201], v[200:201], v[8:9] op_sel_hi:[1,1,0]
	v_mov_b32_e32 v7, v13
	v_mov_b32_e32 v9, v14
	v_pk_add_f32 v[6:7], v[6:7], v[8:9]
	s_waitcnt vmcnt(15)
	v_and_b32_e32 v195, 0xffff0000, v97
	v_and_b32_e32 v194, 0xffff0000, v96
	v_pk_add_f32 v[4:5], v[4:5], v[6:7]
	v_lshlrev_b32_e32 v193, 16, v97
	v_lshlrev_b32_e32 v192, 16, v96
	v_pk_mul_f32 v[6:7], v[194:195], v[194:195]
	s_waitcnt vmcnt(13)
	v_and_b32_e32 v187, 0xffff0000, v161
	v_pk_fma_f32 v[6:7], v[192:193], v[192:193], v[6:7]
	v_and_b32_e32 v186, 0xffff0000, v160
	v_pk_add_f32 v[6:7], v[6:7], v[6:7] op_sel:[0,1] op_sel_hi:[1,0]
	s_waitcnt vmcnt(9)
	v_lshlrev_b32_e32 v167, 16, v180
	v_pk_add_f32 v[4:5], v[4:5], v[4:5] op_sel:[0,1] op_sel_hi:[1,0]
	v_lshlrev_b32_e32 v185, 16, v161
	v_lshlrev_b32_e32 v184, 16, v160
	v_pk_mul_f32 v[8:9], v[186:187], v[186:187]
	v_mov_b32_e32 v166, v4
	v_mov_b32_e32 v10, v6
	v_mov_b32_e32 v11, v167
	v_pk_fma_f32 v[8:9], v[184:185], v[184:185], v[8:9]
	v_and_b32_e32 v161, 0xffff0000, v180
	v_pk_add_f32 v[4:5], v[4:5], v[6:7]
	v_pk_mul_f32 v[6:7], v[166:167], v[10:11]
	v_mul_f32_e32 v12, v161, v161
	v_mov_b32_e32 v5, v7
	v_pk_add_f32 v[6:7], v[8:9], v[8:9] op_sel:[0,1] op_sel_hi:[1,0]
	v_lshlrev_b32_e32 v168, 16, v182
	v_and_b32_e32 v169, 0xffff0000, v182
	v_lshlrev_b32_e32 v182, 16, v183
	v_and_b32_e32 v183, 0xffff0000, v183
	v_mov_b32_e32 v7, v12
	v_lshlrev_b32_e32 v158, 16, v181
	v_and_b32_e32 v159, 0xffff0000, v181
	v_pk_add_f32 v[4:5], v[4:5], v[6:7]
	v_mul_f32_e32 v6, v169, v169
	v_mul_f32_e32 v8, v183, v183
	v_mul_f32_e32 v13, v158, v158
	v_mul_f32_e32 v14, v159, v159
	v_pk_fma_f32 v[6:7], v[168:169], v[168:169], v[6:7] op_sel_hi:[1,1,0]
	v_pk_fma_f32 v[8:9], v[182:183], v[182:183], v[8:9] op_sel_hi:[1,1,0]
	v_mov_b32_e32 v7, v13
	v_mov_b32_e32 v9, v14
	v_pk_add_f32 v[6:7], v[6:7], v[8:9]
	s_add_u32 s26, s33, s4
	v_pk_add_f32 v[4:5], v[4:5], v[6:7]
	v_mov_b32_e32 v7, v2
	v_mov_b32_e32 v6, v4
	v_mov_b32_e32 v2, v5
	v_pk_add_f32 v[2:3], v[6:7], v[2:3]
	ds_bpermute_b32 v5, v171, v3
	ds_bpermute_b32 v4, v171, v2
	s_addc_u32 s27, s34, s5
	s_add_i32 s4, s8, -5
	s_ashr_i32 s5, s4, 31
	s_lshl_b64 s[18:19], s[4:5], 11
	s_waitcnt lgkmcnt(0)
	v_pk_add_f32 v[2:3], v[2:3], v[4:5]
	ds_bpermute_b32 v5, v226, v3
	ds_bpermute_b32 v4, v226, v2
	s_lshl_b64 s[20:21], s[4:5], 12
	s_add_u32 s28, s96, s20
	s_addc_u32 s29, s97, s21
	s_lshl_b64 s[4:5], s[4:5], 13
	s_waitcnt lgkmcnt(0)
	v_pk_add_f32 v[2:3], v[2:3], v[4:5]
	ds_bpermute_b32 v5, v228, v3
	ds_bpermute_b32 v4, v228, v2
	s_add_u32 s30, s6, s4
	s_addc_u32 s31, s7, s5
	ds_read_b128 v[26:29], v233 offset:8192
	ds_read_b128 v[30:33], v233 offset:16384
	ds_read_b128 v[90:93], v233 offset:9216
	ds_read_b128 v[94:97], v233 offset:17408
	ds_read_b128 v[82:85], v233 offset:10240
	ds_read_b128 v[86:89], v233 offset:18432
	s_waitcnt lgkmcnt(6)
	v_pk_add_f32 v[180:181], v[2:3], v[4:5]
	ds_bpermute_b32 v211, v229, v181
	ds_bpermute_b32 v210, v229, v180
	ds_read_b128 v[74:77], v233 offset:11264
	ds_read_b128 v[78:81], v233 offset:19456
	ds_read_b128 v[34:37], v233 offset:12288
	ds_read_b128 v[70:73], v233 offset:20480
	ds_read_b128 v[18:21], v233 offset:13312
	ds_read_b128 v[22:25], v233 offset:21504
	ds_read_b128 v[10:13], v233 offset:14336
	ds_read_b128 v[14:17], v233 offset:22528
	ds_read_b128 v[2:5], v233 offset:15360
	ds_read_b128 v[6:9], v233 offset:23552
	v_lshl_add_u64 v[212:213], s[30:31], 0, v[178:179]
	s_waitcnt lgkmcnt(10)
	v_pk_add_f32 v[180:181], v[180:181], v[210:211]
	ds_bpermute_b32 v211, v230, v181
	ds_bpermute_b32 v210, v230, v180
	s_add_u32 s22, s35, s16
	s_addc_u32 s23, s36, s17
	s_waitcnt lgkmcnt(0)
	v_pk_add_f32 v[180:181], v[180:181], v[210:211]
	ds_bpermute_b32 v211, v231, v181
	ds_bpermute_b32 v210, v231, v180
	s_waitcnt lgkmcnt(0)
	v_pk_add_f32 v[210:211], v[180:181], v[210:211]
	v_mov_b64_e32 v[180:181], s[12:13]
	v_pk_fma_f32 v[210:211], v[210:211], s[10:11], v[180:181] op_sel_hi:[1,0,0]
	s_nop 0
	v_mul_f32_e32 v160, 0x4b800000, v211
	v_cmp_gt_f32_e64 s[4:5], s43, v211
	v_cmp_gt_f32_e32 vcc, s43, v210
	s_nop 0
	v_cndmask_b32_e64 v160, v211, v160, s[4:5]
	v_rsq_f32_e32 v160, v160
	s_nop 0
	v_mul_f32_e32 v166, 0x45800000, v160
	v_cndmask_b32_e64 v160, v160, v166, s[4:5]
	v_pk_mul_f32 v[142:143], v[142:143], v[160:161] op_sel_hi:[1,0]
	v_pk_mul_f32 v[144:145], v[144:145], v[160:161] op_sel_hi:[1,0]
	v_pk_fma_f32 v[142:143], v[26:27], v[142:143], v[30:31]
	v_pk_fma_f32 v[144:145], v[28:29], v[144:145], v[32:33]
	v_bfe_u32 v166, v142, 16, 1
	v_add3_u32 v166, v142, v166, s44
	v_bfe_u32 v188, v143, 16, 1
	v_lshrrev_b32_e32 v166, 16, v166
	v_add3_u32 v188, v143, v188, s44
	v_and_or_b32 v214, v188, s42, v166
	v_med3_f32 v142, v142, s45, v236
	v_med3_f32 v143, v143, s45, v236
	v_mov_b32_e32 v188, 0
	v_cvt_pk_fp8_f32 v188, v142, v143
	v_bfe_u32 v166, v144, 16, 1
	v_add3_u32 v166, v144, v166, s44
	v_bfe_u32 v142, v145, 16, 1
	v_pk_mul_f32 v[130:131], v[130:131], v[160:161] op_sel_hi:[1,0]
	v_lshrrev_b32_e32 v166, 16, v166
	v_med3_f32 v143, v144, s45, v236
	v_med3_f32 v144, v145, s45, v236
	v_add3_u32 v142, v145, v142, s44
	v_pk_fma_f32 v[130:131], v[90:91], v[130:131], v[94:95]
	v_cvt_pk_fp8_f32 v188, v143, v144 op_sel:[0,0,1]
	v_and_or_b32 v215, v142, s42, v166
	v_bfe_u32 v142, v130, 16, 1
	v_bfe_u32 v143, v131, 16, 1
	v_add3_u32 v142, v130, v142, s44
	v_add3_u32 v143, v131, v143, s44
	v_med3_f32 v130, v130, s45, v236
	v_med3_f32 v131, v131, s45, v236
	v_mov_b32_e32 v144, 0
	v_pk_mul_f32 v[132:133], v[132:133], v[160:161] op_sel_hi:[1,0]
	v_cvt_pk_fp8_f32 v144, v130, v131
	v_pk_fma_f32 v[132:133], v[92:93], v[132:133], v[96:97]
	v_lshrrev_b32_e32 v142, 16, v142
	v_and_or_b32 v142, v143, s42, v142
	v_bfe_u32 v143, v132, 16, 1
	v_add3_u32 v143, v132, v143, s44
	v_bfe_u32 v130, v133, 16, 1
	v_med3_f32 v131, v132, s45, v236
	v_med3_f32 v132, v133, s45, v236
	v_lshrrev_b32_e32 v143, 16, v143
	v_cvt_pk_fp8_f32 v144, v131, v132 op_sel:[0,0,1]
	v_add3_u32 v130, v133, v130, s44
	v_and_or_b32 v143, v130, s42, v143
	v_pk_mul_f32 v[130:131], v[146:147], v[160:161] op_sel_hi:[1,0]
	global_store_dwordx2 v234, v[214:215], s[24:25]
	global_store_dword v237, v188, s[26:27]
	v_pk_fma_f32 v[130:131], v[82:83], v[130:131], v[86:87]
	global_store_dwordx2 v234, v[142:143], s[24:25] offset:512
	global_store_dword v237, v144, s[26:27] offset:256
	v_bfe_u32 v142, v130, 16, 1
	v_bfe_u32 v143, v131, 16, 1
	v_add3_u32 v142, v130, v142, s44
	v_add3_u32 v143, v131, v143, s44
	v_med3_f32 v130, v130, s45, v236
	v_med3_f32 v131, v131, s45, v236
	v_mov_b32_e32 v144, 0
	v_pk_mul_f32 v[132:133], v[148:149], v[160:161] op_sel_hi:[1,0]
	v_cvt_pk_fp8_f32 v144, v130, v131
	v_pk_fma_f32 v[132:133], v[84:85], v[132:133], v[88:89]
	v_lshrrev_b32_e32 v142, 16, v142
	v_and_or_b32 v142, v143, s42, v142
	v_bfe_u32 v143, v132, 16, 1
	v_add3_u32 v143, v132, v143, s44
	v_bfe_u32 v130, v133, 16, 1
	v_med3_f32 v131, v132, s45, v236
	v_med3_f32 v132, v133, s45, v236
	v_lshrrev_b32_e32 v143, 16, v143
	v_cvt_pk_fp8_f32 v144, v131, v132 op_sel:[0,0,1]
	v_add3_u32 v130, v133, v130, s44
	v_and_or_b32 v143, v130, s42, v143
	v_pk_mul_f32 v[130:131], v[150:151], v[160:161] op_sel_hi:[1,0]
	global_store_dwordx2 v234, v[142:143], s[24:25] offset:1024
	global_store_dword v237, v144, s[26:27] offset:512
	v_pk_fma_f32 v[130:131], v[130:131], v[74:75], v[78:79]
	v_pk_mul_f32 v[132:133], v[152:153], v[160:161] op_sel_hi:[1,0]
	v_bfe_u32 v142, v130, 16, 1
	v_bfe_u32 v143, v131, 16, 1
	v_add3_u32 v142, v130, v142, s44
	v_add3_u32 v143, v131, v143, s44
	v_med3_f32 v130, v130, s45, v236
	v_med3_f32 v131, v131, s45, v236
	v_mov_b32_e32 v144, 0
	v_pk_fma_f32 v[132:133], v[132:133], v[76:77], v[80:81]
	v_lshrrev_b32_e32 v142, 16, v142
	v_cvt_pk_fp8_f32 v144, v130, v131
	v_and_or_b32 v142, v143, s42, v142
	v_bfe_u32 v143, v132, 16, 1
	v_add3_u32 v143, v132, v143, s44
	v_bfe_u32 v130, v133, 16, 1
	v_lshrrev_b32_e32 v143, 16, v143
	v_med3_f32 v131, v132, s45, v236
	v_med3_f32 v132, v133, s45, v236
	v_add3_u32 v130, v133, v130, s44
	v_cvt_pk_fp8_f32 v144, v131, v132 op_sel:[0,0,1]
	v_and_or_b32 v143, v130, s42, v143
	v_pk_mul_f32 v[130:131], v[154:155], v[160:161] op_sel_hi:[1,0]
	global_store_dwordx2 v234, v[142:143], s[24:25] offset:1536
	global_store_dword v237, v144, s[26:27] offset:768
	v_pk_fma_f32 v[130:131], v[130:131], v[34:35], v[70:71]
	v_mov_b32_e32 v142, 0
	v_bfe_u32 v132, v130, 16, 1
	v_bfe_u32 v133, v131, 16, 1
	v_add3_u32 v132, v130, v132, s44
	v_add3_u32 v133, v131, v133, s44
	v_med3_f32 v130, v130, s45, v236
	v_med3_f32 v131, v131, s45, v236
	v_pk_mul_f32 v[50:51], v[50:51], v[160:161] op_sel_hi:[1,0]
	v_cvt_pk_fp8_f32 v142, v130, v131
	v_pk_fma_f32 v[50:51], v[50:51], v[36:37], v[72:73]
	v_lshrrev_b32_e32 v132, 16, v132
	v_and_or_b32 v132, v133, s42, v132
	v_bfe_u32 v133, v50, 16, 1
	v_add3_u32 v133, v50, v133, s44
	v_bfe_u32 v130, v51, 16, 1
	v_med3_f32 v50, v50, s45, v236
	v_med3_f32 v131, v51, s45, v236
	v_lshrrev_b32_e32 v133, 16, v133
	v_cvt_pk_fp8_f32 v142, v50, v131 op_sel:[0,0,1]
	v_add3_u32 v50, v51, v130, s44
	v_and_or_b32 v133, v50, s42, v133
	v_pk_mul_f32 v[50:51], v[162:163], v[160:161] op_sel_hi:[1,0]
	global_store_dwordx2 v234, v[132:133], s[24:25] offset:2048
	global_store_dword v237, v142, s[26:27] offset:1024
	v_pk_fma_f32 v[50:51], v[50:51], v[18:19], v[22:23]
	v_pk_mul_f32 v[130:131], v[164:165], v[160:161] op_sel_hi:[1,0]
	v_bfe_u32 v132, v50, 16, 1
	v_bfe_u32 v133, v51, 16, 1
	v_add3_u32 v132, v50, v132, s44
	v_add3_u32 v133, v51, v133, s44
	v_med3_f32 v50, v50, s45, v236
	v_med3_f32 v51, v51, s45, v236
	v_mov_b32_e32 v142, 0
	v_pk_fma_f32 v[130:131], v[130:131], v[20:21], v[24:25]
	v_lshrrev_b32_e32 v132, 16, v132
	v_cvt_pk_fp8_f32 v142, v50, v51
	v_and_or_b32 v132, v133, s42, v132
	v_bfe_u32 v133, v130, 16, 1
	v_add3_u32 v133, v130, v133, s44
	v_bfe_u32 v50, v131, 16, 1
	v_lshrrev_b32_e32 v133, 16, v133
	v_med3_f32 v51, v130, s45, v236
	v_med3_f32 v130, v131, s45, v236
	v_add3_u32 v50, v131, v50, s44
	v_cvt_pk_fp8_f32 v142, v51, v130 op_sel:[0,0,1]
	v_and_or_b32 v133, v50, s42, v133
	v_pk_mul_f32 v[50:51], v[64:65], v[160:161] op_sel_hi:[1,0]
	global_store_dwordx2 v234, v[132:133], s[24:25] offset:2560
	global_store_dword v237, v142, s[26:27] offset:1280
	v_pk_fma_f32 v[50:51], v[50:51], v[10:11], v[14:15]
	v_pk_mul_f32 v[64:65], v[156:157], v[160:161] op_sel_hi:[1,0]
	v_bfe_u32 v130, v50, 16, 1
	v_bfe_u32 v131, v51, 16, 1
	v_add3_u32 v130, v50, v130, s44
	v_add3_u32 v131, v51, v131, s44
	v_med3_f32 v50, v50, s45, v236
	v_med3_f32 v51, v51, s45, v236
	v_mov_b32_e32 v132, 0
	v_pk_fma_f32 v[64:65], v[64:65], v[12:13], v[16:17]
	v_lshrrev_b32_e32 v130, 16, v130
	v_cvt_pk_fp8_f32 v132, v50, v51
	v_and_or_b32 v130, v131, s42, v130
	v_bfe_u32 v131, v64, 16, 1
	v_add3_u32 v131, v64, v131, s44
	v_bfe_u32 v50, v65, 16, 1
	v_lshrrev_b32_e32 v131, 16, v131
	v_med3_f32 v51, v64, s45, v236
	v_med3_f32 v64, v65, s45, v236
	v_add3_u32 v50, v65, v50, s44
	v_cvt_pk_fp8_f32 v132, v51, v64 op_sel:[0,0,1]
	v_and_or_b32 v131, v50, s42, v131
	v_pk_mul_f32 v[50:51], v[62:63], v[160:161] op_sel_hi:[1,0]
	v_mov_b32_e32 v64, 0
	v_pk_fma_f32 v[50:51], v[50:51], v[2:3], v[6:7]
	v_pk_mul_f32 v[52:53], v[52:53], v[160:161] op_sel_hi:[1,0]
	v_bfe_u32 v62, v50, 16, 1
	v_bfe_u32 v63, v51, 16, 1
	v_add3_u32 v62, v50, v62, s44
	v_add3_u32 v63, v51, v63, s44
	v_med3_f32 v50, v50, s45, v236
	v_med3_f32 v51, v51, s45, v236
	v_cvt_pk_fp8_f32 v64, v50, v51
	v_pk_fma_f32 v[52:53], v[52:53], v[4:5], v[8:9]
	v_lshrrev_b32_e32 v62, 16, v62
	v_and_or_b32 v62, v63, s42, v62
	v_bfe_u32 v63, v52, 16, 1
	v_add3_u32 v63, v52, v63, s44
	v_med3_f32 v51, v52, s45, v236
	v_med3_f32 v52, v53, s45, v236
	v_bfe_u32 v50, v53, 16, 1
	v_cvt_pk_fp8_f32 v64, v51, v52 op_sel:[0,0,1]
	v_lshrrev_b32_e32 v63, 16, v63
	v_add3_u32 v50, v53, v50, s44
	v_and_or_b32 v63, v50, s42, v63
	global_store_dwordx2 v234, v[130:131], s[24:25] offset:3072
	global_store_dword v237, v132, s[26:27] offset:1536
	global_store_dwordx2 v234, v[62:63], s[24:25] offset:3584
	global_store_dword v237, v64, s[26:27] offset:1792
	global_load_dwordx2 v[220:221], v234, s[28:29]
	global_load_dwordx4 v[162:165], v178, s[30:31] nt
	global_load_dwordx2 v[222:223], v234, s[28:29] offset:512
	global_load_dwordx4 v[154:157], v178, s[30:31] offset:1024 nt
	global_load_dwordx2 v[224:225], v234, s[28:29] offset:1024
	global_load_dwordx4 v[150:153], v178, s[30:31] offset:2048 nt
	global_load_dwordx2 v[238:239], v234, s[28:29] offset:1536
	global_load_dwordx4 v[146:149], v178, s[30:31] offset:3072 nt
	global_load_dwordx2 v[240:241], v234, s[28:29] offset:2048
	v_add_co_u32_e64 v50, s[4:5], s41, v212
	v_mul_f32_e32 v52, 0x4b800000, v210
	s_nop 0
	v_addc_co_u32_e64 v51, s[4:5], 0, v213, s[4:5]
	v_cndmask_b32_e32 v52, v210, v52, vcc
	global_load_dwordx4 v[142:145], v[50:51], off nt
	global_load_dwordx2 v[242:243], v234, s[28:29] offset:2560
	global_load_dwordx4 v[130:133], v[50:51], off offset:1024 nt
	global_load_dwordx2 v[218:219], v234, s[28:29] offset:3072
	v_rsq_f32_e32 v160, v52
	global_load_dwordx4 v[62:65], v[50:51], off offset:2048 nt
	global_load_dwordx2 v[244:245], v234, s[28:29] offset:3584
	s_nop 0
	global_load_dwordx4 v[50:53], v[50:51], off offset:3072 nt
	v_mov_b32_e32 v188, v191
	s_add_u32 s26, s11, s16
	v_mul_f32_e32 v166, 0x45800000, v160
	v_cndmask_b32_e32 v166, v160, v166, vcc
	v_pk_mul_f32 v[206:207], v[166:167], v[206:207] op_sel_hi:[0,1]
	v_pk_mul_f32 v[208:209], v[166:167], v[208:209] op_sel_hi:[0,1]
	v_pk_fma_f32 v[214:215], v[98:99], v[206:207], v[134:135]
	v_pk_fma_f32 v[216:217], v[100:101], v[208:209], v[136:137]
	v_and_b32_sdwa v135, v214, v235 dst_sel:DWORD dst_unused:UNUSED_PAD src0_sel:WORD_1 src1_sel:DWORD
	v_add3_u32 v136, v214, v135, s44
	v_and_b32_sdwa v135, v217, v235 dst_sel:DWORD dst_unused:UNUSED_PAD src0_sel:WORD_1 src1_sel:DWORD
	v_and_b32_sdwa v137, v215, v235 dst_sel:DWORD dst_unused:UNUSED_PAD src0_sel:WORD_1 src1_sel:DWORD
	v_and_b32_sdwa v134, v216, v235 dst_sel:DWORD dst_unused:UNUSED_PAD src0_sel:WORD_1 src1_sel:DWORD
	v_add3_u32 v135, v217, v135, s44
	v_add3_u32 v137, v215, v137, s44
	v_add3_u32 v134, v216, v134, s44
	v_and_b32_e32 v135, 0xffff0000, v135
	v_and_b32_e32 v137, 0xffff0000, v137
	v_or_b32_sdwa v135, v135, v134 dst_sel:DWORD dst_unused:UNUSED_PAD src0_sel:DWORD src1_sel:WORD_1
	v_or_b32_sdwa v134, v137, v136 dst_sel:DWORD dst_unused:UNUSED_PAD src0_sel:DWORD src1_sel:WORD_1
	global_store_dwordx2 v234, v[134:135], s[22:23] nt
	v_mov_b32_e32 v134, v203
	v_mov_b32_e32 v203, v204
	v_mov_b32_e32 v135, v205
	v_pk_mul_f32 v[136:137], v[166:167], v[202:203] op_sel_hi:[0,1]
	v_pk_mul_f32 v[134:135], v[166:167], v[134:135] op_sel_hi:[0,1]
	v_pk_fma_f32 v[210:211], v[102:103], v[136:137], v[138:139]
	v_pk_fma_f32 v[212:213], v[104:105], v[134:135], v[140:141]
	v_and_b32_sdwa v135, v210, v235 dst_sel:DWORD dst_unused:UNUSED_PAD src0_sel:WORD_1 src1_sel:DWORD
	v_add3_u32 v136, v210, v135, s44
	v_and_b32_sdwa v135, v213, v235 dst_sel:DWORD dst_unused:UNUSED_PAD src0_sel:WORD_1 src1_sel:DWORD
	v_and_b32_sdwa v137, v211, v235 dst_sel:DWORD dst_unused:UNUSED_PAD src0_sel:WORD_1 src1_sel:DWORD
	v_and_b32_sdwa v134, v212, v235 dst_sel:DWORD dst_unused:UNUSED_PAD src0_sel:WORD_1 src1_sel:DWORD
	v_add3_u32 v135, v213, v135, s44
	v_add3_u32 v137, v211, v137, s44
	v_add3_u32 v134, v212, v134, s44
	v_and_b32_e32 v135, 0xffff0000, v135
	v_and_b32_e32 v137, 0xffff0000, v137
	v_or_b32_sdwa v135, v135, v134 dst_sel:DWORD dst_unused:UNUSED_PAD src0_sel:DWORD src1_sel:WORD_1
	v_or_b32_sdwa v134, v137, v136 dst_sel:DWORD dst_unused:UNUSED_PAD src0_sel:DWORD src1_sel:WORD_1
	v_mov_b32_e32 v136, v215
	v_mov_b32_e32 v137, v211
	global_store_dwordx2 v234, v[134:135], s[22:23] offset:512 nt
	v_mov_b32_e32 v134, v214
	v_mov_b32_e32 v135, v210
	v_pk_mul_f32 v[136:137], v[136:137], v[136:137]
	v_mov_b32_e32 v138, v217
	v_pk_fma_f32 v[134:135], v[134:135], v[134:135], v[136:137]
	v_mov_b32_e32 v136, v216
	v_mov_b32_e32 v137, v212
	v_pk_mul_f32 v[136:137], v[136:137], v[136:137]
	v_mov_b32_e32 v139, v213
	v_pk_fma_f32 v[136:137], v[138:139], v[138:139], v[136:137]
	v_pk_mul_f32 v[138:139], v[166:167], v[198:199] op_sel_hi:[0,1]
	v_pk_add_f32 v[134:135], v[134:135], v[136:137]
	v_pk_mul_f32 v[136:137], v[166:167], v[200:201] op_sel_hi:[0,1]
	v_pk_fma_f32 v[66:67], v[106:107], v[138:139], v[66:67]
	v_pk_fma_f32 v[68:69], v[108:109], v[136:137], v[68:69]
	v_pk_add_f32 v[134:135], v[134:135], v[134:135] op_sel_hi:[0,1]
	v_and_b32_sdwa v137, v69, v235 dst_sel:DWORD dst_unused:UNUSED_PAD src0_sel:WORD_1 src1_sel:DWORD
	v_and_b32_sdwa v138, v67, v235 dst_sel:DWORD dst_unused:UNUSED_PAD src0_sel:WORD_1 src1_sel:DWORD
	v_and_b32_sdwa v134, v68, v235 dst_sel:DWORD dst_unused:UNUSED_PAD src0_sel:WORD_1 src1_sel:DWORD
	v_and_b32_sdwa v136, v66, v235 dst_sel:DWORD dst_unused:UNUSED_PAD src0_sel:WORD_1 src1_sel:DWORD
	v_add3_u32 v137, v69, v137, s44
	v_add3_u32 v138, v67, v138, s44
	v_add3_u32 v136, v66, v136, s44
	v_add3_u32 v134, v68, v134, s44
	v_and_b32_e32 v137, 0xffff0000, v137
	v_and_b32_e32 v138, 0xffff0000, v138
	v_or_b32_sdwa v137, v137, v134 dst_sel:DWORD dst_unused:UNUSED_PAD src0_sel:DWORD src1_sel:WORD_1
	v_or_b32_sdwa v136, v138, v136 dst_sel:DWORD dst_unused:UNUSED_PAD src0_sel:DWORD src1_sel:WORD_1
	global_store_dwordx2 v234, v[136:137], s[22:23] offset:1024 nt
	v_pk_mul_f32 v[136:137], v[68:69], v[68:69]
	v_pk_mul_f32 v[138:139], v[66:67], v[66:67]
	v_mov_b32_e32 v160, v167
	v_pk_mov_b32 v[140:141], v[138:139], v[136:137] op_sel:[1,0]
	v_mov_b32_e32 v139, v137
	v_pk_add_f32 v[136:137], v[138:139], v[140:141]
	v_pk_mul_f32 v[138:139], v[196:197], v[166:167] op_sel_hi:[1,0]
	v_pk_mul_f32 v[140:141], v[188:189], v[166:167] op_sel_hi:[1,0]
	v_pk_fma_f32 v[60:61], v[112:113], v[138:139], v[60:61]
	v_pk_fma_f32 v[58:59], v[110:111], v[140:141], v[58:59]
	v_pk_add_f32 v[136:137], v[136:137], v[136:137] op_sel_hi:[0,1]
	v_and_b32_sdwa v138, v61, v235 dst_sel:DWORD dst_unused:UNUSED_PAD src0_sel:WORD_1 src1_sel:DWORD
	v_and_b32_sdwa v139, v59, v235 dst_sel:DWORD dst_unused:UNUSED_PAD src0_sel:WORD_1 src1_sel:DWORD
	v_and_b32_sdwa v134, v60, v235 dst_sel:DWORD dst_unused:UNUSED_PAD src0_sel:WORD_1 src1_sel:DWORD
	v_and_b32_sdwa v136, v58, v235 dst_sel:DWORD dst_unused:UNUSED_PAD src0_sel:WORD_1 src1_sel:DWORD
	v_add3_u32 v138, v61, v138, s44
	v_add3_u32 v139, v59, v139, s44
	v_add3_u32 v136, v58, v136, s44
	v_add3_u32 v134, v60, v134, s44
	v_and_b32_e32 v138, 0xffff0000, v138
	v_and_b32_e32 v140, 0xffff0000, v139
	v_or_b32_sdwa v139, v138, v134 dst_sel:DWORD dst_unused:UNUSED_PAD src0_sel:DWORD src1_sel:WORD_1
	v_or_b32_sdwa v138, v140, v136 dst_sel:DWORD dst_unused:UNUSED_PAD src0_sel:DWORD src1_sel:WORD_1
	v_mul_f32_e32 v134, v58, v58
	v_mov_b32_e32 v188, v192
	v_mov_b32_e32 v189, v194
	v_mov_b32_e32 v194, v193
	global_store_dwordx2 v234, v[138:139], s[22:23] offset:1536 nt
	v_pk_fma_f32 v[138:139], v[58:59], v[58:59], v[134:135] op_sel_hi:[1,1,0]
	v_mul_f32_e32 v134, v60, v60
	v_pk_mul_f32 v[188:189], v[166:167], v[188:189] op_sel_hi:[0,1]
	v_pk_mul_f32 v[190:191], v[166:167], v[194:195] op_sel_hi:[0,1]
	v_pk_fma_f32 v[140:141], v[60:61], v[60:61], v[134:135] op_sel_hi:[1,1,0]
	v_pk_fma_f32 v[56:57], v[116:117], v[190:191], v[56:57]
	v_pk_fma_f32 v[54:55], v[114:115], v[188:189], v[54:55]
	v_and_b32_sdwa v138, v57, v235 dst_sel:DWORD dst_unused:UNUSED_PAD src0_sel:WORD_1 src1_sel:DWORD
	v_and_b32_sdwa v140, v55, v235 dst_sel:DWORD dst_unused:UNUSED_PAD src0_sel:WORD_1 src1_sel:DWORD
	v_and_b32_sdwa v134, v56, v235 dst_sel:DWORD dst_unused:UNUSED_PAD src0_sel:WORD_1 src1_sel:DWORD
	v_and_b32_sdwa v136, v54, v235 dst_sel:DWORD dst_unused:UNUSED_PAD src0_sel:WORD_1 src1_sel:DWORD
	v_add3_u32 v138, v57, v138, s44
	v_add3_u32 v140, v55, v140, s44
	v_add3_u32 v136, v54, v136, s44
	v_add3_u32 v134, v56, v134, s44
	v_and_b32_e32 v138, 0xffff0000, v138
	v_and_b32_e32 v140, 0xffff0000, v140
	v_or_b32_sdwa v189, v138, v134 dst_sel:DWORD dst_unused:UNUSED_PAD src0_sel:DWORD src1_sel:WORD_1
	v_or_b32_sdwa v188, v140, v136 dst_sel:DWORD dst_unused:UNUSED_PAD src0_sel:DWORD src1_sel:WORD_1
	v_mul_f32_e32 v138, v54, v54
	v_mul_f32_e32 v140, v55, v55
	v_mul_f32_e32 v134, v56, v56
	v_mul_f32_e32 v136, v57, v57
	v_pk_add_f32 v[138:139], v[138:139], v[140:141]
	v_pk_add_f32 v[134:135], v[136:137], v[134:135]
	v_mov_b32_e32 v136, v185
	v_mov_b32_e32 v137, v187
	v_mov_b32_e32 v185, v186
	v_pk_add_f32 v[134:135], v[138:139], v[134:135]
	v_pk_mul_f32 v[136:137], v[166:167], v[136:137] op_sel_hi:[0,1]
	v_pk_mul_f32 v[138:139], v[166:167], v[184:185] op_sel_hi:[0,1]
	v_pk_fma_f32 v[46:47], v[118:119], v[138:139], v[46:47]
	v_pk_fma_f32 v[48:49], v[120:121], v[136:137], v[48:49]
	v_pk_add_f32 v[134:135], v[134:135], v[134:135] op_sel_hi:[0,1]
	v_and_b32_sdwa v137, v49, v235 dst_sel:DWORD dst_unused:UNUSED_PAD src0_sel:WORD_1 src1_sel:DWORD
	v_and_b32_sdwa v138, v47, v235 dst_sel:DWORD dst_unused:UNUSED_PAD src0_sel:WORD_1 src1_sel:DWORD
	v_and_b32_sdwa v134, v48, v235 dst_sel:DWORD dst_unused:UNUSED_PAD src0_sel:WORD_1 src1_sel:DWORD
	v_and_b32_sdwa v136, v46, v235 dst_sel:DWORD dst_unused:UNUSED_PAD src0_sel:WORD_1 src1_sel:DWORD
	v_add3_u32 v137, v49, v137, s44
	v_add3_u32 v138, v47, v138, s44
	v_add3_u32 v136, v46, v136, s44
	v_add3_u32 v134, v48, v134, s44
	v_and_b32_e32 v137, 0xffff0000, v137
	v_and_b32_e32 v138, 0xffff0000, v138
	v_or_b32_sdwa v137, v137, v134 dst_sel:DWORD dst_unused:UNUSED_PAD src0_sel:DWORD src1_sel:WORD_1
	v_or_b32_sdwa v136, v138, v136 dst_sel:DWORD dst_unused:UNUSED_PAD src0_sel:DWORD src1_sel:WORD_1
	global_store_dwordx2 v234, v[136:137], s[22:23] offset:2560 nt
	v_pk_mul_f32 v[136:137], v[48:49], v[48:49]
	v_pk_mul_f32 v[138:139], v[46:47], v[46:47]
	v_pk_mul_f32 v[160:161], v[160:161], v[166:167] op_sel_hi:[1,0]
	v_pk_mov_b32 v[140:141], v[138:139], v[136:137] op_sel:[1,0]
	v_mov_b32_e32 v139, v137
	v_pk_add_f32 v[136:137], v[138:139], v[140:141]
	v_pk_mul_f32 v[138:139], v[166:167], v[182:183] op_sel_hi:[0,1]
	v_pk_mul_f32 v[140:141], v[166:167], v[168:169] op_sel_hi:[0,1]
	v_pk_fma_f32 v[42:43], v[122:123], v[140:141], v[42:43]
	v_pk_fma_f32 v[44:45], v[124:125], v[138:139], v[44:45]
	v_pk_add_f32 v[136:137], v[136:137], v[136:137] op_sel_hi:[0,1]
	v_and_b32_sdwa v138, v45, v235 dst_sel:DWORD dst_unused:UNUSED_PAD src0_sel:WORD_1 src1_sel:DWORD
	v_and_b32_sdwa v139, v43, v235 dst_sel:DWORD dst_unused:UNUSED_PAD src0_sel:WORD_1 src1_sel:DWORD
	v_and_b32_sdwa v134, v44, v235 dst_sel:DWORD dst_unused:UNUSED_PAD src0_sel:WORD_1 src1_sel:DWORD
	v_and_b32_sdwa v136, v42, v235 dst_sel:DWORD dst_unused:UNUSED_PAD src0_sel:WORD_1 src1_sel:DWORD
	v_add3_u32 v138, v45, v138, s44
	v_add3_u32 v139, v43, v139, s44
	v_add3_u32 v136, v42, v136, s44
	v_add3_u32 v134, v44, v134, s44
	v_and_b32_e32 v138, 0xffff0000, v138
	v_and_b32_e32 v140, 0xffff0000, v139
	v_or_b32_sdwa v139, v138, v134 dst_sel:DWORD dst_unused:UNUSED_PAD src0_sel:DWORD src1_sel:WORD_1
	v_or_b32_sdwa v138, v140, v136 dst_sel:DWORD dst_unused:UNUSED_PAD src0_sel:DWORD src1_sel:WORD_1
	v_mul_f32_e32 v134, v42, v42
	global_store_dwordx2 v234, v[138:139], s[22:23] offset:3072 nt
	v_pk_fma_f32 v[138:139], v[42:43], v[42:43], v[134:135] op_sel_hi:[1,1,0]
	v_mul_f32_e32 v134, v44, v44
	v_pk_mul_f32 v[158:159], v[158:159], v[166:167] op_sel_hi:[1,0]
	s_waitcnt vmcnt(46)
	v_pk_fma_f32 v[38:39], v[126:127], v[160:161], v[38:39]
	v_pk_fma_f32 v[140:141], v[44:45], v[44:45], v[134:135] op_sel_hi:[1,1,0]
	v_pk_fma_f32 v[40:41], v[128:129], v[158:159], v[40:41]
	v_and_b32_sdwa v134, v38, v235 dst_sel:DWORD dst_unused:UNUSED_PAD src0_sel:WORD_1 src1_sel:DWORD
	v_add3_u32 v246, v38, v134, s44
	v_mul_f32_e32 v138, v38, v38
	v_mul_f32_e32 v140, v39, v39
	v_mul_f32_e32 v134, v40, v40
	v_mul_f32_e32 v136, v41, v41
	v_pk_add_f32 v[138:139], v[138:139], v[140:141]
	v_pk_add_f32 v[134:135], v[136:137], v[134:135]
	s_waitcnt vmcnt(21)
	v_and_b32_e32 v207, 0xffff0000, v220
	v_and_b32_e32 v209, 0xffff0000, v221
	v_pk_add_f32 v[158:159], v[138:139], v[134:135]
	v_lshlrev_b32_e32 v206, 16, v220
	v_lshlrev_b32_e32 v208, 16, v221
	v_mul_f32_e32 v134, v209, v209
	s_waitcnt vmcnt(19)
	v_and_b32_e32 v205, 0xffff0000, v223
	v_and_b32_e32 v204, 0xffff0000, v222
	v_mul_f32_e32 v138, v207, v207
	v_pk_fma_f32 v[134:135], v[208:209], v[208:209], v[134:135] op_sel_hi:[1,1,0]
	v_lshlrev_b32_e32 v203, 16, v223
	v_lshlrev_b32_e32 v202, 16, v222
	v_pk_mul_f32 v[136:137], v[204:205], v[204:205]
	s_waitcnt vmcnt(15)
	v_lshlrev_b32_e32 v191, 16, v238
	v_pk_fma_f32 v[138:139], v[206:207], v[206:207], v[138:139] op_sel_hi:[1,1,0]
	global_store_dwordx2 v234, v[188:189], s[22:23] offset:2048 nt
	v_pk_fma_f32 v[136:137], v[202:203], v[202:203], v[136:137]
	v_and_b32_e32 v189, 0xffff0000, v238
	v_mov_b32_e32 v190, v138
	v_mov_b32_e32 v140, v134
	v_mov_b32_e32 v141, v191
	v_mul_f32_e32 v160, v189, v189
	v_pk_add_f32 v[134:135], v[138:139], v[134:135]
	v_pk_mul_f32 v[138:139], v[190:191], v[140:141]
	v_pk_add_f32 v[136:137], v[136:137], v[136:137] op_sel:[0,1] op_sel_hi:[1,0]
	v_and_b32_e32 v199, 0xffff0000, v224
	v_and_b32_e32 v201, 0xffff0000, v225
	v_mov_b32_e32 v135, v139
	v_mov_b32_e32 v137, v160
	v_lshlrev_b32_e32 v198, 16, v224
	v_lshlrev_b32_e32 v200, 16, v225
	v_lshlrev_b32_e32 v196, 16, v239
	v_and_b32_e32 v197, 0xffff0000, v239
	v_pk_add_f32 v[134:135], v[134:135], v[136:137]
	v_mul_f32_e32 v136, v199, v199
	v_mul_f32_e32 v138, v201, v201
	v_mul_f32_e32 v161, v196, v196
	v_mul_f32_e32 v166, v197, v197
	v_pk_fma_f32 v[136:137], v[198:199], v[198:199], v[136:137] op_sel_hi:[1,1,0]
	v_pk_fma_f32 v[138:139], v[200:201], v[200:201], v[138:139] op_sel_hi:[1,1,0]
	v_mov_b32_e32 v137, v161
	v_mov_b32_e32 v139, v166
	v_pk_add_f32 v[136:137], v[136:137], v[138:139]
	s_waitcnt vmcnt(14)
	v_and_b32_e32 v195, 0xffff0000, v241
	v_and_b32_e32 v194, 0xffff0000, v240
	v_pk_add_f32 v[160:161], v[134:135], v[136:137]
	v_lshlrev_b32_e32 v193, 16, v241
	v_lshlrev_b32_e32 v192, 16, v240
	v_pk_mul_f32 v[134:135], v[194:195], v[194:195]
	s_waitcnt vmcnt(12)
	v_and_b32_e32 v187, 0xffff0000, v243
	v_pk_fma_f32 v[134:135], v[192:193], v[192:193], v[134:135]
	v_and_b32_e32 v186, 0xffff0000, v242
	v_pk_add_f32 v[166:167], v[134:135], v[134:135] op_sel:[0,1] op_sel_hi:[1,0]
	s_waitcnt vmcnt(8)
	v_lshlrev_b32_e32 v139, 16, v244
	v_pk_add_f32 v[160:161], v[160:161], v[160:161] op_sel:[0,1] op_sel_hi:[1,0]
	v_lshlrev_b32_e32 v185, 16, v243
	v_lshlrev_b32_e32 v184, 16, v242
	v_pk_mul_f32 v[134:135], v[186:187], v[186:187]
	v_lshlrev_b32_e32 v140, 16, v218
	v_and_b32_e32 v141, 0xffff0000, v218
	v_lshlrev_b32_e32 v182, 16, v219
	v_and_b32_e32 v183, 0xffff0000, v219
	v_mov_b32_e32 v138, v160
	v_mov_b32_e32 v218, v166
	v_mov_b32_e32 v219, v139
	v_pk_fma_f32 v[168:169], v[184:185], v[184:185], v[134:135]
	v_and_b32_e32 v137, 0xffff0000, v244
	v_pk_add_f32 v[160:161], v[160:161], v[166:167]
	v_pk_mul_f32 v[166:167], v[138:139], v[218:219]
	v_mul_f32_e32 v136, v137, v137
	v_mov_b32_e32 v161, v167
	v_pk_add_f32 v[166:167], v[168:169], v[168:169] op_sel:[0,1] op_sel_hi:[1,0]
	v_lshlrev_b32_e32 v134, 16, v245
	v_mov_b32_e32 v167, v136
	v_mul_f32_e32 v136, v141, v141
	v_and_b32_e32 v135, 0xffff0000, v245
	v_pk_add_f32 v[160:161], v[160:161], v[166:167]
	v_pk_fma_f32 v[166:167], v[140:141], v[140:141], v[136:137] op_sel_hi:[1,1,0]
	v_mul_f32_e32 v136, v183, v183
	v_mul_f32_e32 v190, v134, v134
	v_mul_f32_e32 v220, v135, v135
	v_pk_fma_f32 v[168:169], v[182:183], v[182:183], v[136:137] op_sel_hi:[1,1,0]
	v_mov_b32_e32 v167, v190
	v_mov_b32_e32 v169, v220
	v_pk_add_f32 v[166:167], v[166:167], v[168:169]
	v_and_b32_sdwa v138, v41, v235 dst_sel:DWORD dst_unused:UNUSED_PAD src0_sel:WORD_1 src1_sel:DWORD
	v_pk_add_f32 v[160:161], v[160:161], v[166:167]
	v_mov_b32_e32 v167, v158
	v_mov_b32_e32 v166, v160
	v_mov_b32_e32 v158, v161
	v_pk_add_f32 v[158:159], v[166:167], v[158:159]
	ds_bpermute_b32 v161, v171, v159
	ds_bpermute_b32 v160, v171, v158
	v_and_b32_sdwa v166, v39, v235 dst_sel:DWORD dst_unused:UNUSED_PAD src0_sel:WORD_1 src1_sel:DWORD
	s_addc_u32 s27, s13, s17
	v_and_b32_sdwa v188, v40, v235 dst_sel:DWORD dst_unused:UNUSED_PAD src0_sel:WORD_1 src1_sel:DWORD
	v_add3_u32 v138, v41, v138, s44
	s_waitcnt lgkmcnt(0)
	v_pk_add_f32 v[158:159], v[158:159], v[160:161]
	ds_bpermute_b32 v161, v226, v159
	ds_bpermute_b32 v160, v226, v158
	v_add3_u32 v166, v39, v166, s44
	s_add_u32 s28, s33, s14
	v_add3_u32 v136, v40, v188, s44
	v_and_b32_e32 v138, 0xffff0000, v138
	s_waitcnt lgkmcnt(0)
	v_pk_add_f32 v[158:159], v[158:159], v[160:161]
	ds_bpermute_b32 v161, v228, v159
	ds_bpermute_b32 v160, v228, v158
	v_and_b32_e32 v166, 0xffff0000, v166
	s_addc_u32 s29, s34, s15
	s_add_i32 s4, s8, -4
	v_or_b32_sdwa v167, v138, v136 dst_sel:DWORD dst_unused:UNUSED_PAD src0_sel:DWORD src1_sel:WORD_1
	s_waitcnt lgkmcnt(0)
	v_pk_add_f32 v[158:159], v[158:159], v[160:161]
	ds_bpermute_b32 v161, v229, v159
	ds_bpermute_b32 v160, v229, v158
	v_or_b32_sdwa v166, v166, v246 dst_sel:DWORD dst_unused:UNUSED_PAD src0_sel:DWORD src1_sel:WORD_1
	s_ashr_i32 s5, s4, 31
	global_store_dwordx2 v234, v[166:167], s[22:23] offset:3584 nt
	s_lshl_b64 s[14:15], s[4:5], 11
	s_waitcnt lgkmcnt(0)
	v_pk_add_f32 v[158:159], v[158:159], v[160:161]
	ds_bpermute_b32 v161, v230, v159
	ds_bpermute_b32 v160, v230, v158
	s_lshl_b64 s[22:23], s[4:5], 12
	s_add_u32 s24, s96, s22
	s_addc_u32 s25, s97, s23
	s_lshl_b64 s[4:5], s[4:5], 13
	s_waitcnt lgkmcnt(0)
	v_pk_add_f32 v[158:159], v[158:159], v[160:161]
	ds_bpermute_b32 v161, v231, v159
	ds_bpermute_b32 v160, v231, v158
	s_add_u32 s30, s6, s4
	s_addc_u32 s31, s7, s5
	v_mov_b32_e32 v168, 0
	v_lshl_add_u64 v[218:219], s[30:31], 0, v[178:179]
	s_waitcnt lgkmcnt(0)
	v_pk_add_f32 v[158:159], v[158:159], v[160:161]
	s_add_u32 s16, s35, s20
	v_pk_fma_f32 v[220:221], v[158:159], s[10:11], v[180:181] op_sel_hi:[1,0,0]
	s_addc_u32 s17, s36, s21
	v_mul_f32_e32 v136, 0x4b800000, v221
	v_cmp_gt_f32_e64 s[4:5], s43, v221
	v_cmp_gt_f32_e32 vcc, s43, v220
	s_nop 0
	v_cndmask_b32_e64 v136, v221, v136, s[4:5]
	v_rsq_f32_e32 v136, v136
	s_nop 0
	v_mul_f32_e32 v138, 0x45800000, v136
	v_cndmask_b32_e64 v136, v136, v138, s[4:5]
	v_pk_mul_f32 v[158:159], v[214:215], v[136:137] op_sel_hi:[1,0]
	v_pk_mul_f32 v[160:161], v[216:217], v[136:137] op_sel_hi:[1,0]
	v_pk_fma_f32 v[158:159], v[26:27], v[158:159], v[30:31]
	v_pk_fma_f32 v[160:161], v[28:29], v[160:161], v[32:33]
	v_bfe_u32 v138, v158, 16, 1
	v_bfe_u32 v166, v159, 16, 1
	v_add3_u32 v138, v158, v138, s44
	v_add3_u32 v166, v159, v166, s44
	v_med3_f32 v158, v158, s45, v236
	v_med3_f32 v159, v159, s45, v236
	v_lshrrev_b32_e32 v138, 16, v138
	v_cvt_pk_fp8_f32 v168, v158, v159
	v_and_or_b32 v166, v166, s42, v138
	v_bfe_u32 v138, v160, 16, 1
	v_add3_u32 v138, v160, v138, s44
	v_bfe_u32 v158, v161, 16, 1
	v_lshrrev_b32_e32 v138, 16, v138
	v_med3_f32 v159, v160, s45, v236
	v_med3_f32 v160, v161, s45, v236
	v_add3_u32 v158, v161, v158, s44
	v_cvt_pk_fp8_f32 v168, v159, v160 op_sel:[0,0,1]
	v_and_or_b32 v167, v158, s42, v138
	v_pk_mul_f32 v[158:159], v[210:211], v[136:137] op_sel_hi:[1,0]
	global_store_dwordx2 v234, v[166:167], s[26:27]
	global_store_dword v237, v168, s[28:29]
	v_pk_fma_f32 v[158:159], v[90:91], v[158:159], v[94:95]
	v_pk_mul_f32 v[160:161], v[212:213], v[136:137] op_sel_hi:[1,0]
	v_bfe_u32 v138, v158, 16, 1
	v_add3_u32 v138, v158, v138, s44
	v_bfe_u32 v166, v159, 16, 1
	v_pk_fma_f32 v[160:161], v[92:93], v[160:161], v[96:97]
	v_lshrrev_b32_e32 v138, 16, v138
	v_add3_u32 v166, v159, v166, s44
	v_med3_f32 v158, v158, s45, v236
	v_med3_f32 v159, v159, s45, v236
	v_mov_b32_e32 v168, 0
	v_and_or_b32 v166, v166, s42, v138
	v_bfe_u32 v138, v160, 16, 1
	v_cvt_pk_fp8_f32 v168, v158, v159
	v_add3_u32 v138, v160, v138, s44
	v_bfe_u32 v158, v161, 16, 1
	v_pk_mul_f32 v[66:67], v[66:67], v[136:137] op_sel_hi:[1,0]
	v_lshrrev_b32_e32 v138, 16, v138
	v_add3_u32 v158, v161, v158, s44
	v_pk_fma_f32 v[66:67], v[82:83], v[66:67], v[86:87]
	v_med3_f32 v159, v160, s45, v236
	v_med3_f32 v160, v161, s45, v236
	v_and_or_b32 v167, v158, s42, v138
	v_bfe_u32 v138, v66, 16, 1
	v_bfe_u32 v158, v67, 16, 1
	v_cvt_pk_fp8_f32 v168, v159, v160 op_sel:[0,0,1]
	v_pk_mul_f32 v[68:69], v[68:69], v[136:137] op_sel_hi:[1,0]
	v_add3_u32 v138, v66, v138, s44
	v_add3_u32 v158, v67, v158, s44
	v_med3_f32 v66, v66, s45, v236
	v_med3_f32 v67, v67, s45, v236
	v_mov_b32_e32 v160, 0
	v_pk_fma_f32 v[68:69], v[84:85], v[68:69], v[88:89]
	v_lshrrev_b32_e32 v138, 16, v138
	v_cvt_pk_fp8_f32 v160, v66, v67
	v_and_or_b32 v158, v158, s42, v138
	v_bfe_u32 v138, v68, 16, 1
	v_add3_u32 v138, v68, v138, s44
	v_bfe_u32 v66, v69, 16, 1
	v_pk_mul_f32 v[58:59], v[58:59], v[136:137] op_sel_hi:[1,0]
	v_lshrrev_b32_e32 v138, 16, v138
	v_med3_f32 v67, v68, s45, v236
	v_med3_f32 v68, v69, s45, v236
	v_add3_u32 v66, v69, v66, s44
	v_pk_fma_f32 v[58:59], v[74:75], v[58:59], v[78:79]
	v_cvt_pk_fp8_f32 v160, v67, v68 op_sel:[0,0,1]
	v_and_or_b32 v159, v66, s42, v138
	v_bfe_u32 v66, v58, 16, 1
	v_bfe_u32 v67, v59, 16, 1
	v_pk_mul_f32 v[60:61], v[60:61], v[136:137] op_sel_hi:[1,0]
	v_add3_u32 v66, v58, v66, s44
	v_add3_u32 v67, v59, v67, s44
	v_med3_f32 v58, v58, s45, v236
	v_med3_f32 v59, v59, s45, v236
	v_mov_b32_e32 v68, 0
	v_pk_fma_f32 v[60:61], v[76:77], v[60:61], v[80:81]
	v_lshrrev_b32_e32 v66, 16, v66
	v_cvt_pk_fp8_f32 v68, v58, v59
	v_and_or_b32 v66, v67, s42, v66
	v_bfe_u32 v67, v60, 16, 1
	v_add3_u32 v67, v60, v67, s44
	v_bfe_u32 v58, v61, 16, 1
	v_pk_mul_f32 v[54:55], v[54:55], v[136:137] op_sel_hi:[1,0]
	v_lshrrev_b32_e32 v67, 16, v67
	v_med3_f32 v59, v60, s45, v236
	v_med3_f32 v60, v61, s45, v236
	v_add3_u32 v58, v61, v58, s44
	v_pk_fma_f32 v[54:55], v[34:35], v[54:55], v[70:71]
	v_cvt_pk_fp8_f32 v68, v59, v60 op_sel:[0,0,1]
	v_and_or_b32 v67, v58, s42, v67
	v_bfe_u32 v58, v54, 16, 1
	v_bfe_u32 v59, v55, 16, 1
	v_pk_mul_f32 v[56:57], v[56:57], v[136:137] op_sel_hi:[1,0]
	v_add3_u32 v58, v54, v58, s44
	v_add3_u32 v59, v55, v59, s44
	v_med3_f32 v54, v54, s45, v236
	v_med3_f32 v55, v55, s45, v236
	v_mov_b32_e32 v60, 0
	v_pk_fma_f32 v[56:57], v[36:37], v[56:57], v[72:73]
	v_lshrrev_b32_e32 v58, 16, v58
	v_cvt_pk_fp8_f32 v60, v54, v55
	v_and_or_b32 v58, v59, s42, v58
	v_bfe_u32 v59, v56, 16, 1
	v_add3_u32 v59, v56, v59, s44
	v_bfe_u32 v54, v57, 16, 1
	v_pk_mul_f32 v[46:47], v[46:47], v[136:137] op_sel_hi:[1,0]
	v_lshrrev_b32_e32 v59, 16, v59
	v_med3_f32 v55, v56, s45, v236
	v_med3_f32 v56, v57, s45, v236
	v_add3_u32 v54, v57, v54, s44
	v_pk_fma_f32 v[46:47], v[18:19], v[46:47], v[22:23]
	v_cvt_pk_fp8_f32 v60, v55, v56 op_sel:[0,0,1]
	v_and_or_b32 v59, v54, s42, v59
	v_bfe_u32 v54, v46, 16, 1
	v_bfe_u32 v55, v47, 16, 1
	v_pk_mul_f32 v[48:49], v[48:49], v[136:137] op_sel_hi:[1,0]
	v_add3_u32 v54, v46, v54, s44
	v_add3_u32 v55, v47, v55, s44
	v_med3_f32 v46, v46, s45, v236
	v_med3_f32 v47, v47, s45, v236
	v_mov_b32_e32 v56, 0
	v_pk_fma_f32 v[48:49], v[20:21], v[48:49], v[24:25]
	v_lshrrev_b32_e32 v54, 16, v54
	v_cvt_pk_fp8_f32 v56, v46, v47
	v_and_or_b32 v54, v55, s42, v54
	v_bfe_u32 v55, v48, 16, 1
	v_add3_u32 v55, v48, v55, s44
	v_bfe_u32 v46, v49, 16, 1
	v_pk_mul_f32 v[42:43], v[42:43], v[136:137] op_sel_hi:[1,0]
	v_lshrrev_b32_e32 v55, 16, v55
	v_med3_f32 v47, v48, s45, v236
	v_med3_f32 v48, v49, s45, v236
	v_add3_u32 v46, v49, v46, s44
	v_pk_fma_f32 v[42:43], v[10:11], v[42:43], v[14:15]
	v_cvt_pk_fp8_f32 v56, v47, v48 op_sel:[0,0,1]
	v_and_or_b32 v55, v46, s42, v55
	v_bfe_u32 v46, v42, 16, 1
	v_bfe_u32 v47, v43, 16, 1
	v_pk_mul_f32 v[44:45], v[44:45], v[136:137] op_sel_hi:[1,0]
	v_add3_u32 v46, v42, v46, s44
	v_add3_u32 v47, v43, v47, s44
	v_med3_f32 v42, v42, s45, v236
	v_med3_f32 v43, v43, s45, v236
	v_mov_b32_e32 v48, 0
	v_pk_fma_f32 v[44:45], v[12:13], v[44:45], v[16:17]
	v_lshrrev_b32_e32 v46, 16, v46
	v_cvt_pk_fp8_f32 v48, v42, v43
	v_and_or_b32 v46, v47, s42, v46
	v_bfe_u32 v47, v44, 16, 1
	v_add3_u32 v47, v44, v47, s44
	v_bfe_u32 v42, v45, 16, 1
	v_pk_mul_f32 v[38:39], v[38:39], v[136:137] op_sel_hi:[1,0]
	v_lshrrev_b32_e32 v47, 16, v47
	v_med3_f32 v43, v44, s45, v236
	v_med3_f32 v44, v45, s45, v236
	v_add3_u32 v42, v45, v42, s44
	v_pk_fma_f32 v[38:39], v[2:3], v[38:39], v[6:7]
	v_cvt_pk_fp8_f32 v48, v43, v44 op_sel:[0,0,1]
	v_and_or_b32 v47, v42, s42, v47
	v_bfe_u32 v42, v38, 16, 1
	v_bfe_u32 v43, v39, 16, 1
	v_add3_u32 v42, v38, v42, s44
	v_add3_u32 v43, v39, v43, s44
	v_med3_f32 v38, v38, s45, v236
	v_med3_f32 v39, v39, s45, v236
	v_mov_b32_e32 v44, 0
	v_pk_mul_f32 v[40:41], v[40:41], v[136:137] op_sel_hi:[1,0]
	v_cvt_pk_fp8_f32 v44, v38, v39
	v_pk_fma_f32 v[40:41], v[4:5], v[40:41], v[8:9]
	v_lshrrev_b32_e32 v42, 16, v42
	v_and_or_b32 v42, v43, s42, v42
	v_bfe_u32 v43, v40, 16, 1
	v_add3_u32 v43, v40, v43, s44
	v_med3_f32 v39, v40, s45, v236
	v_med3_f32 v40, v41, s45, v236
	v_bfe_u32 v38, v41, 16, 1
	v_cvt_pk_fp8_f32 v44, v39, v40 op_sel:[0,0,1]
	v_lshrrev_b32_e32 v43, 16, v43
	v_add3_u32 v38, v41, v38, s44
	v_and_or_b32 v43, v38, s42, v43
	global_store_dwordx2 v234, v[166:167], s[26:27] offset:512
	global_store_dword v237, v168, s[28:29] offset:256
	global_store_dwordx2 v234, v[158:159], s[26:27] offset:1024
	global_store_dword v237, v160, s[28:29] offset:512
	global_store_dwordx2 v234, v[66:67], s[26:27] offset:1536
	global_store_dword v237, v68, s[28:29] offset:768
	global_store_dwordx2 v234, v[58:59], s[26:27] offset:2048
	global_store_dword v237, v60, s[28:29] offset:1024
	global_store_dwordx2 v234, v[54:55], s[26:27] offset:2560
	global_store_dword v237, v56, s[28:29] offset:1280
	global_store_dwordx2 v234, v[46:47], s[26:27] offset:3072
	global_store_dword v237, v48, s[28:29] offset:1536
	global_store_dwordx2 v234, v[42:43], s[26:27] offset:3584
	global_store_dword v237, v44, s[28:29] offset:1792
	global_load_dwordx2 v[222:223], v234, s[24:25]
	global_load_dwordx4 v[166:169], v178, s[30:31] nt
	global_load_dwordx2 v[224:225], v234, s[24:25] offset:512
	global_load_dwordx4 v[158:161], v178, s[30:31] offset:1024 nt
	global_load_dwordx2 v[238:239], v234, s[24:25] offset:1024
	global_load_dwordx4 v[66:69], v178, s[30:31] offset:2048 nt
	global_load_dwordx2 v[240:241], v234, s[24:25] offset:1536
	global_load_dwordx4 v[58:61], v178, s[30:31] offset:3072 nt
	global_load_dwordx2 v[242:243], v234, s[24:25] offset:2048
	v_add_co_u32_e64 v38, s[4:5], s41, v218
	v_mul_f32_e32 v40, 0x4b800000, v220
	s_nop 0
	v_addc_co_u32_e64 v39, s[4:5], 0, v219, s[4:5]
	v_cndmask_b32_e32 v40, v220, v40, vcc
	global_load_dwordx4 v[54:57], v[38:39], off nt
	global_load_dwordx2 v[218:219], v234, s[24:25] offset:2560
	global_load_dwordx4 v[46:49], v[38:39], off offset:1024 nt
	global_load_dwordx2 v[216:217], v234, s[24:25] offset:3072
	v_rsq_f32_e32 v136, v40
	global_load_dwordx4 v[42:45], v[38:39], off offset:2048 nt
	global_load_dwordx2 v[220:221], v234, s[24:25] offset:3584
	s_nop 0
	global_load_dwordx4 v[38:41], v[38:39], off offset:3072 nt
	s_add_u32 s26, s11, s20
	s_addc_u32 s27, s13, s21
	v_mul_f32_e32 v138, 0x45800000, v136
	v_cndmask_b32_e32 v138, v136, v138, vcc
	v_pk_mul_f32 v[208:209], v[138:139], v[208:209] op_sel_hi:[0,1]
	v_pk_mul_f32 v[206:207], v[138:139], v[206:207] op_sel_hi:[0,1]
	v_pk_fma_f32 v[162:163], v[98:99], v[206:207], v[162:163]
	v_pk_fma_f32 v[164:165], v[100:101], v[208:209], v[164:165]
	v_and_b32_sdwa v206, v163, v235 dst_sel:DWORD dst_unused:UNUSED_PAD src0_sel:WORD_1 src1_sel:DWORD
	v_and_b32_sdwa v190, v165, v235 dst_sel:DWORD dst_unused:UNUSED_PAD src0_sel:WORD_1 src1_sel:DWORD
	v_and_b32_sdwa v136, v164, v235 dst_sel:DWORD dst_unused:UNUSED_PAD src0_sel:WORD_1 src1_sel:DWORD
	v_and_b32_sdwa v188, v162, v235 dst_sel:DWORD dst_unused:UNUSED_PAD src0_sel:WORD_1 src1_sel:DWORD
	v_add3_u32 v190, v165, v190, s44
	v_add3_u32 v206, v163, v206, s44
	v_add3_u32 v188, v162, v188, s44
	v_add3_u32 v136, v164, v136, s44
	v_and_b32_e32 v190, 0xffff0000, v190
	v_and_b32_e32 v206, 0xffff0000, v206
	v_or_b32_sdwa v207, v190, v136 dst_sel:DWORD dst_unused:UNUSED_PAD src0_sel:DWORD src1_sel:WORD_1
	v_or_b32_sdwa v206, v206, v188 dst_sel:DWORD dst_unused:UNUSED_PAD src0_sel:DWORD src1_sel:WORD_1
	global_store_dwordx2 v234, v[206:207], s[16:17] nt
	v_mov_b32_e32 v206, v203
	v_mov_b32_e32 v203, v204
	v_mov_b32_e32 v207, v205
	v_pk_mul_f32 v[202:203], v[138:139], v[202:203] op_sel_hi:[0,1]
	v_pk_mul_f32 v[206:207], v[138:139], v[206:207] op_sel_hi:[0,1]
	v_pk_fma_f32 v[154:155], v[102:103], v[202:203], v[154:155]
	v_pk_fma_f32 v[156:157], v[104:105], v[206:207], v[156:157]
	v_and_b32_sdwa v202, v155, v235 dst_sel:DWORD dst_unused:UNUSED_PAD src0_sel:WORD_1 src1_sel:DWORD
	v_and_b32_sdwa v188, v154, v235 dst_sel:DWORD dst_unused:UNUSED_PAD src0_sel:WORD_1 src1_sel:DWORD
	v_and_b32_sdwa v190, v157, v235 dst_sel:DWORD dst_unused:UNUSED_PAD src0_sel:WORD_1 src1_sel:DWORD
	v_add3_u32 v202, v155, v202, s44
	v_pk_mul_f32 v[200:201], v[138:139], v[200:201] op_sel_hi:[0,1]
	v_pk_mul_f32 v[198:199], v[138:139], v[198:199] op_sel_hi:[0,1]
	v_and_b32_sdwa v136, v156, v235 dst_sel:DWORD dst_unused:UNUSED_PAD src0_sel:WORD_1 src1_sel:DWORD
	v_add3_u32 v188, v154, v188, s44
	v_add3_u32 v190, v157, v190, s44
	v_and_b32_e32 v202, 0xffff0000, v202
	v_pk_fma_f32 v[210:211], v[106:107], v[198:199], v[150:151]
	v_pk_fma_f32 v[152:153], v[108:109], v[200:201], v[152:153]
	v_add3_u32 v136, v156, v136, s44
	v_and_b32_e32 v190, 0xffff0000, v190
	v_or_b32_sdwa v202, v202, v188 dst_sel:DWORD dst_unused:UNUSED_PAD src0_sel:DWORD src1_sel:WORD_1
	v_and_b32_sdwa v151, v153, v235 dst_sel:DWORD dst_unused:UNUSED_PAD src0_sel:WORD_1 src1_sel:DWORD
	v_and_b32_sdwa v188, v211, v235 dst_sel:DWORD dst_unused:UNUSED_PAD src0_sel:WORD_1 src1_sel:DWORD
	v_or_b32_sdwa v203, v190, v136 dst_sel:DWORD dst_unused:UNUSED_PAD src0_sel:DWORD src1_sel:WORD_1
	v_and_b32_sdwa v136, v152, v235 dst_sel:DWORD dst_unused:UNUSED_PAD src0_sel:WORD_1 src1_sel:DWORD
	v_and_b32_sdwa v150, v210, v235 dst_sel:DWORD dst_unused:UNUSED_PAD src0_sel:WORD_1 src1_sel:DWORD
	v_add3_u32 v151, v153, v151, s44
	v_add3_u32 v188, v211, v188, s44
	v_add3_u32 v150, v210, v150, s44
	v_add3_u32 v136, v152, v136, s44
	v_and_b32_e32 v151, 0xffff0000, v151
	v_and_b32_e32 v188, 0xffff0000, v188
	v_or_b32_sdwa v151, v151, v136 dst_sel:DWORD dst_unused:UNUSED_PAD src0_sel:DWORD src1_sel:WORD_1
	v_or_b32_sdwa v150, v188, v150 dst_sel:DWORD dst_unused:UNUSED_PAD src0_sel:DWORD src1_sel:WORD_1
	global_store_dwordx2 v234, v[150:151], s[16:17] offset:1024 nt
	v_pk_mul_f32 v[150:151], v[152:153], v[152:153]
	v_pk_mul_f32 v[198:199], v[210:211], v[210:211]
	v_mov_b32_e32 v188, v191
	v_pk_mov_b32 v[200:201], v[198:199], v[150:151] op_sel:[1,0]
	v_mov_b32_e32 v199, v151
	v_pk_mul_f32 v[196:197], v[196:197], v[138:139] op_sel_hi:[1,0]
	v_pk_mul_f32 v[188:189], v[188:189], v[138:139] op_sel_hi:[1,0]
	v_pk_add_f32 v[150:151], v[198:199], v[200:201]
	v_pk_fma_f32 v[146:147], v[110:111], v[188:189], v[146:147]
	v_pk_fma_f32 v[148:149], v[112:113], v[196:197], v[148:149]
	v_pk_add_f32 v[150:151], v[150:151], v[150:151] op_sel_hi:[0,1]
	v_and_b32_sdwa v188, v149, v235 dst_sel:DWORD dst_unused:UNUSED_PAD src0_sel:WORD_1 src1_sel:DWORD
	v_and_b32_sdwa v189, v147, v235 dst_sel:DWORD dst_unused:UNUSED_PAD src0_sel:WORD_1 src1_sel:DWORD
	v_and_b32_sdwa v136, v148, v235 dst_sel:DWORD dst_unused:UNUSED_PAD src0_sel:WORD_1 src1_sel:DWORD
	v_and_b32_sdwa v150, v146, v235 dst_sel:DWORD dst_unused:UNUSED_PAD src0_sel:WORD_1 src1_sel:DWORD
	v_add3_u32 v188, v149, v188, s44
	v_add3_u32 v189, v147, v189, s44
	v_mov_b32_e32 v204, v163
	v_mov_b32_e32 v205, v155
	v_add3_u32 v150, v146, v150, s44
	v_add3_u32 v136, v148, v136, s44
	v_and_b32_e32 v188, 0xffff0000, v188
	v_and_b32_e32 v190, 0xffff0000, v189
	global_store_dwordx2 v234, v[202:203], s[16:17] offset:512 nt
	v_mov_b32_e32 v202, v162
	v_mov_b32_e32 v203, v154
	v_pk_mul_f32 v[204:205], v[204:205], v[204:205]
	v_or_b32_sdwa v189, v188, v136 dst_sel:DWORD dst_unused:UNUSED_PAD src0_sel:DWORD src1_sel:WORD_1
	v_or_b32_sdwa v188, v190, v150 dst_sel:DWORD dst_unused:UNUSED_PAD src0_sel:DWORD src1_sel:WORD_1
	v_mul_f32_e32 v136, v146, v146
	v_mov_b32_e32 v196, v192
	v_mov_b32_e32 v197, v194
	v_mov_b32_e32 v194, v193
	v_pk_fma_f32 v[202:203], v[202:203], v[202:203], v[204:205]
	v_mov_b32_e32 v204, v164
	v_mov_b32_e32 v205, v156
	global_store_dwordx2 v234, v[188:189], s[16:17] offset:1536 nt
	v_pk_fma_f32 v[188:189], v[146:147], v[146:147], v[136:137] op_sel_hi:[1,1,0]
	v_mul_f32_e32 v136, v148, v148
	v_pk_mul_f32 v[196:197], v[138:139], v[196:197] op_sel_hi:[0,1]
	v_pk_mul_f32 v[192:193], v[138:139], v[194:195] op_sel_hi:[0,1]
	v_pk_mul_f32 v[204:205], v[204:205], v[204:205]
	v_mov_b32_e32 v206, v165
	v_mov_b32_e32 v207, v157
	v_pk_fma_f32 v[190:191], v[148:149], v[148:149], v[136:137] op_sel_hi:[1,1,0]
	v_pk_fma_f32 v[144:145], v[116:117], v[192:193], v[144:145]
	v_pk_fma_f32 v[142:143], v[114:115], v[196:197], v[142:143]
	v_pk_fma_f32 v[204:205], v[206:207], v[206:207], v[204:205]
	v_and_b32_sdwa v188, v145, v235 dst_sel:DWORD dst_unused:UNUSED_PAD src0_sel:WORD_1 src1_sel:DWORD
	v_and_b32_sdwa v190, v143, v235 dst_sel:DWORD dst_unused:UNUSED_PAD src0_sel:WORD_1 src1_sel:DWORD
	v_pk_add_f32 v[202:203], v[202:203], v[204:205]
	v_and_b32_sdwa v136, v144, v235 dst_sel:DWORD dst_unused:UNUSED_PAD src0_sel:WORD_1 src1_sel:DWORD
	v_and_b32_sdwa v150, v142, v235 dst_sel:DWORD dst_unused:UNUSED_PAD src0_sel:WORD_1 src1_sel:DWORD
	v_add3_u32 v188, v145, v188, s44
	v_add3_u32 v190, v143, v190, s44
	v_pk_add_f32 v[202:203], v[202:203], v[202:203] op_sel_hi:[0,1]
	v_add3_u32 v150, v142, v150, s44
	v_add3_u32 v136, v144, v136, s44
	v_and_b32_e32 v188, 0xffff0000, v188
	v_and_b32_e32 v190, 0xffff0000, v190
	v_or_b32_sdwa v193, v188, v136 dst_sel:DWORD dst_unused:UNUSED_PAD src0_sel:DWORD src1_sel:WORD_1
	v_or_b32_sdwa v192, v190, v150 dst_sel:DWORD dst_unused:UNUSED_PAD src0_sel:DWORD src1_sel:WORD_1
	v_mul_f32_e32 v188, v142, v142
	v_mul_f32_e32 v190, v143, v143
	v_mul_f32_e32 v202, v144, v144
	v_mul_f32_e32 v150, v145, v145
	v_pk_add_f32 v[188:189], v[188:189], v[190:191]
	v_pk_add_f32 v[150:151], v[150:151], v[202:203]
	v_mov_b32_e32 v136, v139
	v_pk_add_f32 v[150:151], v[188:189], v[150:151]
	s_waitcnt vmcnt(19)
	v_and_b32_e32 v207, 0xffff0000, v222
	v_pk_add_f32 v[188:189], v[150:151], v[150:151] op_sel_hi:[0,1]
	v_mov_b32_e32 v150, v185
	v_mov_b32_e32 v185, v186
	v_mov_b32_e32 v151, v187
	v_pk_mul_f32 v[184:185], v[138:139], v[184:185] op_sel_hi:[0,1]
	v_pk_mul_f32 v[150:151], v[138:139], v[150:151] op_sel_hi:[0,1]
	v_pk_fma_f32 v[212:213], v[118:119], v[184:185], v[130:131]
	v_pk_fma_f32 v[214:215], v[120:121], v[150:151], v[132:133]
	v_and_b32_sdwa v131, v212, v235 dst_sel:DWORD dst_unused:UNUSED_PAD src0_sel:WORD_1 src1_sel:DWORD
	v_add3_u32 v132, v212, v131, s44
	v_and_b32_sdwa v131, v215, v235 dst_sel:DWORD dst_unused:UNUSED_PAD src0_sel:WORD_1 src1_sel:DWORD
	v_and_b32_sdwa v133, v213, v235 dst_sel:DWORD dst_unused:UNUSED_PAD src0_sel:WORD_1 src1_sel:DWORD
	v_and_b32_sdwa v130, v214, v235 dst_sel:DWORD dst_unused:UNUSED_PAD src0_sel:WORD_1 src1_sel:DWORD
	v_add3_u32 v131, v215, v131, s44
	v_add3_u32 v133, v213, v133, s44
	v_add3_u32 v130, v214, v130, s44
	v_and_b32_e32 v131, 0xffff0000, v131
	v_and_b32_e32 v133, 0xffff0000, v133
	v_or_b32_sdwa v131, v131, v130 dst_sel:DWORD dst_unused:UNUSED_PAD src0_sel:DWORD src1_sel:WORD_1
	v_or_b32_sdwa v130, v133, v132 dst_sel:DWORD dst_unused:UNUSED_PAD src0_sel:DWORD src1_sel:WORD_1
	global_store_dwordx2 v234, v[130:131], s[16:17] offset:2560 nt
	v_pk_mul_f32 v[130:131], v[214:215], v[214:215]
	v_pk_mul_f32 v[132:133], v[212:213], v[212:213]
	v_and_b32_e32 v209, 0xffff0000, v223
	v_pk_mov_b32 v[150:151], v[132:133], v[130:131] op_sel:[1,0]
	v_mov_b32_e32 v133, v131
	v_pk_add_f32 v[130:131], v[132:133], v[150:151]
	v_pk_mul_f32 v[132:133], v[138:139], v[140:141] op_sel_hi:[0,1]
	v_pk_add_f32 v[184:185], v[130:131], v[130:131] op_sel_hi:[0,1]
	v_pk_mul_f32 v[130:131], v[138:139], v[182:183] op_sel_hi:[0,1]
	v_pk_fma_f32 v[140:141], v[122:123], v[132:133], v[62:63]
	v_pk_fma_f32 v[150:151], v[124:125], v[130:131], v[64:65]
	v_and_b32_sdwa v63, v140, v235 dst_sel:DWORD dst_unused:UNUSED_PAD src0_sel:WORD_1 src1_sel:DWORD
	v_add3_u32 v64, v140, v63, s44
	v_and_b32_sdwa v63, v151, v235 dst_sel:DWORD dst_unused:UNUSED_PAD src0_sel:WORD_1 src1_sel:DWORD
	v_and_b32_sdwa v65, v141, v235 dst_sel:DWORD dst_unused:UNUSED_PAD src0_sel:WORD_1 src1_sel:DWORD
	v_and_b32_sdwa v62, v150, v235 dst_sel:DWORD dst_unused:UNUSED_PAD src0_sel:WORD_1 src1_sel:DWORD
	v_add3_u32 v63, v151, v63, s44
	v_add3_u32 v65, v141, v65, s44
	v_add3_u32 v62, v150, v62, s44
	v_and_b32_e32 v63, 0xffff0000, v63
	v_and_b32_e32 v65, 0xffff0000, v65
	v_or_b32_sdwa v63, v63, v62 dst_sel:DWORD dst_unused:UNUSED_PAD src0_sel:DWORD src1_sel:WORD_1
	v_or_b32_sdwa v62, v65, v64 dst_sel:DWORD dst_unused:UNUSED_PAD src0_sel:DWORD src1_sel:WORD_1
	global_store_dwordx2 v234, v[62:63], s[16:17] offset:3072 nt
	v_mul_f32_e32 v62, v140, v140
	v_pk_fma_f32 v[62:63], v[140:141], v[140:141], v[62:63] op_sel_hi:[1,1,0]
	v_pk_mul_f32 v[132:133], v[136:137], v[138:139] op_sel_hi:[1,0]
	v_mul_f32_e32 v62, v150, v150
	v_pk_mul_f32 v[130:131], v[134:135], v[138:139] op_sel_hi:[1,0]
	v_pk_fma_f32 v[64:65], v[150:151], v[150:151], v[62:63] op_sel_hi:[1,1,0]
	v_pk_fma_f32 v[130:131], v[128:129], v[130:131], v[52:53]
	v_pk_fma_f32 v[132:133], v[126:127], v[132:133], v[50:51]
	v_mul_f32_e32 v188, v130, v130
	v_and_b32_sdwa v50, v132, v235 dst_sel:DWORD dst_unused:UNUSED_PAD src0_sel:WORD_1 src1_sel:DWORD
	v_mul_f32_e32 v62, v132, v132
	v_mul_f32_e32 v64, v133, v133
	v_mul_f32_e32 v184, v131, v131
	v_add3_u32 v245, v132, v50, s44
	v_pk_add_f32 v[50:51], v[62:63], v[64:65]
	v_pk_add_f32 v[52:53], v[184:185], v[188:189]
	v_lshlrev_b32_e32 v206, 16, v222
	v_pk_add_f32 v[134:135], v[50:51], v[52:53]
	v_lshlrev_b32_e32 v208, 16, v223
	v_mul_f32_e32 v50, v209, v209
	s_waitcnt vmcnt(19)
	v_and_b32_e32 v205, 0xffff0000, v225
	v_and_b32_e32 v204, 0xffff0000, v224
	v_mul_f32_e32 v62, v207, v207
	v_pk_fma_f32 v[50:51], v[208:209], v[208:209], v[50:51] op_sel_hi:[1,1,0]
	v_lshlrev_b32_e32 v203, 16, v225
	v_lshlrev_b32_e32 v202, 16, v224
	v_pk_mul_f32 v[52:53], v[204:205], v[204:205]
	s_waitcnt vmcnt(15)
	v_lshlrev_b32_e32 v191, 16, v240
	v_pk_fma_f32 v[62:63], v[206:207], v[206:207], v[62:63] op_sel_hi:[1,1,0]
	v_pk_fma_f32 v[52:53], v[202:203], v[202:203], v[52:53]
	v_and_b32_e32 v189, 0xffff0000, v240
	v_mov_b32_e32 v190, v62
	v_mov_b32_e32 v64, v50
	v_mov_b32_e32 v65, v191
	v_mul_f32_e32 v136, v189, v189
	v_pk_add_f32 v[50:51], v[62:63], v[50:51]
	v_pk_mul_f32 v[62:63], v[190:191], v[64:65]
	v_pk_add_f32 v[52:53], v[52:53], v[52:53] op_sel:[0,1] op_sel_hi:[1,0]
	v_and_b32_e32 v199, 0xffff0000, v238
	v_and_b32_e32 v201, 0xffff0000, v239
	v_mov_b32_e32 v51, v63
	v_mov_b32_e32 v53, v136
	v_lshlrev_b32_e32 v198, 16, v238
	v_lshlrev_b32_e32 v200, 16, v239
	v_lshlrev_b32_e32 v196, 16, v241
	v_and_b32_e32 v197, 0xffff0000, v241
	v_pk_add_f32 v[50:51], v[50:51], v[52:53]
	v_mul_f32_e32 v52, v199, v199
	v_mul_f32_e32 v62, v201, v201
	v_mul_f32_e32 v137, v196, v196
	v_mul_f32_e32 v138, v197, v197
	v_pk_fma_f32 v[52:53], v[198:199], v[198:199], v[52:53] op_sel_hi:[1,1,0]
	v_pk_fma_f32 v[62:63], v[200:201], v[200:201], v[62:63] op_sel_hi:[1,1,0]
	v_mov_b32_e32 v53, v137
	v_mov_b32_e32 v63, v138
	v_pk_add_f32 v[52:53], v[52:53], v[62:63]
	s_waitcnt vmcnt(13)
	v_and_b32_e32 v195, 0xffff0000, v243
	v_and_b32_e32 v194, 0xffff0000, v242
	global_store_dwordx2 v234, v[192:193], s[16:17] offset:2048 nt
	v_pk_add_f32 v[136:137], v[50:51], v[52:53]
	v_lshlrev_b32_e32 v193, 16, v243
	v_lshlrev_b32_e32 v192, 16, v242
	v_pk_mul_f32 v[50:51], v[194:195], v[194:195]
	s_waitcnt vmcnt(12)
	v_and_b32_e32 v187, 0xffff0000, v219
	v_pk_fma_f32 v[50:51], v[192:193], v[192:193], v[50:51]
	v_and_b32_e32 v186, 0xffff0000, v218
	v_pk_add_f32 v[138:139], v[50:51], v[50:51] op_sel:[0,1] op_sel_hi:[1,0]
	s_waitcnt vmcnt(8)
	v_lshlrev_b32_e32 v63, 16, v220
	v_pk_add_f32 v[136:137], v[136:137], v[136:137] op_sel:[0,1] op_sel_hi:[1,0]
	v_lshlrev_b32_e32 v185, 16, v219
	v_lshlrev_b32_e32 v184, 16, v218
	v_pk_mul_f32 v[50:51], v[186:187], v[186:187]
	v_lshlrev_b32_e32 v64, 16, v216
	v_and_b32_e32 v65, 0xffff0000, v216
	v_lshlrev_b32_e32 v182, 16, v217
	v_and_b32_e32 v183, 0xffff0000, v217
	v_mov_b32_e32 v62, v136
	v_mov_b32_e32 v216, v138
	v_mov_b32_e32 v217, v63
	v_pk_fma_f32 v[218:219], v[184:185], v[184:185], v[50:51]
	v_and_b32_e32 v53, 0xffff0000, v220
	v_pk_add_f32 v[136:137], v[136:137], v[138:139]
	v_pk_mul_f32 v[138:139], v[62:63], v[216:217]
	v_mul_f32_e32 v52, v53, v53
	v_mov_b32_e32 v137, v139
	v_pk_add_f32 v[138:139], v[218:219], v[218:219] op_sel:[0,1] op_sel_hi:[1,0]
	v_lshlrev_b32_e32 v50, 16, v221
	v_mov_b32_e32 v139, v52
	v_mul_f32_e32 v52, v65, v65
	v_and_b32_e32 v51, 0xffff0000, v221
	v_pk_add_f32 v[136:137], v[136:137], v[138:139]
	v_pk_fma_f32 v[138:139], v[64:65], v[64:65], v[52:53] op_sel_hi:[1,1,0]
	v_mul_f32_e32 v52, v183, v183
	v_mul_f32_e32 v188, v50, v50
	v_mul_f32_e32 v190, v51, v51
	v_pk_fma_f32 v[216:217], v[182:183], v[182:183], v[52:53] op_sel_hi:[1,1,0]
	v_mov_b32_e32 v139, v188
	v_mov_b32_e32 v217, v190
	v_pk_add_f32 v[138:139], v[138:139], v[216:217]
	v_and_b32_sdwa v62, v131, v235 dst_sel:DWORD dst_unused:UNUSED_PAD src0_sel:WORD_1 src1_sel:DWORD
	v_pk_add_f32 v[136:137], v[136:137], v[138:139]
	v_mov_b32_e32 v139, v134
	v_mov_b32_e32 v138, v136
	v_mov_b32_e32 v134, v137
	v_pk_add_f32 v[134:135], v[138:139], v[134:135]
	ds_bpermute_b32 v137, v171, v135
	ds_bpermute_b32 v136, v171, v134
	v_and_b32_sdwa v138, v133, v235 dst_sel:DWORD dst_unused:UNUSED_PAD src0_sel:WORD_1 src1_sel:DWORD
	v_and_b32_sdwa v244, v130, v235 dst_sel:DWORD dst_unused:UNUSED_PAD src0_sel:WORD_1 src1_sel:DWORD
	v_add3_u32 v62, v131, v62, s44
	v_add3_u32 v138, v133, v138, s44
	s_waitcnt lgkmcnt(0)
	v_pk_add_f32 v[134:135], v[134:135], v[136:137]
	ds_bpermute_b32 v137, v226, v135
	ds_bpermute_b32 v136, v226, v134
	s_add_u32 s28, s33, s18
	v_add3_u32 v52, v130, v244, s44
	v_and_b32_e32 v62, 0xffff0000, v62
	v_and_b32_e32 v138, 0xffff0000, v138
	s_waitcnt lgkmcnt(0)
	v_pk_add_f32 v[134:135], v[134:135], v[136:137]
	ds_bpermute_b32 v137, v228, v135
	ds_bpermute_b32 v136, v228, v134
	s_addc_u32 s29, s34, s19
	s_add_i32 s4, s8, -3
	v_or_b32_sdwa v139, v62, v52 dst_sel:DWORD dst_unused:UNUSED_PAD src0_sel:DWORD src1_sel:WORD_1
	v_or_b32_sdwa v138, v138, v245 dst_sel:DWORD dst_unused:UNUSED_PAD src0_sel:DWORD src1_sel:WORD_1
	s_waitcnt lgkmcnt(0)
	v_pk_add_f32 v[134:135], v[134:135], v[136:137]
	ds_bpermute_b32 v137, v229, v135
	ds_bpermute_b32 v136, v229, v134
	s_ashr_i32 s5, s4, 31
	global_store_dwordx2 v234, v[138:139], s[16:17] offset:3584 nt
	s_lshl_b64 s[16:17], s[4:5], 11
	s_lshl_b64 s[24:25], s[4:5], 12
	s_waitcnt lgkmcnt(0)
	v_pk_add_f32 v[134:135], v[134:135], v[136:137]
	ds_bpermute_b32 v137, v230, v135
	ds_bpermute_b32 v136, v230, v134
	s_add_u32 s20, s96, s24
	s_addc_u32 s21, s97, s25
	s_lshl_b64 s[4:5], s[4:5], 13
	s_add_u32 s30, s6, s4
	s_waitcnt lgkmcnt(0)
	v_pk_add_f32 v[134:135], v[134:135], v[136:137]
	ds_bpermute_b32 v137, v231, v135
	ds_bpermute_b32 v136, v231, v134
	s_addc_u32 s31, s7, s5
	v_lshl_add_u64 v[138:139], s[30:31], 0, v[178:179]
	s_add_u32 s18, s35, s22
	s_addc_u32 s19, s36, s23
	s_waitcnt lgkmcnt(0)
	v_pk_add_f32 v[134:135], v[134:135], v[136:137]
	v_mov_b32_e32 v188, v191
	v_pk_fma_f32 v[134:135], v[134:135], s[10:11], v[180:181] op_sel_hi:[1,0,0]
	s_nop 0
	v_mul_f32_e32 v52, 0x4b800000, v135
	v_cmp_gt_f32_e64 s[4:5], s43, v135
	v_cmp_gt_f32_e32 vcc, s43, v134
	s_nop 0
	v_cndmask_b32_e64 v52, v135, v52, s[4:5]
	v_rsq_f32_e32 v52, v52
	s_nop 0
	v_mul_f32_e32 v62, 0x45800000, v52
	v_cndmask_b32_e64 v52, v52, v62, s[4:5]
	v_pk_mul_f32 v[136:137], v[162:163], v[52:53] op_sel_hi:[1,0]
	v_pk_mul_f32 v[162:163], v[164:165], v[52:53] op_sel_hi:[1,0]
	v_pk_fma_f32 v[136:137], v[26:27], v[136:137], v[30:31]
	v_pk_fma_f32 v[162:163], v[28:29], v[162:163], v[32:33]
	v_bfe_u32 v62, v136, 16, 1
	v_add3_u32 v62, v136, v62, s44
	v_bfe_u32 v135, v137, 16, 1
	v_lshrrev_b32_e32 v62, 16, v62
	v_add3_u32 v135, v137, v135, s44
	v_and_or_b32 v164, v135, s42, v62
	v_med3_f32 v135, v136, s45, v236
	v_med3_f32 v136, v137, s45, v236
	v_mov_b32_e32 v137, 0
	v_cvt_pk_fp8_f32 v137, v135, v136
	v_bfe_u32 v62, v162, 16, 1
	v_add3_u32 v62, v162, v62, s44
	v_med3_f32 v136, v162, s45, v236
	v_med3_f32 v162, v163, s45, v236
	v_bfe_u32 v135, v163, 16, 1
	v_cvt_pk_fp8_f32 v137, v136, v162 op_sel:[0,0,1]
	v_lshrrev_b32_e32 v62, 16, v62
	v_add3_u32 v135, v163, v135, s44
	v_and_or_b32 v165, v135, s42, v62
	global_store_dwordx2 v234, v[164:165], s[26:27]
	global_store_dword v237, v137, s[28:29]
	v_pk_mul_f32 v[136:137], v[154:155], v[52:53] op_sel_hi:[1,0]
	v_pk_mul_f32 v[154:155], v[156:157], v[52:53] op_sel_hi:[1,0]
	v_pk_fma_f32 v[136:137], v[90:91], v[136:137], v[94:95]
	v_pk_fma_f32 v[154:155], v[92:93], v[154:155], v[96:97]
	v_bfe_u32 v62, v136, 16, 1
	v_add3_u32 v62, v136, v62, s44
	v_bfe_u32 v135, v137, 16, 1
	v_lshrrev_b32_e32 v62, 16, v62
	v_add3_u32 v135, v137, v135, s44
	v_and_or_b32 v156, v135, s42, v62
	v_med3_f32 v135, v136, s45, v236
	v_med3_f32 v136, v137, s45, v236
	v_mov_b32_e32 v137, 0
	v_cvt_pk_fp8_f32 v137, v135, v136
	v_bfe_u32 v62, v154, 16, 1
	v_add3_u32 v62, v154, v62, s44
	v_med3_f32 v136, v154, s45, v236
	v_med3_f32 v154, v155, s45, v236
	v_bfe_u32 v135, v155, 16, 1
	v_cvt_pk_fp8_f32 v137, v136, v154 op_sel:[0,0,1]
	v_lshrrev_b32_e32 v62, 16, v62
	v_add3_u32 v135, v155, v135, s44
	v_and_or_b32 v157, v135, s42, v62
	global_store_dwordx2 v234, v[156:157], s[26:27] offset:512
	global_store_dword v237, v137, s[28:29] offset:256
	v_pk_mul_f32 v[136:137], v[210:211], v[52:53] op_sel_hi:[1,0]
	v_pk_mul_f32 v[152:153], v[152:153], v[52:53] op_sel_hi:[1,0]
	v_pk_fma_f32 v[136:137], v[82:83], v[136:137], v[86:87]
	v_pk_fma_f32 v[152:153], v[84:85], v[152:153], v[88:89]
	v_bfe_u32 v62, v136, 16, 1
	v_add3_u32 v62, v136, v62, s44
	v_bfe_u32 v135, v137, 16, 1
	v_lshrrev_b32_e32 v62, 16, v62
	v_add3_u32 v135, v137, v135, s44
	v_and_or_b32 v154, v135, s42, v62
	v_med3_f32 v135, v136, s45, v236
	v_med3_f32 v136, v137, s45, v236
	v_mov_b32_e32 v137, 0
	v_cvt_pk_fp8_f32 v137, v135, v136
	v_bfe_u32 v62, v152, 16, 1
	v_add3_u32 v62, v152, v62, s44
	v_med3_f32 v136, v152, s45, v236
	v_med3_f32 v152, v153, s45, v236
	v_bfe_u32 v135, v153, 16, 1
	v_cvt_pk_fp8_f32 v137, v136, v152 op_sel:[0,0,1]
	v_lshrrev_b32_e32 v62, 16, v62
	v_add3_u32 v135, v153, v135, s44
	v_and_or_b32 v155, v135, s42, v62
	global_store_dwordx2 v234, v[154:155], s[26:27] offset:1024
	global_store_dword v237, v137, s[28:29] offset:512
	v_pk_mul_f32 v[136:137], v[146:147], v[52:53] op_sel_hi:[1,0]
	v_pk_mul_f32 v[146:147], v[148:149], v[52:53] op_sel_hi:[1,0]
	v_pk_fma_f32 v[136:137], v[74:75], v[136:137], v[78:79]
	v_pk_fma_f32 v[146:147], v[76:77], v[146:147], v[80:81]
	v_bfe_u32 v62, v136, 16, 1
	v_add3_u32 v62, v136, v62, s44
	v_bfe_u32 v135, v137, 16, 1
	v_lshrrev_b32_e32 v62, 16, v62
	v_add3_u32 v135, v137, v135, s44
	v_and_or_b32 v148, v135, s42, v62
	v_med3_f32 v135, v136, s45, v236
	v_med3_f32 v136, v137, s45, v236
	v_mov_b32_e32 v137, 0
	v_cvt_pk_fp8_f32 v137, v135, v136
	v_bfe_u32 v62, v146, 16, 1
	v_add3_u32 v62, v146, v62, s44
	v_med3_f32 v136, v146, s45, v236
	v_med3_f32 v146, v147, s45, v236
	v_bfe_u32 v135, v147, 16, 1
	v_cvt_pk_fp8_f32 v137, v136, v146 op_sel:[0,0,1]
	v_lshrrev_b32_e32 v62, 16, v62
	v_add3_u32 v135, v147, v135, s44
	v_and_or_b32 v149, v135, s42, v62
	global_store_dwordx2 v234, v[148:149], s[26:27] offset:1536
	global_store_dword v237, v137, s[28:29] offset:768
	v_pk_mul_f32 v[136:137], v[142:143], v[52:53] op_sel_hi:[1,0]
	v_pk_mul_f32 v[142:143], v[144:145], v[52:53] op_sel_hi:[1,0]
	v_pk_fma_f32 v[136:137], v[34:35], v[136:137], v[70:71]
	v_pk_fma_f32 v[142:143], v[36:37], v[142:143], v[72:73]
	v_bfe_u32 v62, v136, 16, 1
	v_add3_u32 v62, v136, v62, s44
	v_bfe_u32 v135, v137, 16, 1
	v_lshrrev_b32_e32 v62, 16, v62
	v_add3_u32 v135, v137, v135, s44
	v_and_or_b32 v144, v135, s42, v62
	v_med3_f32 v135, v136, s45, v236
	v_med3_f32 v136, v137, s45, v236
	v_mov_b32_e32 v137, 0
	v_cvt_pk_fp8_f32 v137, v135, v136
	v_bfe_u32 v62, v142, 16, 1
	v_add3_u32 v62, v142, v62, s44
	v_med3_f32 v136, v142, s45, v236
	v_med3_f32 v142, v143, s45, v236
	v_bfe_u32 v135, v143, 16, 1
	v_cvt_pk_fp8_f32 v137, v136, v142 op_sel:[0,0,1]
	v_lshrrev_b32_e32 v62, 16, v62
	v_add3_u32 v135, v143, v135, s44
	v_and_or_b32 v145, v135, s42, v62
	global_store_dwordx2 v234, v[144:145], s[26:27] offset:2048
	global_store_dword v237, v137, s[28:29] offset:1024
	v_pk_mul_f32 v[136:137], v[212:213], v[52:53] op_sel_hi:[1,0]
	v_pk_mul_f32 v[142:143], v[214:215], v[52:53] op_sel_hi:[1,0]
	v_pk_fma_f32 v[136:137], v[18:19], v[136:137], v[22:23]
	v_pk_fma_f32 v[142:143], v[20:21], v[142:143], v[24:25]
	v_bfe_u32 v62, v136, 16, 1
	v_add3_u32 v62, v136, v62, s44
	v_bfe_u32 v135, v137, 16, 1
	v_lshrrev_b32_e32 v62, 16, v62
	v_add3_u32 v135, v137, v135, s44
	v_and_or_b32 v144, v135, s42, v62
	v_med3_f32 v135, v136, s45, v236
	v_med3_f32 v136, v137, s45, v236
	v_mov_b32_e32 v137, 0
	v_cvt_pk_fp8_f32 v137, v135, v136
	v_bfe_u32 v62, v142, 16, 1
	v_add3_u32 v62, v142, v62, s44
	v_med3_f32 v136, v142, s45, v236
	v_med3_f32 v142, v143, s45, v236
	v_bfe_u32 v135, v143, 16, 1
	v_cvt_pk_fp8_f32 v137, v136, v142 op_sel:[0,0,1]
	v_lshrrev_b32_e32 v62, 16, v62
	v_add3_u32 v135, v143, v135, s44
	v_and_or_b32 v145, v135, s42, v62
	global_store_dwordx2 v234, v[144:145], s[26:27] offset:2560
	global_store_dword v237, v137, s[28:29] offset:1280
	v_pk_mul_f32 v[136:137], v[140:141], v[52:53] op_sel_hi:[1,0]
	v_pk_mul_f32 v[140:141], v[150:151], v[52:53] op_sel_hi:[1,0]
	v_pk_fma_f32 v[136:137], v[10:11], v[136:137], v[14:15]
	v_pk_fma_f32 v[140:141], v[12:13], v[140:141], v[16:17]
	v_bfe_u32 v62, v136, 16, 1
	v_add3_u32 v62, v136, v62, s44
	v_bfe_u32 v135, v137, 16, 1
	v_lshrrev_b32_e32 v62, 16, v62
	v_add3_u32 v135, v137, v135, s44
	v_and_or_b32 v142, v135, s42, v62
	v_bfe_u32 v62, v140, 16, 1
	v_med3_f32 v135, v136, s45, v236
	v_med3_f32 v136, v137, s45, v236
	v_mov_b32_e32 v137, 0
	v_pk_mul_f32 v[132:133], v[132:133], v[52:53] op_sel_hi:[1,0]
	v_add3_u32 v62, v140, v62, s44
	v_cvt_pk_fp8_f32 v137, v135, v136
	v_bfe_u32 v135, v141, 16, 1
	v_pk_fma_f32 v[132:133], v[2:3], v[132:133], v[6:7]
	v_lshrrev_b32_e32 v62, 16, v62
	v_add3_u32 v135, v141, v135, s44
	v_pk_mul_f32 v[130:131], v[130:131], v[52:53] op_sel_hi:[1,0]
	v_bfe_u32 v52, v132, 16, 1
	v_and_or_b32 v143, v135, s42, v62
	v_add3_u32 v52, v132, v52, s44
	v_bfe_u32 v62, v133, 16, 1
	v_med3_f32 v136, v140, s45, v236
	v_med3_f32 v140, v141, s45, v236
	v_lshrrev_b32_e32 v52, 16, v52
	v_add3_u32 v62, v133, v62, s44
	v_cvt_pk_fp8_f32 v137, v136, v140 op_sel:[0,0,1]
	v_and_or_b32 v136, v62, s42, v52
	v_med3_f32 v62, v132, s45, v236
	v_med3_f32 v132, v133, s45, v236
	v_mov_b32_e32 v133, 0
	v_cvt_pk_fp8_f32 v133, v62, v132
	v_pk_fma_f32 v[130:131], v[4:5], v[130:131], v[8:9]
	global_store_dwordx2 v234, v[142:143], s[26:27] offset:3072
	global_store_dword v237, v137, s[28:29] offset:1536
	v_bfe_u32 v52, v130, 16, 1
	v_add3_u32 v52, v130, v52, s44
	v_med3_f32 v130, v130, s45, v236
	v_med3_f32 v132, v131, s45, v236
	v_bfe_u32 v62, v131, 16, 1
	v_cvt_pk_fp8_f32 v133, v130, v132 op_sel:[0,0,1]
	v_lshrrev_b32_e32 v52, 16, v52
	v_add3_u32 v62, v131, v62, s44
	v_and_or_b32 v137, v62, s42, v52
	global_store_dwordx2 v234, v[136:137], s[26:27] offset:3584
	global_store_dword v237, v133, s[28:29] offset:1792
	global_load_dwordx2 v[220:221], v234, s[20:21]
	global_load_dwordx4 v[162:165], v178, s[30:31] nt
	global_load_dwordx2 v[222:223], v234, s[20:21] offset:512
	global_load_dwordx4 v[154:157], v178, s[30:31] offset:1024 nt
	global_load_dwordx2 v[224:225], v234, s[20:21] offset:1024
	global_load_dwordx4 v[150:153], v178, s[30:31] offset:2048 nt
	global_load_dwordx2 v[238:239], v234, s[20:21] offset:1536
	global_load_dwordx4 v[146:149], v178, s[30:31] offset:3072 nt
	global_load_dwordx2 v[240:241], v234, s[20:21] offset:2048
	v_add_co_u32_e64 v130, s[4:5], s41, v138
	v_mul_f32_e32 v52, 0x4b800000, v134
	s_nop 0
	v_addc_co_u32_e64 v131, s[4:5], 0, v139, s[4:5]
	global_load_dwordx4 v[142:145], v[130:131], off nt
	global_load_dwordx2 v[242:243], v234, s[20:21] offset:2560
	global_load_dwordx4 v[138:141], v[130:131], off offset:1024 nt
	global_load_dwordx2 v[218:219], v234, s[20:21] offset:3072
	v_cndmask_b32_e32 v52, v134, v52, vcc
	global_load_dwordx4 v[134:137], v[130:131], off offset:2048 nt
	global_load_dwordx2 v[244:245], v234, s[20:21] offset:3584
	s_nop 0
	global_load_dwordx4 v[130:133], v[130:131], off offset:3072 nt
	v_rsq_f32_e32 v52, v52
	s_add_u32 s26, s11, s22
	s_addc_u32 s27, s13, s23
	s_add_u32 s28, s33, s14
	v_mul_f32_e32 v62, 0x45800000, v52
	v_cndmask_b32_e32 v62, v52, v62, vcc
	v_pk_mul_f32 v[208:209], v[62:63], v[208:209] op_sel_hi:[0,1]
	v_pk_mul_f32 v[206:207], v[62:63], v[206:207] op_sel_hi:[0,1]
	v_pk_fma_f32 v[214:215], v[98:99], v[206:207], v[166:167]
	v_pk_fma_f32 v[216:217], v[100:101], v[208:209], v[168:169]
	v_and_b32_sdwa v168, v215, v235 dst_sel:DWORD dst_unused:UNUSED_PAD src0_sel:WORD_1 src1_sel:DWORD
	v_and_b32_sdwa v167, v217, v235 dst_sel:DWORD dst_unused:UNUSED_PAD src0_sel:WORD_1 src1_sel:DWORD
	v_and_b32_sdwa v52, v216, v235 dst_sel:DWORD dst_unused:UNUSED_PAD src0_sel:WORD_1 src1_sel:DWORD
	v_and_b32_sdwa v166, v214, v235 dst_sel:DWORD dst_unused:UNUSED_PAD src0_sel:WORD_1 src1_sel:DWORD
	v_add3_u32 v167, v217, v167, s44
	v_add3_u32 v168, v215, v168, s44
	v_add3_u32 v166, v214, v166, s44
	v_add3_u32 v52, v216, v52, s44
	v_and_b32_e32 v167, 0xffff0000, v167
	v_and_b32_e32 v168, 0xffff0000, v168
	v_or_b32_sdwa v167, v167, v52 dst_sel:DWORD dst_unused:UNUSED_PAD src0_sel:DWORD src1_sel:WORD_1
	v_or_b32_sdwa v166, v168, v166 dst_sel:DWORD dst_unused:UNUSED_PAD src0_sel:DWORD src1_sel:WORD_1
	global_store_dwordx2 v234, v[166:167], s[18:19] nt
	v_mov_b32_e32 v166, v203
	v_mov_b32_e32 v167, v205
	v_mov_b32_e32 v203, v204
	v_pk_mul_f32 v[166:167], v[62:63], v[166:167] op_sel_hi:[0,1]
	v_pk_mul_f32 v[168:169], v[62:63], v[202:203] op_sel_hi:[0,1]
	v_pk_fma_f32 v[210:211], v[102:103], v[168:169], v[158:159]
	v_pk_fma_f32 v[212:213], v[104:105], v[166:167], v[160:161]
	v_and_b32_sdwa v160, v211, v235 dst_sel:DWORD dst_unused:UNUSED_PAD src0_sel:WORD_1 src1_sel:DWORD
	v_and_b32_sdwa v159, v213, v235 dst_sel:DWORD dst_unused:UNUSED_PAD src0_sel:WORD_1 src1_sel:DWORD
	v_and_b32_sdwa v52, v212, v235 dst_sel:DWORD dst_unused:UNUSED_PAD src0_sel:WORD_1 src1_sel:DWORD
	v_and_b32_sdwa v158, v210, v235 dst_sel:DWORD dst_unused:UNUSED_PAD src0_sel:WORD_1 src1_sel:DWORD
	v_add3_u32 v159, v213, v159, s44
	v_add3_u32 v160, v211, v160, s44
	v_add3_u32 v158, v210, v158, s44
	v_add3_u32 v52, v212, v52, s44
	v_and_b32_e32 v159, 0xffff0000, v159
	v_and_b32_e32 v160, 0xffff0000, v160
	v_or_b32_sdwa v159, v159, v52 dst_sel:DWORD dst_unused:UNUSED_PAD src0_sel:DWORD src1_sel:WORD_1
	v_or_b32_sdwa v158, v160, v158 dst_sel:DWORD dst_unused:UNUSED_PAD src0_sel:DWORD src1_sel:WORD_1
	v_mov_b32_e32 v160, v215
	v_mov_b32_e32 v161, v211
	global_store_dwordx2 v234, v[158:159], s[18:19] offset:512 nt
	v_mov_b32_e32 v158, v214
	v_mov_b32_e32 v159, v210
	v_pk_mul_f32 v[160:161], v[160:161], v[160:161]
	v_mov_b32_e32 v166, v217
	v_pk_fma_f32 v[158:159], v[158:159], v[158:159], v[160:161]
	v_mov_b32_e32 v160, v216
	v_mov_b32_e32 v161, v212
	v_pk_mul_f32 v[160:161], v[160:161], v[160:161]
	v_mov_b32_e32 v167, v213
	v_pk_fma_f32 v[160:161], v[166:167], v[166:167], v[160:161]
	v_pk_mul_f32 v[166:167], v[62:63], v[198:199] op_sel_hi:[0,1]
	v_pk_add_f32 v[158:159], v[158:159], v[160:161]
	v_pk_mul_f32 v[160:161], v[62:63], v[200:201] op_sel_hi:[0,1]
	v_pk_fma_f32 v[66:67], v[106:107], v[166:167], v[66:67]
	v_pk_fma_f32 v[68:69], v[108:109], v[160:161], v[68:69]
	v_pk_add_f32 v[158:159], v[158:159], v[158:159] op_sel_hi:[0,1]
	v_and_b32_sdwa v160, v69, v235 dst_sel:DWORD dst_unused:UNUSED_PAD src0_sel:WORD_1 src1_sel:DWORD
	v_and_b32_sdwa v161, v67, v235 dst_sel:DWORD dst_unused:UNUSED_PAD src0_sel:WORD_1 src1_sel:DWORD
	v_and_b32_sdwa v52, v68, v235 dst_sel:DWORD dst_unused:UNUSED_PAD src0_sel:WORD_1 src1_sel:DWORD
	v_and_b32_sdwa v158, v66, v235 dst_sel:DWORD dst_unused:UNUSED_PAD src0_sel:WORD_1 src1_sel:DWORD
	v_add3_u32 v160, v69, v160, s44
	v_add3_u32 v161, v67, v161, s44
	v_add3_u32 v158, v66, v158, s44
	v_add3_u32 v52, v68, v52, s44
	v_and_b32_e32 v160, 0xffff0000, v160
	v_and_b32_e32 v166, 0xffff0000, v161
	v_or_b32_sdwa v161, v160, v52 dst_sel:DWORD dst_unused:UNUSED_PAD src0_sel:DWORD src1_sel:WORD_1
	v_or_b32_sdwa v160, v166, v158 dst_sel:DWORD dst_unused:UNUSED_PAD src0_sel:DWORD src1_sel:WORD_1
	global_store_dwordx2 v234, v[160:161], s[18:19] offset:1024 nt
	v_pk_mul_f32 v[160:161], v[68:69], v[68:69]
	v_pk_mul_f32 v[166:167], v[66:67], v[66:67]
	v_pk_mul_f32 v[64:65], v[62:63], v[64:65] op_sel_hi:[0,1]
	v_pk_mov_b32 v[168:169], v[166:167], v[160:161] op_sel:[1,0]
	v_mov_b32_e32 v167, v161
	v_pk_add_f32 v[160:161], v[166:167], v[168:169]
	v_pk_mul_f32 v[166:167], v[196:197], v[62:63] op_sel_hi:[1,0]
	v_pk_mul_f32 v[168:169], v[188:189], v[62:63] op_sel_hi:[1,0]
	v_pk_add_f32 v[160:161], v[160:161], v[160:161] op_sel_hi:[0,1]
	v_pk_fma_f32 v[58:59], v[110:111], v[168:169], v[58:59]
	v_pk_fma_f32 v[60:61], v[112:113], v[166:167], v[60:61]
	v_and_b32_sdwa v166, v59, v235 dst_sel:DWORD dst_unused:UNUSED_PAD src0_sel:WORD_1 src1_sel:DWORD
	v_and_b32_sdwa v160, v61, v235 dst_sel:DWORD dst_unused:UNUSED_PAD src0_sel:WORD_1 src1_sel:DWORD
	v_and_b32_sdwa v52, v60, v235 dst_sel:DWORD dst_unused:UNUSED_PAD src0_sel:WORD_1 src1_sel:DWORD
	v_and_b32_sdwa v158, v58, v235 dst_sel:DWORD dst_unused:UNUSED_PAD src0_sel:WORD_1 src1_sel:DWORD
	v_add3_u32 v160, v61, v160, s44
	v_add3_u32 v166, v59, v166, s44
	v_add3_u32 v158, v58, v158, s44
	v_add3_u32 v52, v60, v52, s44
	v_and_b32_e32 v160, 0xffff0000, v160
	v_and_b32_e32 v166, 0xffff0000, v166
	v_mov_b32_e32 v188, v192
	v_mov_b32_e32 v189, v194
	v_mov_b32_e32 v194, v193
	v_or_b32_sdwa v167, v160, v52 dst_sel:DWORD dst_unused:UNUSED_PAD src0_sel:DWORD src1_sel:WORD_1
	v_or_b32_sdwa v166, v166, v158 dst_sel:DWORD dst_unused:UNUSED_PAD src0_sel:DWORD src1_sel:WORD_1
	v_mul_f32_e32 v52, v58, v58
	v_pk_mul_f32 v[188:189], v[62:63], v[188:189] op_sel_hi:[0,1]
	v_pk_mul_f32 v[190:191], v[62:63], v[194:195] op_sel_hi:[0,1]
	global_store_dwordx2 v234, v[166:167], s[18:19] offset:1536 nt
	v_pk_fma_f32 v[166:167], v[58:59], v[58:59], v[52:53] op_sel_hi:[1,1,0]
	v_pk_fma_f32 v[56:57], v[116:117], v[190:191], v[56:57]
	v_pk_fma_f32 v[54:55], v[114:115], v[188:189], v[54:55]
	v_mul_f32_e32 v52, v60, v60
	v_and_b32_sdwa v160, v57, v235 dst_sel:DWORD dst_unused:UNUSED_PAD src0_sel:WORD_1 src1_sel:DWORD
	v_and_b32_sdwa v166, v55, v235 dst_sel:DWORD dst_unused:UNUSED_PAD src0_sel:WORD_1 src1_sel:DWORD
	v_pk_fma_f32 v[168:169], v[60:61], v[60:61], v[52:53] op_sel_hi:[1,1,0]
	v_and_b32_sdwa v52, v56, v235 dst_sel:DWORD dst_unused:UNUSED_PAD src0_sel:WORD_1 src1_sel:DWORD
	v_and_b32_sdwa v158, v54, v235 dst_sel:DWORD dst_unused:UNUSED_PAD src0_sel:WORD_1 src1_sel:DWORD
	v_add3_u32 v160, v57, v160, s44
	v_add3_u32 v166, v55, v166, s44
	v_add3_u32 v158, v54, v158, s44
	v_add3_u32 v52, v56, v52, s44
	v_and_b32_e32 v160, 0xffff0000, v160
	v_and_b32_e32 v166, 0xffff0000, v166
	v_or_b32_sdwa v189, v160, v52 dst_sel:DWORD dst_unused:UNUSED_PAD src0_sel:DWORD src1_sel:WORD_1
	v_or_b32_sdwa v188, v166, v158 dst_sel:DWORD dst_unused:UNUSED_PAD src0_sel:DWORD src1_sel:WORD_1
	v_mul_f32_e32 v166, v54, v54
	v_mul_f32_e32 v168, v55, v55
	v_mul_f32_e32 v158, v56, v56
	v_mul_f32_e32 v160, v57, v57
	v_pk_add_f32 v[166:167], v[166:167], v[168:169]
	v_pk_add_f32 v[158:159], v[160:161], v[158:159]
	v_mov_b32_e32 v160, v185
	v_mov_b32_e32 v161, v187
	v_mov_b32_e32 v185, v186
	v_pk_add_f32 v[158:159], v[166:167], v[158:159]
	v_pk_mul_f32 v[160:161], v[62:63], v[160:161] op_sel_hi:[0,1]
	v_pk_mul_f32 v[166:167], v[62:63], v[184:185] op_sel_hi:[0,1]
	v_pk_fma_f32 v[46:47], v[118:119], v[166:167], v[46:47]
	v_pk_fma_f32 v[48:49], v[120:121], v[160:161], v[48:49]
	v_pk_add_f32 v[158:159], v[158:159], v[158:159] op_sel_hi:[0,1]
	v_and_b32_sdwa v160, v49, v235 dst_sel:DWORD dst_unused:UNUSED_PAD src0_sel:WORD_1 src1_sel:DWORD
	v_and_b32_sdwa v161, v47, v235 dst_sel:DWORD dst_unused:UNUSED_PAD src0_sel:WORD_1 src1_sel:DWORD
	v_and_b32_sdwa v52, v48, v235 dst_sel:DWORD dst_unused:UNUSED_PAD src0_sel:WORD_1 src1_sel:DWORD
	v_and_b32_sdwa v158, v46, v235 dst_sel:DWORD dst_unused:UNUSED_PAD src0_sel:WORD_1 src1_sel:DWORD
	v_add3_u32 v160, v49, v160, s44
	v_add3_u32 v161, v47, v161, s44
	v_add3_u32 v158, v46, v158, s44
	v_add3_u32 v52, v48, v52, s44
	v_and_b32_e32 v160, 0xffff0000, v160
	v_and_b32_e32 v166, 0xffff0000, v161
	v_or_b32_sdwa v161, v160, v52 dst_sel:DWORD dst_unused:UNUSED_PAD src0_sel:DWORD src1_sel:WORD_1
	v_or_b32_sdwa v160, v166, v158 dst_sel:DWORD dst_unused:UNUSED_PAD src0_sel:DWORD src1_sel:WORD_1
	global_store_dwordx2 v234, v[160:161], s[18:19] offset:2560 nt
	v_pk_mul_f32 v[160:161], v[48:49], v[48:49]
	v_pk_mul_f32 v[166:167], v[46:47], v[46:47]
	v_pk_fma_f32 v[42:43], v[122:123], v[64:65], v[42:43]
	v_pk_mov_b32 v[168:169], v[166:167], v[160:161] op_sel:[1,0]
	v_mov_b32_e32 v167, v161
	v_pk_add_f32 v[160:161], v[166:167], v[168:169]
	v_pk_mul_f32 v[166:167], v[62:63], v[182:183] op_sel_hi:[0,1]
	v_pk_fma_f32 v[44:45], v[124:125], v[166:167], v[44:45]
	v_and_b32_sdwa v158, v43, v235 dst_sel:DWORD dst_unused:UNUSED_PAD src0_sel:WORD_1 src1_sel:DWORD
	v_and_b32_sdwa v65, v45, v235 dst_sel:DWORD dst_unused:UNUSED_PAD src0_sel:WORD_1 src1_sel:DWORD
	v_and_b32_sdwa v52, v44, v235 dst_sel:DWORD dst_unused:UNUSED_PAD src0_sel:WORD_1 src1_sel:DWORD
	v_and_b32_sdwa v64, v42, v235 dst_sel:DWORD dst_unused:UNUSED_PAD src0_sel:WORD_1 src1_sel:DWORD
	v_add3_u32 v65, v45, v65, s44
	v_add3_u32 v158, v43, v158, s44
	v_add3_u32 v64, v42, v64, s44
	v_add3_u32 v52, v44, v52, s44
	v_and_b32_e32 v65, 0xffff0000, v65
	v_and_b32_e32 v158, 0xffff0000, v158
	v_or_b32_sdwa v65, v65, v52 dst_sel:DWORD dst_unused:UNUSED_PAD src0_sel:DWORD src1_sel:WORD_1
	v_or_b32_sdwa v64, v158, v64 dst_sel:DWORD dst_unused:UNUSED_PAD src0_sel:DWORD src1_sel:WORD_1
	v_mul_f32_e32 v52, v42, v42
	global_store_dwordx2 v234, v[64:65], s[18:19] offset:3072 nt
	v_pk_fma_f32 v[64:65], v[42:43], v[42:43], v[52:53] op_sel_hi:[1,1,0]
	v_mul_f32_e32 v52, v44, v44
	v_pk_fma_f32 v[166:167], v[44:45], v[44:45], v[52:53] op_sel_hi:[1,1,0]
	v_mov_b32_e32 v52, v63
	v_pk_mul_f32 v[52:53], v[52:53], v[62:63] op_sel_hi:[1,0]
	v_pk_mul_f32 v[50:51], v[50:51], v[62:63] op_sel_hi:[1,0]
	v_pk_add_f32 v[160:161], v[160:161], v[160:161] op_sel_hi:[0,1]
	s_waitcnt vmcnt(46)
	v_pk_fma_f32 v[40:41], v[128:129], v[50:51], v[40:41]
	v_pk_fma_f32 v[38:39], v[126:127], v[52:53], v[38:39]
	v_mul_f32_e32 v158, v40, v40
	v_and_b32_sdwa v50, v38, v235 dst_sel:DWORD dst_unused:UNUSED_PAD src0_sel:WORD_1 src1_sel:DWORD
	v_mul_f32_e32 v64, v38, v38
	v_mul_f32_e32 v166, v39, v39
	v_mul_f32_e32 v160, v41, v41
	v_add3_u32 v246, v38, v50, s44
	v_pk_add_f32 v[50:51], v[64:65], v[166:167]
	v_pk_add_f32 v[52:53], v[160:161], v[158:159]
	s_waitcnt vmcnt(21)
	v_and_b32_e32 v207, 0xffff0000, v220
	v_and_b32_e32 v209, 0xffff0000, v221
	v_pk_add_f32 v[50:51], v[50:51], v[52:53]
	v_lshlrev_b32_e32 v206, 16, v220
	v_lshlrev_b32_e32 v208, 16, v221
	v_mul_f32_e32 v52, v209, v209
	s_waitcnt vmcnt(19)
	v_and_b32_e32 v205, 0xffff0000, v223
	v_and_b32_e32 v204, 0xffff0000, v222
	v_mul_f32_e32 v64, v207, v207
	v_pk_fma_f32 v[52:53], v[208:209], v[208:209], v[52:53] op_sel_hi:[1,1,0]
	v_lshlrev_b32_e32 v203, 16, v223
	v_lshlrev_b32_e32 v202, 16, v222
	v_pk_mul_f32 v[62:63], v[204:205], v[204:205]
	s_waitcnt vmcnt(15)
	v_lshlrev_b32_e32 v191, 16, v238
	v_pk_fma_f32 v[64:65], v[206:207], v[206:207], v[64:65] op_sel_hi:[1,1,0]
	global_store_dwordx2 v234, v[188:189], s[18:19] offset:2048 nt
	v_pk_fma_f32 v[62:63], v[202:203], v[202:203], v[62:63]
	v_and_b32_e32 v189, 0xffff0000, v238
	v_mov_b32_e32 v190, v64
	v_mov_b32_e32 v158, v52
	v_mov_b32_e32 v159, v191
	v_mul_f32_e32 v160, v189, v189
	v_pk_add_f32 v[52:53], v[64:65], v[52:53]
	v_pk_mul_f32 v[64:65], v[190:191], v[158:159]
	v_pk_add_f32 v[62:63], v[62:63], v[62:63] op_sel:[0,1] op_sel_hi:[1,0]
	v_and_b32_e32 v199, 0xffff0000, v224
	v_and_b32_e32 v201, 0xffff0000, v225
	v_mov_b32_e32 v53, v65
	v_mov_b32_e32 v63, v160
	v_lshlrev_b32_e32 v198, 16, v224
	v_lshlrev_b32_e32 v200, 16, v225
	v_lshlrev_b32_e32 v196, 16, v239
	v_and_b32_e32 v197, 0xffff0000, v239
	v_pk_add_f32 v[52:53], v[52:53], v[62:63]
	v_mul_f32_e32 v62, v199, v199
	v_mul_f32_e32 v64, v201, v201
	v_mul_f32_e32 v161, v196, v196
	v_mul_f32_e32 v166, v197, v197
	v_pk_fma_f32 v[62:63], v[198:199], v[198:199], v[62:63] op_sel_hi:[1,1,0]
	v_pk_fma_f32 v[64:65], v[200:201], v[200:201], v[64:65] op_sel_hi:[1,1,0]
	v_mov_b32_e32 v63, v161
	v_mov_b32_e32 v65, v166
	v_pk_add_f32 v[62:63], v[62:63], v[64:65]
	s_waitcnt vmcnt(14)
	v_and_b32_e32 v195, 0xffff0000, v241
	v_and_b32_e32 v194, 0xffff0000, v240
	v_pk_add_f32 v[52:53], v[52:53], v[62:63]
	v_lshlrev_b32_e32 v193, 16, v241
	v_lshlrev_b32_e32 v192, 16, v240
	v_pk_mul_f32 v[62:63], v[194:195], v[194:195]
	s_waitcnt vmcnt(12)
	v_and_b32_e32 v187, 0xffff0000, v243
	v_pk_fma_f32 v[62:63], v[192:193], v[192:193], v[62:63]
	v_and_b32_e32 v186, 0xffff0000, v242
	v_pk_add_f32 v[62:63], v[62:63], v[62:63] op_sel:[0,1] op_sel_hi:[1,0]
	s_waitcnt vmcnt(8)
	v_lshlrev_b32_e32 v167, 16, v244
	v_pk_add_f32 v[52:53], v[52:53], v[52:53] op_sel:[0,1] op_sel_hi:[1,0]
	v_lshlrev_b32_e32 v185, 16, v243
	v_lshlrev_b32_e32 v184, 16, v242
	v_pk_mul_f32 v[64:65], v[186:187], v[186:187]
	v_lshlrev_b32_e32 v168, 16, v218
	v_and_b32_e32 v169, 0xffff0000, v218
	v_lshlrev_b32_e32 v182, 16, v219
	v_and_b32_e32 v183, 0xffff0000, v219
	v_mov_b32_e32 v166, v52
	v_mov_b32_e32 v218, v62
	v_mov_b32_e32 v219, v167
	v_pk_fma_f32 v[64:65], v[184:185], v[184:185], v[64:65]
	v_and_b32_e32 v161, 0xffff0000, v244
	v_pk_add_f32 v[52:53], v[52:53], v[62:63]
	v_pk_mul_f32 v[62:63], v[166:167], v[218:219]
	v_mul_f32_e32 v160, v161, v161
	v_mov_b32_e32 v53, v63
	v_pk_add_f32 v[62:63], v[64:65], v[64:65] op_sel:[0,1] op_sel_hi:[1,0]
	v_lshlrev_b32_e32 v158, 16, v245
	v_mov_b32_e32 v63, v160
	v_and_b32_e32 v159, 0xffff0000, v245
	v_pk_add_f32 v[52:53], v[52:53], v[62:63]
	v_mul_f32_e32 v62, v169, v169
	v_mul_f32_e32 v64, v183, v183
	v_mul_f32_e32 v190, v158, v158
	v_mul_f32_e32 v220, v159, v159
	v_pk_fma_f32 v[62:63], v[168:169], v[168:169], v[62:63] op_sel_hi:[1,1,0]
	v_pk_fma_f32 v[64:65], v[182:183], v[182:183], v[64:65] op_sel_hi:[1,1,0]
	v_mov_b32_e32 v63, v190
	v_mov_b32_e32 v65, v220
	v_pk_add_f32 v[62:63], v[62:63], v[64:65]
	v_and_b32_sdwa v64, v39, v235 dst_sel:DWORD dst_unused:UNUSED_PAD src0_sel:WORD_1 src1_sel:DWORD
	v_pk_add_f32 v[52:53], v[52:53], v[62:63]
	v_mov_b32_e32 v63, v50
	v_mov_b32_e32 v62, v52
	v_mov_b32_e32 v50, v53
	v_pk_add_f32 v[50:51], v[62:63], v[50:51]
	ds_bpermute_b32 v53, v171, v51
	ds_bpermute_b32 v52, v171, v50
	v_and_b32_sdwa v63, v41, v235 dst_sel:DWORD dst_unused:UNUSED_PAD src0_sel:WORD_1 src1_sel:DWORD
	v_and_b32_sdwa v188, v40, v235 dst_sel:DWORD dst_unused:UNUSED_PAD src0_sel:WORD_1 src1_sel:DWORD
	v_add3_u32 v63, v41, v63, s44
	v_add3_u32 v64, v39, v64, s44
	s_waitcnt lgkmcnt(0)
	v_pk_add_f32 v[50:51], v[50:51], v[52:53]
	ds_bpermute_b32 v53, v226, v51
	ds_bpermute_b32 v52, v226, v50
	v_add3_u32 v62, v40, v188, s44
	v_and_b32_e32 v63, 0xffff0000, v63
	v_and_b32_e32 v64, 0xffff0000, v64
	s_addc_u32 s29, s34, s15
	s_waitcnt lgkmcnt(0)
	v_pk_add_f32 v[50:51], v[50:51], v[52:53]
	ds_bpermute_b32 v53, v228, v51
	ds_bpermute_b32 v52, v228, v50
	s_add_i32 s4, s8, -2
	v_or_b32_sdwa v63, v63, v62 dst_sel:DWORD dst_unused:UNUSED_PAD src0_sel:DWORD src1_sel:WORD_1
	v_or_b32_sdwa v62, v64, v246 dst_sel:DWORD dst_unused:UNUSED_PAD src0_sel:DWORD src1_sel:WORD_1
	s_ashr_i32 s5, s4, 31
	s_waitcnt lgkmcnt(0)
	v_pk_add_f32 v[50:51], v[50:51], v[52:53]
	ds_bpermute_b32 v53, v229, v51
	ds_bpermute_b32 v52, v229, v50
	global_store_dwordx2 v234, v[62:63], s[18:19] offset:3584 nt
	s_lshl_b64 s[18:19], s[4:5], 11
	s_lshl_b64 s[20:21], s[4:5], 12
	s_add_u32 s22, s96, s20
	s_waitcnt lgkmcnt(0)
	v_pk_add_f32 v[50:51], v[50:51], v[52:53]
	ds_bpermute_b32 v53, v230, v51
	ds_bpermute_b32 v52, v230, v50
	s_addc_u32 s23, s97, s21
	s_lshl_b64 s[4:5], s[4:5], 13
	s_add_u32 s30, s6, s4
	s_addc_u32 s31, s7, s5
	s_waitcnt lgkmcnt(0)
	v_pk_add_f32 v[50:51], v[50:51], v[52:53]
	ds_bpermute_b32 v53, v231, v51
	ds_bpermute_b32 v52, v231, v50
	v_lshl_add_u64 v[62:63], s[30:31], 0, v[178:179]
	s_add_u32 s14, s35, s24
	s_addc_u32 s15, s36, s25
	v_mov_b32_e32 v188, v191
	s_waitcnt lgkmcnt(0)
	v_pk_add_f32 v[50:51], v[50:51], v[52:53]
	s_nop 0
	v_pk_fma_f32 v[50:51], v[50:51], s[10:11], v[180:181] op_sel_hi:[1,0,0]
	s_nop 0
	v_mul_f32_e32 v52, 0x4b800000, v51
	v_cmp_gt_f32_e64 s[4:5], s43, v51
	v_cmp_gt_f32_e32 vcc, s43, v50
	s_nop 0
	v_cndmask_b32_e64 v51, v51, v52, s[4:5]
	v_rsq_f32_e32 v51, v51
	s_nop 0
	v_mul_f32_e32 v52, 0x45800000, v51
	v_cndmask_b32_e64 v52, v51, v52, s[4:5]
	v_pk_mul_f32 v[64:65], v[214:215], v[52:53] op_sel_hi:[1,0]
	v_pk_mul_f32 v[214:215], v[216:217], v[52:53] op_sel_hi:[1,0]
	v_pk_fma_f32 v[64:65], v[26:27], v[64:65], v[30:31]
	v_pk_fma_f32 v[214:215], v[28:29], v[214:215], v[32:33]
	v_bfe_u32 v51, v64, 16, 1
	v_add3_u32 v51, v64, v51, s44
	v_bfe_u32 v53, v65, 16, 1
	v_lshrrev_b32_e32 v51, 16, v51
	v_add3_u32 v53, v65, v53, s44
	v_and_or_b32 v216, v53, s42, v51
	v_med3_f32 v53, v64, s45, v236
	v_med3_f32 v64, v65, s45, v236
	v_mov_b32_e32 v65, 0
	v_cvt_pk_fp8_f32 v65, v53, v64
	v_bfe_u32 v51, v214, 16, 1
	v_med3_f32 v64, v214, s45, v236
	v_med3_f32 v160, v215, s45, v236
	v_add3_u32 v51, v214, v51, s44
	v_bfe_u32 v53, v215, 16, 1
	v_cvt_pk_fp8_f32 v65, v64, v160 op_sel:[0,0,1]
	v_lshrrev_b32_e32 v51, 16, v51
	v_add3_u32 v53, v215, v53, s44
	v_and_or_b32 v217, v53, s42, v51
	global_store_dwordx2 v234, v[216:217], s[26:27]
	global_store_dword v237, v65, s[28:29]
	v_pk_mul_f32 v[64:65], v[210:211], v[52:53] op_sel_hi:[1,0]
	v_pk_mul_f32 v[210:211], v[212:213], v[52:53] op_sel_hi:[1,0]
	v_pk_fma_f32 v[64:65], v[90:91], v[64:65], v[94:95]
	v_pk_fma_f32 v[210:211], v[92:93], v[210:211], v[96:97]
	v_bfe_u32 v51, v64, 16, 1
	v_add3_u32 v51, v64, v51, s44
	v_bfe_u32 v53, v65, 16, 1
	v_lshrrev_b32_e32 v51, 16, v51
	v_add3_u32 v53, v65, v53, s44
	v_and_or_b32 v212, v53, s42, v51
	v_med3_f32 v53, v64, s45, v236
	v_med3_f32 v64, v65, s45, v236
	v_mov_b32_e32 v65, 0
	v_cvt_pk_fp8_f32 v65, v53, v64
	v_bfe_u32 v51, v210, 16, 1
	v_med3_f32 v64, v210, s45, v236
	v_med3_f32 v160, v211, s45, v236
	v_add3_u32 v51, v210, v51, s44
	v_bfe_u32 v53, v211, 16, 1
	v_cvt_pk_fp8_f32 v65, v64, v160 op_sel:[0,0,1]
	v_lshrrev_b32_e32 v51, 16, v51
	v_add3_u32 v53, v211, v53, s44
	v_and_or_b32 v213, v53, s42, v51
	global_store_dwordx2 v234, v[212:213], s[26:27] offset:512
	global_store_dword v237, v65, s[28:29] offset:256
	v_pk_mul_f32 v[64:65], v[66:67], v[52:53] op_sel_hi:[1,0]
	v_pk_mul_f32 v[66:67], v[68:69], v[52:53] op_sel_hi:[1,0]
	v_pk_fma_f32 v[64:65], v[82:83], v[64:65], v[86:87]
	v_pk_fma_f32 v[66:67], v[84:85], v[66:67], v[88:89]
	v_bfe_u32 v51, v64, 16, 1
	v_add3_u32 v51, v64, v51, s44
	v_bfe_u32 v53, v65, 16, 1
	v_lshrrev_b32_e32 v51, 16, v51
	v_add3_u32 v53, v65, v53, s44
	v_and_or_b32 v68, v53, s42, v51
	v_med3_f32 v53, v64, s45, v236
	v_med3_f32 v64, v65, s45, v236
	v_mov_b32_e32 v65, 0
	v_cvt_pk_fp8_f32 v65, v53, v64
	v_bfe_u32 v53, v67, 16, 1
	v_bfe_u32 v51, v66, 16, 1
	v_add3_u32 v53, v67, v53, s44
	v_add3_u32 v51, v66, v51, s44
	v_pk_mul_f32 v[58:59], v[58:59], v[52:53] op_sel_hi:[1,0]
	v_lshrrev_b32_e32 v51, 16, v51
	v_pk_fma_f32 v[58:59], v[74:75], v[58:59], v[78:79]
	v_and_or_b32 v69, v53, s42, v51
	v_bfe_u32 v51, v58, 16, 1
	v_pk_mul_f32 v[60:61], v[60:61], v[52:53] op_sel_hi:[1,0]
	v_add3_u32 v51, v58, v51, s44
	v_bfe_u32 v53, v59, 16, 1
	v_med3_f32 v64, v66, s45, v236
	v_med3_f32 v66, v67, s45, v236
	v_lshrrev_b32_e32 v51, 16, v51
	v_add3_u32 v53, v59, v53, s44
	v_cvt_pk_fp8_f32 v65, v64, v66 op_sel:[0,0,1]
	v_pk_fma_f32 v[60:61], v[76:77], v[60:61], v[80:81]
	v_and_or_b32 v64, v53, s42, v51
	v_med3_f32 v53, v58, s45, v236
	v_med3_f32 v58, v59, s45, v236
	v_mov_b32_e32 v59, 0
	v_cvt_pk_fp8_f32 v59, v53, v58
	v_bfe_u32 v53, v61, 16, 1
	v_bfe_u32 v51, v60, 16, 1
	v_add3_u32 v53, v61, v53, s44
	v_add3_u32 v51, v60, v51, s44
	v_pk_mul_f32 v[54:55], v[54:55], v[52:53] op_sel_hi:[1,0]
	v_lshrrev_b32_e32 v51, 16, v51
	v_pk_fma_f32 v[54:55], v[34:35], v[54:55], v[70:71]
	global_store_dwordx2 v234, v[68:69], s[26:27] offset:1024
	global_store_dword v237, v65, s[28:29] offset:512
	v_and_or_b32 v65, v53, s42, v51
	v_bfe_u32 v51, v54, 16, 1
	v_pk_mul_f32 v[56:57], v[56:57], v[52:53] op_sel_hi:[1,0]
	v_add3_u32 v51, v54, v51, s44
	v_bfe_u32 v53, v55, 16, 1
	v_med3_f32 v58, v60, s45, v236
	v_med3_f32 v60, v61, s45, v236
	v_lshrrev_b32_e32 v51, 16, v51
	v_add3_u32 v53, v55, v53, s44
	v_cvt_pk_fp8_f32 v59, v58, v60 op_sel:[0,0,1]
	v_pk_fma_f32 v[56:57], v[36:37], v[56:57], v[72:73]
	v_and_or_b32 v58, v53, s42, v51
	v_med3_f32 v53, v54, s45, v236
	v_med3_f32 v54, v55, s45, v236
	v_mov_b32_e32 v55, 0
	v_cvt_pk_fp8_f32 v55, v53, v54
	v_bfe_u32 v53, v57, 16, 1
	v_bfe_u32 v51, v56, 16, 1
	v_add3_u32 v53, v57, v53, s44
	v_add3_u32 v51, v56, v51, s44
	v_pk_mul_f32 v[46:47], v[46:47], v[52:53] op_sel_hi:[1,0]
	v_lshrrev_b32_e32 v51, 16, v51
	v_pk_fma_f32 v[46:47], v[18:19], v[46:47], v[22:23]
	global_store_dwordx2 v234, v[64:65], s[26:27] offset:1536
	global_store_dword v237, v59, s[28:29] offset:768
	v_and_or_b32 v59, v53, s42, v51
	v_bfe_u32 v51, v46, 16, 1
	v_pk_mul_f32 v[48:49], v[48:49], v[52:53] op_sel_hi:[1,0]
	v_add3_u32 v51, v46, v51, s44
	v_bfe_u32 v53, v47, 16, 1
	v_med3_f32 v54, v56, s45, v236
	v_med3_f32 v56, v57, s45, v236
	v_lshrrev_b32_e32 v51, 16, v51
	v_add3_u32 v53, v47, v53, s44
	v_cvt_pk_fp8_f32 v55, v54, v56 op_sel:[0,0,1]
	v_and_or_b32 v54, v53, s42, v51
	v_med3_f32 v46, v46, s45, v236
	v_med3_f32 v47, v47, s45, v236
	v_mov_b32_e32 v53, 0
	v_cvt_pk_fp8_f32 v53, v46, v47
	v_pk_fma_f32 v[48:49], v[20:21], v[48:49], v[24:25]
	global_store_dwordx2 v234, v[58:59], s[26:27] offset:2048
	global_store_dword v237, v55, s[28:29] offset:1024
	v_bfe_u32 v51, v48, 16, 1
	v_add3_u32 v51, v48, v51, s44
	v_med3_f32 v47, v48, s45, v236
	v_med3_f32 v48, v49, s45, v236
	v_cvt_pk_fp8_f32 v53, v47, v48 op_sel:[0,0,1]
	v_bfe_u32 v46, v49, 16, 1
	v_lshrrev_b32_e32 v51, 16, v51
	v_add3_u32 v46, v49, v46, s44
	v_pk_mul_f32 v[42:43], v[42:43], v[52:53] op_sel_hi:[1,0]
	v_and_or_b32 v55, v46, s42, v51
	v_pk_fma_f32 v[42:43], v[10:11], v[42:43], v[14:15]
	v_pk_mul_f32 v[44:45], v[44:45], v[52:53] op_sel_hi:[1,0]
	v_bfe_u32 v46, v42, 16, 1
	v_bfe_u32 v47, v43, 16, 1
	v_add3_u32 v46, v42, v46, s44
	v_add3_u32 v47, v43, v47, s44
	v_med3_f32 v42, v42, s45, v236
	v_med3_f32 v43, v43, s45, v236
	v_mov_b32_e32 v48, 0
	v_pk_fma_f32 v[44:45], v[12:13], v[44:45], v[16:17]
	v_lshrrev_b32_e32 v46, 16, v46
	v_cvt_pk_fp8_f32 v48, v42, v43
	v_and_or_b32 v46, v47, s42, v46
	v_bfe_u32 v47, v44, 16, 1
	v_add3_u32 v47, v44, v47, s44
	v_bfe_u32 v42, v45, 16, 1
	v_pk_mul_f32 v[38:39], v[38:39], v[52:53] op_sel_hi:[1,0]
	v_lshrrev_b32_e32 v47, 16, v47
	v_med3_f32 v43, v44, s45, v236
	v_med3_f32 v44, v45, s45, v236
	v_add3_u32 v42, v45, v42, s44
	v_pk_fma_f32 v[38:39], v[2:3], v[38:39], v[6:7]
	v_cvt_pk_fp8_f32 v48, v43, v44 op_sel:[0,0,1]
	v_and_or_b32 v47, v42, s42, v47
	v_bfe_u32 v42, v38, 16, 1
	v_bfe_u32 v43, v39, 16, 1
	v_add3_u32 v42, v38, v42, s44
	v_add3_u32 v43, v39, v43, s44
	v_med3_f32 v38, v38, s45, v236
	v_med3_f32 v39, v39, s45, v236
	v_mov_b32_e32 v44, 0
	v_pk_mul_f32 v[40:41], v[40:41], v[52:53] op_sel_hi:[1,0]
	v_cvt_pk_fp8_f32 v44, v38, v39
	v_pk_fma_f32 v[40:41], v[4:5], v[40:41], v[8:9]
	v_lshrrev_b32_e32 v42, 16, v42
	v_and_or_b32 v42, v43, s42, v42
	v_bfe_u32 v43, v40, 16, 1
	v_add3_u32 v43, v40, v43, s44
	v_med3_f32 v39, v40, s45, v236
	v_med3_f32 v40, v41, s45, v236
	v_bfe_u32 v38, v41, 16, 1
	v_cvt_pk_fp8_f32 v44, v39, v40 op_sel:[0,0,1]
	v_lshrrev_b32_e32 v43, 16, v43
	v_add3_u32 v38, v41, v38, s44
	v_and_or_b32 v43, v38, s42, v43
	global_store_dwordx2 v234, v[54:55], s[26:27] offset:2560
	global_store_dword v237, v53, s[28:29] offset:1280
	global_store_dwordx2 v234, v[46:47], s[26:27] offset:3072
	global_store_dword v237, v48, s[28:29] offset:1536
	global_store_dwordx2 v234, v[42:43], s[26:27] offset:3584
	global_store_dword v237, v44, s[28:29] offset:1792
	global_load_dwordx2 v[212:213], v234, s[22:23]
	global_load_dwordx4 v[38:41], v178, s[30:31] nt
	global_load_dwordx2 v[214:215], v234, s[22:23] offset:512
	global_load_dwordx4 v[46:49], v178, s[30:31] offset:1024 nt
	global_load_dwordx2 v[216:217], v234, s[22:23] offset:1024
	global_load_dwordx4 v[54:57], v178, s[30:31] offset:2048 nt
	global_load_dwordx2 v[218:219], v234, s[22:23] offset:1536
	global_load_dwordx4 v[58:61], v178, s[30:31] offset:3072 nt
	global_load_dwordx2 v[220:221], v234, s[22:23] offset:2048
	v_add_co_u32_e64 v42, s[4:5], s41, v62
	v_mul_f32_e32 v44, 0x4b800000, v50
	s_nop 0
	v_addc_co_u32_e64 v43, s[4:5], 0, v63, s[4:5]
	v_cndmask_b32_e32 v44, v50, v44, vcc
	global_load_dwordx4 v[66:69], v[42:43], off nt
	global_load_dwordx2 v[222:223], v234, s[22:23] offset:2560
	global_load_dwordx4 v[62:65], v[42:43], off offset:1024 nt
	global_load_dwordx2 v[210:211], v234, s[22:23] offset:3072
	v_rsq_f32_e32 v160, v44
	global_load_dwordx4 v[50:53], v[42:43], off offset:2048 nt
	global_load_dwordx2 v[224:225], v234, s[22:23] offset:3584
	s_nop 0
	global_load_dwordx4 v[42:45], v[42:43], off offset:3072 nt
	s_add_u32 s26, s11, s24
	s_addc_u32 s27, s13, s25
	v_mul_f32_e32 v166, 0x45800000, v160
	v_cndmask_b32_e32 v166, v160, v166, vcc
	v_pk_mul_f32 v[206:207], v[166:167], v[206:207] op_sel_hi:[0,1]
	v_pk_mul_f32 v[208:209], v[166:167], v[208:209] op_sel_hi:[0,1]
	v_pk_fma_f32 v[162:163], v[98:99], v[206:207], v[162:163]
	v_pk_fma_f32 v[164:165], v[100:101], v[208:209], v[164:165]
	v_and_b32_sdwa v99, v162, v235 dst_sel:DWORD dst_unused:UNUSED_PAD src0_sel:WORD_1 src1_sel:DWORD
	v_add3_u32 v100, v162, v99, s44
	v_and_b32_sdwa v99, v165, v235 dst_sel:DWORD dst_unused:UNUSED_PAD src0_sel:WORD_1 src1_sel:DWORD
	v_and_b32_sdwa v101, v163, v235 dst_sel:DWORD dst_unused:UNUSED_PAD src0_sel:WORD_1 src1_sel:DWORD
	v_and_b32_sdwa v98, v164, v235 dst_sel:DWORD dst_unused:UNUSED_PAD src0_sel:WORD_1 src1_sel:DWORD
	v_add3_u32 v99, v165, v99, s44
	v_add3_u32 v101, v163, v101, s44
	v_add3_u32 v98, v164, v98, s44
	v_and_b32_e32 v99, 0xffff0000, v99
	v_and_b32_e32 v101, 0xffff0000, v101
	v_or_b32_sdwa v99, v99, v98 dst_sel:DWORD dst_unused:UNUSED_PAD src0_sel:DWORD src1_sel:WORD_1
	v_or_b32_sdwa v98, v101, v100 dst_sel:DWORD dst_unused:UNUSED_PAD src0_sel:DWORD src1_sel:WORD_1
	global_store_dwordx2 v234, v[98:99], s[14:15] nt
	v_mov_b32_e32 v98, v203
	v_mov_b32_e32 v203, v204
	v_mov_b32_e32 v99, v205
	v_pk_mul_f32 v[100:101], v[166:167], v[202:203] op_sel_hi:[0,1]
	v_pk_mul_f32 v[98:99], v[166:167], v[98:99] op_sel_hi:[0,1]
	v_pk_fma_f32 v[154:155], v[102:103], v[100:101], v[154:155]
	v_pk_fma_f32 v[156:157], v[104:105], v[98:99], v[156:157]
	v_and_b32_sdwa v99, v154, v235 dst_sel:DWORD dst_unused:UNUSED_PAD src0_sel:WORD_1 src1_sel:DWORD
	v_add3_u32 v100, v154, v99, s44
	v_and_b32_sdwa v99, v157, v235 dst_sel:DWORD dst_unused:UNUSED_PAD src0_sel:WORD_1 src1_sel:DWORD
	v_and_b32_sdwa v101, v155, v235 dst_sel:DWORD dst_unused:UNUSED_PAD src0_sel:WORD_1 src1_sel:DWORD
	v_and_b32_sdwa v98, v156, v235 dst_sel:DWORD dst_unused:UNUSED_PAD src0_sel:WORD_1 src1_sel:DWORD
	v_add3_u32 v99, v157, v99, s44
	v_add3_u32 v101, v155, v101, s44
	v_add3_u32 v98, v156, v98, s44
	v_and_b32_e32 v99, 0xffff0000, v99
	v_and_b32_e32 v101, 0xffff0000, v101
	v_or_b32_sdwa v99, v99, v98 dst_sel:DWORD dst_unused:UNUSED_PAD src0_sel:DWORD src1_sel:WORD_1
	v_or_b32_sdwa v98, v101, v100 dst_sel:DWORD dst_unused:UNUSED_PAD src0_sel:DWORD src1_sel:WORD_1
	v_mov_b32_e32 v100, v163
	v_mov_b32_e32 v101, v155
	global_store_dwordx2 v234, v[98:99], s[14:15] offset:512 nt
	v_mov_b32_e32 v98, v162
	v_mov_b32_e32 v99, v154
	v_pk_mul_f32 v[100:101], v[100:101], v[100:101]
	v_mov_b32_e32 v102, v165
	v_pk_fma_f32 v[98:99], v[98:99], v[98:99], v[100:101]
	v_mov_b32_e32 v100, v164
	v_mov_b32_e32 v101, v156
	v_pk_mul_f32 v[100:101], v[100:101], v[100:101]
	v_mov_b32_e32 v103, v157
	v_pk_fma_f32 v[100:101], v[102:103], v[102:103], v[100:101]
	v_pk_mul_f32 v[102:103], v[166:167], v[198:199] op_sel_hi:[0,1]
	v_pk_add_f32 v[98:99], v[98:99], v[100:101]
	v_pk_mul_f32 v[100:101], v[166:167], v[200:201] op_sel_hi:[0,1]
	v_pk_fma_f32 v[150:151], v[106:107], v[102:103], v[150:151]
	v_pk_fma_f32 v[152:153], v[108:109], v[100:101], v[152:153]
	v_pk_add_f32 v[98:99], v[98:99], v[98:99] op_sel_hi:[0,1]
	v_and_b32_sdwa v101, v153, v235 dst_sel:DWORD dst_unused:UNUSED_PAD src0_sel:WORD_1 src1_sel:DWORD
	v_and_b32_sdwa v102, v151, v235 dst_sel:DWORD dst_unused:UNUSED_PAD src0_sel:WORD_1 src1_sel:DWORD
	v_and_b32_sdwa v98, v152, v235 dst_sel:DWORD dst_unused:UNUSED_PAD src0_sel:WORD_1 src1_sel:DWORD
	v_and_b32_sdwa v100, v150, v235 dst_sel:DWORD dst_unused:UNUSED_PAD src0_sel:WORD_1 src1_sel:DWORD
	v_add3_u32 v101, v153, v101, s44
	v_add3_u32 v102, v151, v102, s44
	v_add3_u32 v100, v150, v100, s44
	v_add3_u32 v98, v152, v98, s44
	v_and_b32_e32 v101, 0xffff0000, v101
	v_and_b32_e32 v102, 0xffff0000, v102
	v_or_b32_sdwa v101, v101, v98 dst_sel:DWORD dst_unused:UNUSED_PAD src0_sel:DWORD src1_sel:WORD_1
	v_or_b32_sdwa v100, v102, v100 dst_sel:DWORD dst_unused:UNUSED_PAD src0_sel:DWORD src1_sel:WORD_1
	global_store_dwordx2 v234, v[100:101], s[14:15] offset:1024 nt
	v_pk_mul_f32 v[100:101], v[152:153], v[152:153]
	v_pk_mul_f32 v[102:103], v[150:151], v[150:151]
	v_mov_b32_e32 v106, v192
	v_pk_mov_b32 v[104:105], v[102:103], v[100:101] op_sel:[1,0]
	v_mov_b32_e32 v103, v101
	v_pk_add_f32 v[100:101], v[102:103], v[104:105]
	v_pk_mul_f32 v[102:103], v[196:197], v[166:167] op_sel_hi:[1,0]
	v_pk_mul_f32 v[104:105], v[188:189], v[166:167] op_sel_hi:[1,0]
	v_pk_fma_f32 v[148:149], v[112:113], v[102:103], v[148:149]
	v_pk_fma_f32 v[146:147], v[110:111], v[104:105], v[146:147]
	v_pk_add_f32 v[100:101], v[100:101], v[100:101] op_sel_hi:[0,1]
	v_and_b32_sdwa v102, v149, v235 dst_sel:DWORD dst_unused:UNUSED_PAD src0_sel:WORD_1 src1_sel:DWORD
	v_and_b32_sdwa v103, v147, v235 dst_sel:DWORD dst_unused:UNUSED_PAD src0_sel:WORD_1 src1_sel:DWORD
	v_and_b32_sdwa v98, v148, v235 dst_sel:DWORD dst_unused:UNUSED_PAD src0_sel:WORD_1 src1_sel:DWORD
	v_and_b32_sdwa v100, v146, v235 dst_sel:DWORD dst_unused:UNUSED_PAD src0_sel:WORD_1 src1_sel:DWORD
	v_add3_u32 v102, v149, v102, s44
	v_add3_u32 v103, v147, v103, s44
	v_add3_u32 v100, v146, v100, s44
	v_add3_u32 v98, v148, v98, s44
	v_and_b32_e32 v102, 0xffff0000, v102
	v_and_b32_e32 v104, 0xffff0000, v103
	v_or_b32_sdwa v103, v102, v98 dst_sel:DWORD dst_unused:UNUSED_PAD src0_sel:DWORD src1_sel:WORD_1
	v_or_b32_sdwa v102, v104, v100 dst_sel:DWORD dst_unused:UNUSED_PAD src0_sel:DWORD src1_sel:WORD_1
	v_mul_f32_e32 v98, v146, v146
	v_mov_b32_e32 v107, v194
	v_mov_b32_e32 v194, v193
	global_store_dwordx2 v234, v[102:103], s[14:15] offset:1536 nt
	v_pk_fma_f32 v[102:103], v[146:147], v[146:147], v[98:99] op_sel_hi:[1,1,0]
	v_mul_f32_e32 v98, v148, v148
	v_pk_mul_f32 v[106:107], v[166:167], v[106:107] op_sel_hi:[0,1]
	v_pk_mul_f32 v[108:109], v[166:167], v[194:195] op_sel_hi:[0,1]
	v_pk_fma_f32 v[104:105], v[148:149], v[148:149], v[98:99] op_sel_hi:[1,1,0]
	v_pk_fma_f32 v[144:145], v[116:117], v[108:109], v[144:145]
	v_pk_fma_f32 v[142:143], v[114:115], v[106:107], v[142:143]
	v_and_b32_sdwa v102, v145, v235 dst_sel:DWORD dst_unused:UNUSED_PAD src0_sel:WORD_1 src1_sel:DWORD
	v_and_b32_sdwa v104, v143, v235 dst_sel:DWORD dst_unused:UNUSED_PAD src0_sel:WORD_1 src1_sel:DWORD
	v_and_b32_sdwa v98, v144, v235 dst_sel:DWORD dst_unused:UNUSED_PAD src0_sel:WORD_1 src1_sel:DWORD
	v_and_b32_sdwa v100, v142, v235 dst_sel:DWORD dst_unused:UNUSED_PAD src0_sel:WORD_1 src1_sel:DWORD
	v_add3_u32 v102, v145, v102, s44
	v_add3_u32 v104, v143, v104, s44
	v_add3_u32 v100, v142, v100, s44
	v_add3_u32 v98, v144, v98, s44
	v_and_b32_e32 v102, 0xffff0000, v102
	v_and_b32_e32 v104, 0xffff0000, v104
	v_or_b32_sdwa v107, v102, v98 dst_sel:DWORD dst_unused:UNUSED_PAD src0_sel:DWORD src1_sel:WORD_1
	v_or_b32_sdwa v106, v104, v100 dst_sel:DWORD dst_unused:UNUSED_PAD src0_sel:DWORD src1_sel:WORD_1
	v_mul_f32_e32 v102, v142, v142
	v_mul_f32_e32 v104, v143, v143
	v_mul_f32_e32 v98, v144, v144
	v_mul_f32_e32 v100, v145, v145
	v_pk_add_f32 v[102:103], v[102:103], v[104:105]
	v_pk_add_f32 v[98:99], v[100:101], v[98:99]
	v_mov_b32_e32 v100, v185
	v_mov_b32_e32 v101, v187
	v_mov_b32_e32 v185, v186
	v_pk_add_f32 v[98:99], v[102:103], v[98:99]
	v_pk_mul_f32 v[100:101], v[166:167], v[100:101] op_sel_hi:[0,1]
	v_pk_mul_f32 v[102:103], v[166:167], v[184:185] op_sel_hi:[0,1]
	v_pk_fma_f32 v[184:185], v[118:119], v[102:103], v[138:139]
	v_pk_fma_f32 v[186:187], v[120:121], v[100:101], v[140:141]
	v_pk_add_f32 v[98:99], v[98:99], v[98:99] op_sel_hi:[0,1]
	v_and_b32_sdwa v101, v187, v235 dst_sel:DWORD dst_unused:UNUSED_PAD src0_sel:WORD_1 src1_sel:DWORD
	v_and_b32_sdwa v102, v185, v235 dst_sel:DWORD dst_unused:UNUSED_PAD src0_sel:WORD_1 src1_sel:DWORD
	v_and_b32_sdwa v98, v186, v235 dst_sel:DWORD dst_unused:UNUSED_PAD src0_sel:WORD_1 src1_sel:DWORD
	v_and_b32_sdwa v100, v184, v235 dst_sel:DWORD dst_unused:UNUSED_PAD src0_sel:WORD_1 src1_sel:DWORD
	v_add3_u32 v101, v187, v101, s44
	v_add3_u32 v102, v185, v102, s44
	v_add3_u32 v100, v184, v100, s44
	v_add3_u32 v98, v186, v98, s44
	v_and_b32_e32 v101, 0xffff0000, v101
	v_and_b32_e32 v102, 0xffff0000, v102
	v_or_b32_sdwa v101, v101, v98 dst_sel:DWORD dst_unused:UNUSED_PAD src0_sel:DWORD src1_sel:WORD_1
	v_or_b32_sdwa v100, v102, v100 dst_sel:DWORD dst_unused:UNUSED_PAD src0_sel:DWORD src1_sel:WORD_1
	global_store_dwordx2 v234, v[100:101], s[14:15] offset:2560 nt
	v_pk_mul_f32 v[100:101], v[186:187], v[186:187]
	v_pk_mul_f32 v[102:103], v[184:185], v[184:185]
	v_mov_b32_e32 v160, v167
	v_pk_mov_b32 v[104:105], v[102:103], v[100:101] op_sel:[1,0]
	v_mov_b32_e32 v103, v101
	v_pk_add_f32 v[100:101], v[102:103], v[104:105]
	v_pk_mul_f32 v[102:103], v[166:167], v[182:183] op_sel_hi:[0,1]
	v_pk_mul_f32 v[104:105], v[166:167], v[168:169] op_sel_hi:[0,1]
	v_pk_fma_f32 v[138:139], v[122:123], v[104:105], v[134:135]
	v_pk_fma_f32 v[140:141], v[124:125], v[102:103], v[136:137]
	v_pk_add_f32 v[100:101], v[100:101], v[100:101] op_sel_hi:[0,1]
	v_and_b32_sdwa v102, v141, v235 dst_sel:DWORD dst_unused:UNUSED_PAD src0_sel:WORD_1 src1_sel:DWORD
	v_and_b32_sdwa v103, v139, v235 dst_sel:DWORD dst_unused:UNUSED_PAD src0_sel:WORD_1 src1_sel:DWORD
	v_and_b32_sdwa v98, v140, v235 dst_sel:DWORD dst_unused:UNUSED_PAD src0_sel:WORD_1 src1_sel:DWORD
	v_and_b32_sdwa v100, v138, v235 dst_sel:DWORD dst_unused:UNUSED_PAD src0_sel:WORD_1 src1_sel:DWORD
	v_add3_u32 v102, v141, v102, s44
	v_add3_u32 v103, v139, v103, s44
	v_add3_u32 v100, v138, v100, s44
	v_add3_u32 v98, v140, v98, s44
	v_and_b32_e32 v102, 0xffff0000, v102
	v_and_b32_e32 v104, 0xffff0000, v103
	global_store_dwordx2 v234, v[106:107], s[14:15] offset:2048 nt
	v_or_b32_sdwa v103, v102, v98 dst_sel:DWORD dst_unused:UNUSED_PAD src0_sel:DWORD src1_sel:WORD_1
	v_or_b32_sdwa v102, v104, v100 dst_sel:DWORD dst_unused:UNUSED_PAD src0_sel:DWORD src1_sel:WORD_1
	v_mul_f32_e32 v98, v138, v138
	v_pk_mul_f32 v[106:107], v[160:161], v[166:167] op_sel_hi:[1,0]
	global_store_dwordx2 v234, v[102:103], s[14:15] offset:3072 nt
	v_pk_fma_f32 v[102:103], v[138:139], v[138:139], v[98:99] op_sel_hi:[1,1,0]
	v_mul_f32_e32 v98, v140, v140
	v_pk_mul_f32 v[108:109], v[158:159], v[166:167] op_sel_hi:[1,0]
	s_waitcnt vmcnt(47)
	v_pk_fma_f32 v[136:137], v[126:127], v[106:107], v[130:131]
	v_pk_fma_f32 v[104:105], v[140:141], v[140:141], v[98:99] op_sel_hi:[1,1,0]
	v_pk_fma_f32 v[134:135], v[128:129], v[108:109], v[132:133]
	v_and_b32_sdwa v98, v136, v235 dst_sel:DWORD dst_unused:UNUSED_PAD src0_sel:WORD_1 src1_sel:DWORD
	v_add3_u32 v188, v136, v98, s44
	v_mul_f32_e32 v102, v136, v136
	v_mul_f32_e32 v104, v137, v137
	v_mul_f32_e32 v98, v134, v134
	v_mul_f32_e32 v100, v135, v135
	v_pk_add_f32 v[102:103], v[102:103], v[104:105]
	v_pk_add_f32 v[98:99], v[100:101], v[98:99]
	s_waitcnt vmcnt(22)
	v_and_b32_e32 v131, 0xffff0000, v212
	v_and_b32_e32 v133, 0xffff0000, v213
	v_pk_add_f32 v[158:159], v[102:103], v[98:99]
	v_lshlrev_b32_e32 v130, 16, v212
	v_lshlrev_b32_e32 v132, 16, v213
	v_mul_f32_e32 v98, v133, v133
	s_waitcnt vmcnt(20)
	v_and_b32_e32 v129, 0xffff0000, v215
	v_and_b32_e32 v128, 0xffff0000, v214
	v_mul_f32_e32 v102, v131, v131
	v_pk_fma_f32 v[98:99], v[132:133], v[132:133], v[98:99] op_sel_hi:[1,1,0]
	v_lshlrev_b32_e32 v127, 16, v215
	v_lshlrev_b32_e32 v126, 16, v214
	v_pk_mul_f32 v[100:101], v[128:129], v[128:129]
	s_waitcnt vmcnt(16)
	v_lshlrev_b32_e32 v121, 16, v218
	v_pk_fma_f32 v[102:103], v[130:131], v[130:131], v[102:103] op_sel_hi:[1,1,0]
	v_pk_fma_f32 v[100:101], v[126:127], v[126:127], v[100:101]
	v_and_b32_e32 v119, 0xffff0000, v218
	v_mov_b32_e32 v120, v102
	v_mov_b32_e32 v104, v98
	v_mov_b32_e32 v105, v121
	v_mul_f32_e32 v106, v119, v119
	v_pk_add_f32 v[98:99], v[102:103], v[98:99]
	v_pk_mul_f32 v[102:103], v[120:121], v[104:105]
	v_pk_add_f32 v[100:101], v[100:101], v[100:101] op_sel:[0,1] op_sel_hi:[1,0]
	v_and_b32_e32 v123, 0xffff0000, v216
	v_and_b32_e32 v125, 0xffff0000, v217
	v_mov_b32_e32 v99, v103
	v_mov_b32_e32 v101, v106
	v_lshlrev_b32_e32 v122, 16, v216
	v_lshlrev_b32_e32 v124, 16, v217
	v_lshlrev_b32_e32 v116, 16, v219
	v_and_b32_e32 v117, 0xffff0000, v219
	v_pk_add_f32 v[98:99], v[98:99], v[100:101]
	v_mul_f32_e32 v100, v123, v123
	v_mul_f32_e32 v102, v125, v125
	v_mul_f32_e32 v107, v116, v116
	v_mul_f32_e32 v108, v117, v117
	v_pk_fma_f32 v[100:101], v[122:123], v[122:123], v[100:101] op_sel_hi:[1,1,0]
	v_pk_fma_f32 v[102:103], v[124:125], v[124:125], v[102:103] op_sel_hi:[1,1,0]
	v_mov_b32_e32 v101, v107
	v_mov_b32_e32 v103, v108
	v_pk_add_f32 v[100:101], v[100:101], v[102:103]
	s_waitcnt vmcnt(14)
	v_and_b32_e32 v115, 0xffff0000, v221
	v_and_b32_e32 v114, 0xffff0000, v220
	v_pk_add_f32 v[160:161], v[98:99], v[100:101]
	v_lshlrev_b32_e32 v113, 16, v221
	v_lshlrev_b32_e32 v112, 16, v220
	v_pk_mul_f32 v[98:99], v[114:115], v[114:115]
	s_waitcnt vmcnt(12)
	v_and_b32_e32 v111, 0xffff0000, v223
	v_pk_fma_f32 v[98:99], v[112:113], v[112:113], v[98:99]
	v_and_b32_e32 v110, 0xffff0000, v222
	v_pk_add_f32 v[166:167], v[98:99], v[98:99] op_sel:[0,1] op_sel_hi:[1,0]
	s_waitcnt vmcnt(8)
	v_lshlrev_b32_e32 v103, 16, v224
	v_pk_add_f32 v[160:161], v[160:161], v[160:161] op_sel:[0,1] op_sel_hi:[1,0]
	v_lshlrev_b32_e32 v109, 16, v223
	v_lshlrev_b32_e32 v108, 16, v222
	v_pk_mul_f32 v[98:99], v[110:111], v[110:111]
	v_mov_b32_e32 v102, v160
	v_mov_b32_e32 v182, v166
	v_mov_b32_e32 v183, v103
	v_pk_fma_f32 v[168:169], v[108:109], v[108:109], v[98:99]
	v_and_b32_e32 v101, 0xffff0000, v224
	v_pk_add_f32 v[160:161], v[160:161], v[166:167]
	v_pk_mul_f32 v[166:167], v[102:103], v[182:183]
	v_and_b32_e32 v105, 0xffff0000, v210
	v_mul_f32_e32 v100, v101, v101
	v_mov_b32_e32 v161, v167
	v_pk_add_f32 v[166:167], v[168:169], v[168:169] op_sel:[0,1] op_sel_hi:[1,0]
	v_lshlrev_b32_e32 v104, 16, v210
	v_and_b32_e32 v107, 0xffff0000, v211
	v_mov_b32_e32 v167, v100
	v_mul_f32_e32 v100, v105, v105
	v_lshlrev_b32_e32 v106, 16, v211
	v_lshlrev_b32_e32 v98, 16, v225
	v_and_b32_e32 v99, 0xffff0000, v225
	v_pk_add_f32 v[160:161], v[160:161], v[166:167]
	v_pk_fma_f32 v[166:167], v[104:105], v[104:105], v[100:101] op_sel_hi:[1,1,0]
	v_mul_f32_e32 v100, v107, v107
	v_mul_f32_e32 v120, v98, v98
	v_mul_f32_e32 v189, v99, v99
	v_pk_fma_f32 v[168:169], v[106:107], v[106:107], v[100:101] op_sel_hi:[1,1,0]
	v_mov_b32_e32 v167, v120
	v_mov_b32_e32 v169, v189
	v_pk_add_f32 v[166:167], v[166:167], v[168:169]
	v_and_b32_sdwa v118, v134, v235 dst_sel:DWORD dst_unused:UNUSED_PAD src0_sel:WORD_1 src1_sel:DWORD
	v_pk_add_f32 v[160:161], v[160:161], v[166:167]
	v_mov_b32_e32 v167, v158
	v_mov_b32_e32 v166, v160
	v_mov_b32_e32 v158, v161
	v_pk_add_f32 v[158:159], v[166:167], v[158:159]
	ds_bpermute_b32 v161, v171, v159
	ds_bpermute_b32 v160, v171, v158
	v_add3_u32 v100, v134, v118, s44
	v_and_b32_sdwa v102, v135, v235 dst_sel:DWORD dst_unused:UNUSED_PAD src0_sel:WORD_1 src1_sel:DWORD
	v_and_b32_sdwa v118, v137, v235 dst_sel:DWORD dst_unused:UNUSED_PAD src0_sel:WORD_1 src1_sel:DWORD
	v_add3_u32 v102, v135, v102, s44
	s_waitcnt lgkmcnt(0)
	v_pk_add_f32 v[158:159], v[158:159], v[160:161]
	ds_bpermute_b32 v161, v226, v159
	ds_bpermute_b32 v160, v226, v158
	v_add3_u32 v118, v137, v118, s44
	s_add_u32 s28, s33, s16
	v_and_b32_e32 v102, 0xffff0000, v102
	v_and_b32_e32 v118, 0xffff0000, v118
	s_waitcnt lgkmcnt(0)
	v_pk_add_f32 v[158:159], v[158:159], v[160:161]
	ds_bpermute_b32 v161, v228, v159
	ds_bpermute_b32 v160, v228, v158
	s_addc_u32 s29, s34, s17
	s_add_i32 s4, s8, -1
	v_or_b32_sdwa v167, v102, v100 dst_sel:DWORD dst_unused:UNUSED_PAD src0_sel:DWORD src1_sel:WORD_1
	v_or_b32_sdwa v166, v118, v188 dst_sel:DWORD dst_unused:UNUSED_PAD src0_sel:DWORD src1_sel:WORD_1
	s_waitcnt lgkmcnt(0)
	v_pk_add_f32 v[158:159], v[158:159], v[160:161]
	ds_bpermute_b32 v161, v229, v159
	ds_bpermute_b32 v160, v229, v158
	s_ashr_i32 s5, s4, 31
	global_store_dwordx2 v234, v[166:167], s[14:15] offset:3584 nt
	s_lshl_b64 s[14:15], s[4:5], 11
	s_lshl_b64 s[16:17], s[4:5], 12
	s_waitcnt lgkmcnt(0)
	v_pk_add_f32 v[158:159], v[158:159], v[160:161]
	ds_bpermute_b32 v161, v230, v159
	ds_bpermute_b32 v160, v230, v158
	s_add_u32 s24, s96, s16
	s_addc_u32 s25, s97, s17
	s_lshl_b64 s[4:5], s[4:5], 13
	s_add_u32 s30, s6, s4
	s_waitcnt lgkmcnt(0)
	v_pk_add_f32 v[158:159], v[158:159], v[160:161]
	ds_bpermute_b32 v161, v231, v159
	ds_bpermute_b32 v160, v231, v158
	s_addc_u32 s31, s7, s5
	v_lshl_add_u64 v[166:167], s[30:31], 0, v[178:179]
	s_add_u32 s22, s35, s20
	s_addc_u32 s23, s36, s21
	s_waitcnt lgkmcnt(0)
	v_pk_add_f32 v[158:159], v[158:159], v[160:161]
	v_mov_b32_e32 v118, v121
	v_pk_fma_f32 v[158:159], v[158:159], s[10:11], v[180:181] op_sel_hi:[1,0,0]
	s_add_u32 s20, s11, s20
	v_mul_f32_e32 v100, 0x4b800000, v159
	v_cmp_gt_f32_e64 s[4:5], s43, v159
	v_cmp_gt_f32_e32 vcc, s43, v158
	s_addc_u32 s21, s13, s21
	v_cndmask_b32_e64 v100, v159, v100, s[4:5]
	v_rsq_f32_e32 v100, v100
	s_add_u32 s18, s33, s18
	s_addc_u32 s19, s34, s19
	s_ashr_i32 s9, s8, 31
	v_mul_f32_e32 v102, 0x45800000, v100
	v_cndmask_b32_e64 v100, v100, v102, s[4:5]
	v_pk_mul_f32 v[160:161], v[162:163], v[100:101] op_sel_hi:[1,0]
	v_pk_mul_f32 v[162:163], v[164:165], v[100:101] op_sel_hi:[1,0]
	v_pk_fma_f32 v[26:27], v[26:27], v[160:161], v[30:31]
	v_pk_fma_f32 v[28:29], v[28:29], v[162:163], v[32:33]
	v_bfe_u32 v30, v26, 16, 1
	v_bfe_u32 v31, v27, 16, 1
	v_add3_u32 v30, v26, v30, s44
	v_add3_u32 v31, v27, v31, s44
	v_med3_f32 v26, v26, s45, v236
	v_med3_f32 v27, v27, s45, v236
	v_mov_b32_e32 v32, 0
	v_cvt_pk_fp8_f32 v32, v26, v27
	v_lshrrev_b32_e32 v30, 16, v30
	v_and_or_b32 v30, v31, s42, v30
	v_bfe_u32 v31, v28, 16, 1
	v_add3_u32 v31, v28, v31, s44
	v_bfe_u32 v26, v29, 16, 1
	v_med3_f32 v27, v28, s45, v236
	v_med3_f32 v28, v29, s45, v236
	v_lshrrev_b32_e32 v31, 16, v31
	v_cvt_pk_fp8_f32 v32, v27, v28 op_sel:[0,0,1]
	v_add3_u32 v26, v29, v26, s44
	v_and_or_b32 v31, v26, s42, v31
	v_pk_mul_f32 v[26:27], v[154:155], v[100:101] op_sel_hi:[1,0]
	global_store_dwordx2 v234, v[30:31], s[26:27]
	global_store_dword v237, v32, s[28:29]
	v_pk_fma_f32 v[26:27], v[90:91], v[26:27], v[94:95]
	v_mov_b32_e32 v32, 0
	v_bfe_u32 v30, v26, 16, 1
	v_bfe_u32 v31, v27, 16, 1
	v_add3_u32 v30, v26, v30, s44
	v_add3_u32 v31, v27, v31, s44
	v_med3_f32 v26, v26, s45, v236
	v_med3_f32 v27, v27, s45, v236
	v_pk_mul_f32 v[28:29], v[156:157], v[100:101] op_sel_hi:[1,0]
	v_cvt_pk_fp8_f32 v32, v26, v27
	v_pk_fma_f32 v[28:29], v[92:93], v[28:29], v[96:97]
	v_lshrrev_b32_e32 v30, 16, v30
	v_and_or_b32 v30, v31, s42, v30
	v_bfe_u32 v31, v28, 16, 1
	v_add3_u32 v31, v28, v31, s44
	v_bfe_u32 v26, v29, 16, 1
	v_med3_f32 v27, v28, s45, v236
	v_med3_f32 v28, v29, s45, v236
	v_lshrrev_b32_e32 v31, 16, v31
	v_cvt_pk_fp8_f32 v32, v27, v28 op_sel:[0,0,1]
	v_add3_u32 v26, v29, v26, s44
	v_and_or_b32 v31, v26, s42, v31
	v_pk_mul_f32 v[26:27], v[150:151], v[100:101] op_sel_hi:[1,0]
	global_store_dwordx2 v234, v[30:31], s[26:27] offset:512
	global_store_dword v237, v32, s[28:29] offset:256
	v_pk_fma_f32 v[26:27], v[82:83], v[26:27], v[86:87]
	v_mov_b32_e32 v32, 0
	v_bfe_u32 v30, v26, 16, 1
	v_bfe_u32 v31, v27, 16, 1
	v_add3_u32 v30, v26, v30, s44
	v_add3_u32 v31, v27, v31, s44
	v_med3_f32 v26, v26, s45, v236
	v_med3_f32 v27, v27, s45, v236
	v_pk_mul_f32 v[28:29], v[152:153], v[100:101] op_sel_hi:[1,0]
	v_cvt_pk_fp8_f32 v32, v26, v27
	v_pk_fma_f32 v[28:29], v[84:85], v[28:29], v[88:89]
	v_lshrrev_b32_e32 v30, 16, v30
	v_and_or_b32 v30, v31, s42, v30
	v_bfe_u32 v31, v28, 16, 1
	v_add3_u32 v31, v28, v31, s44
	v_bfe_u32 v26, v29, 16, 1
	v_med3_f32 v27, v28, s45, v236
	v_med3_f32 v28, v29, s45, v236
	v_lshrrev_b32_e32 v31, 16, v31
	v_cvt_pk_fp8_f32 v32, v27, v28 op_sel:[0,0,1]
	v_add3_u32 v26, v29, v26, s44
	v_and_or_b32 v31, v26, s42, v31
	v_pk_mul_f32 v[26:27], v[146:147], v[100:101] op_sel_hi:[1,0]
	global_store_dwordx2 v234, v[30:31], s[26:27] offset:1024
	global_store_dword v237, v32, s[28:29] offset:512
	v_pk_fma_f32 v[26:27], v[74:75], v[26:27], v[78:79]
	v_mov_b32_e32 v32, 0
	v_bfe_u32 v30, v26, 16, 1
	v_bfe_u32 v31, v27, 16, 1
	v_add3_u32 v30, v26, v30, s44
	v_add3_u32 v31, v27, v31, s44
	v_med3_f32 v26, v26, s45, v236
	v_med3_f32 v27, v27, s45, v236
	v_pk_mul_f32 v[28:29], v[148:149], v[100:101] op_sel_hi:[1,0]
	v_cvt_pk_fp8_f32 v32, v26, v27
	v_pk_fma_f32 v[28:29], v[76:77], v[28:29], v[80:81]
	v_lshrrev_b32_e32 v30, 16, v30
	v_and_or_b32 v30, v31, s42, v30
	v_bfe_u32 v31, v28, 16, 1
	v_add3_u32 v31, v28, v31, s44
	v_bfe_u32 v26, v29, 16, 1
	v_med3_f32 v27, v28, s45, v236
	v_med3_f32 v28, v29, s45, v236
	v_lshrrev_b32_e32 v31, 16, v31
	v_cvt_pk_fp8_f32 v32, v27, v28 op_sel:[0,0,1]
	v_add3_u32 v26, v29, v26, s44
	v_and_or_b32 v31, v26, s42, v31
	v_pk_mul_f32 v[26:27], v[142:143], v[100:101] op_sel_hi:[1,0]
	global_store_dwordx2 v234, v[30:31], s[26:27] offset:1536
	global_store_dword v237, v32, s[28:29] offset:768
	v_pk_fma_f32 v[26:27], v[34:35], v[26:27], v[70:71]
	v_pk_mul_f32 v[28:29], v[144:145], v[100:101] op_sel_hi:[1,0]
	v_bfe_u32 v30, v26, 16, 1
	v_bfe_u32 v31, v27, 16, 1
	v_add3_u32 v30, v26, v30, s44
	v_add3_u32 v31, v27, v31, s44
	v_med3_f32 v26, v26, s45, v236
	v_med3_f32 v27, v27, s45, v236
	v_mov_b32_e32 v32, 0
	v_pk_fma_f32 v[28:29], v[36:37], v[28:29], v[72:73]
	v_lshrrev_b32_e32 v30, 16, v30
	v_cvt_pk_fp8_f32 v32, v26, v27
	v_and_or_b32 v30, v31, s42, v30
	v_bfe_u32 v31, v28, 16, 1
	v_add3_u32 v31, v28, v31, s44
	v_bfe_u32 v26, v29, 16, 1
	v_lshrrev_b32_e32 v31, 16, v31
	v_med3_f32 v27, v28, s45, v236
	v_med3_f32 v28, v29, s45, v236
	v_add3_u32 v26, v29, v26, s44
	v_cvt_pk_fp8_f32 v32, v27, v28 op_sel:[0,0,1]
	v_and_or_b32 v31, v26, s42, v31
	v_pk_mul_f32 v[26:27], v[184:185], v[100:101] op_sel_hi:[1,0]
	v_pk_mul_f32 v[28:29], v[186:187], v[100:101] op_sel_hi:[1,0]
	v_pk_fma_f32 v[18:19], v[18:19], v[26:27], v[22:23]
	v_pk_fma_f32 v[20:21], v[20:21], v[28:29], v[24:25]
	v_bfe_u32 v22, v18, 16, 1
	v_bfe_u32 v23, v19, 16, 1
	v_add3_u32 v22, v18, v22, s44
	v_add3_u32 v23, v19, v23, s44
	v_med3_f32 v18, v18, s45, v236
	v_med3_f32 v19, v19, s45, v236
	v_mov_b32_e32 v24, 0
	v_lshrrev_b32_e32 v22, 16, v22
	v_cvt_pk_fp8_f32 v24, v18, v19
	v_and_or_b32 v22, v23, s42, v22
	v_bfe_u32 v23, v20, 16, 1
	v_add3_u32 v23, v20, v23, s44
	v_bfe_u32 v18, v21, 16, 1
	v_lshrrev_b32_e32 v23, 16, v23
	v_med3_f32 v19, v20, s45, v236
	v_med3_f32 v20, v21, s45, v236
	v_add3_u32 v18, v21, v18, s44
	v_cvt_pk_fp8_f32 v24, v19, v20 op_sel:[0,0,1]
	v_and_or_b32 v23, v18, s42, v23
	v_pk_mul_f32 v[18:19], v[138:139], v[100:101] op_sel_hi:[1,0]
	v_pk_mul_f32 v[20:21], v[140:141], v[100:101] op_sel_hi:[1,0]
	v_pk_fma_f32 v[10:11], v[10:11], v[18:19], v[14:15]
	v_pk_fma_f32 v[12:13], v[12:13], v[20:21], v[16:17]
	v_bfe_u32 v14, v10, 16, 1
	v_bfe_u32 v15, v11, 16, 1
	v_add3_u32 v14, v10, v14, s44
	v_add3_u32 v15, v11, v15, s44
	v_med3_f32 v10, v10, s45, v236
	v_med3_f32 v11, v11, s45, v236
	v_mov_b32_e32 v16, 0
	v_lshrrev_b32_e32 v14, 16, v14
	v_cvt_pk_fp8_f32 v16, v10, v11
	v_and_or_b32 v14, v15, s42, v14
	v_bfe_u32 v15, v12, 16, 1
	v_add3_u32 v15, v12, v15, s44
	v_bfe_u32 v10, v13, 16, 1
	v_lshrrev_b32_e32 v15, 16, v15
	v_med3_f32 v11, v12, s45, v236
	v_med3_f32 v12, v13, s45, v236
	v_add3_u32 v10, v13, v10, s44
	v_cvt_pk_fp8_f32 v16, v11, v12 op_sel:[0,0,1]
	v_and_or_b32 v15, v10, s42, v15
	v_pk_mul_f32 v[10:11], v[136:137], v[100:101] op_sel_hi:[1,0]
	v_pk_mul_f32 v[12:13], v[134:135], v[100:101] op_sel_hi:[1,0]
	v_pk_fma_f32 v[2:3], v[2:3], v[10:11], v[6:7]
	v_pk_fma_f32 v[4:5], v[4:5], v[12:13], v[8:9]
	v_bfe_u32 v6, v2, 16, 1
	v_bfe_u32 v7, v3, 16, 1
	v_add3_u32 v6, v2, v6, s44
	v_add3_u32 v7, v3, v7, s44
	v_med3_f32 v2, v2, s45, v236
	v_med3_f32 v3, v3, s45, v236
	v_mov_b32_e32 v8, 0
	v_cvt_pk_fp8_f32 v8, v2, v3
	v_lshrrev_b32_e32 v6, 16, v6
	v_and_or_b32 v6, v7, s42, v6
	v_bfe_u32 v7, v4, 16, 1
	v_add3_u32 v7, v4, v7, s44
	v_med3_f32 v3, v4, s45, v236
	v_med3_f32 v4, v5, s45, v236
	v_bfe_u32 v2, v5, 16, 1
	v_cvt_pk_fp8_f32 v8, v3, v4 op_sel:[0,0,1]
	v_mul_f32_e32 v4, 0x4b800000, v158
	v_lshrrev_b32_e32 v7, 16, v7
	v_add3_u32 v2, v5, v2, s44
	v_cndmask_b32_e32 v4, v158, v4, vcc
	v_and_or_b32 v7, v2, s42, v7
	v_add_co_u32_e64 v2, s[4:5], s41, v166
	v_rsq_f32_e32 v86, v4
	global_store_dwordx2 v234, v[30:31], s[26:27] offset:2048
	global_store_dword v237, v32, s[28:29] offset:1024
	global_store_dwordx2 v234, v[22:23], s[26:27] offset:2560
	global_store_dword v237, v24, s[28:29] offset:1280
	global_store_dwordx2 v234, v[14:15], s[26:27] offset:3072
	global_store_dword v237, v16, s[28:29] offset:1536
	global_store_dwordx2 v234, v[6:7], s[26:27] offset:3584
	global_store_dword v237, v8, s[28:29] offset:1792
	v_addc_co_u32_e64 v3, s[4:5], 0, v167, s[4:5]
	global_load_dwordx2 v[84:85], v234, s[24:25]
	global_load_dwordx4 v[30:33], v178, s[30:31] nt
	global_load_dwordx2 v[82:83], v234, s[24:25] offset:512
	global_load_dwordx4 v[26:29], v178, s[30:31] offset:1024 nt
	global_load_dwordx2 v[80:81], v234, s[24:25] offset:1024
	global_load_dwordx4 v[22:25], v178, s[30:31] offset:2048 nt
	global_load_dwordx2 v[78:79], v234, s[24:25] offset:1536
	global_load_dwordx4 v[18:21], v178, s[30:31] offset:3072 nt
	global_load_dwordx2 v[76:77], v234, s[24:25] offset:2048
	global_load_dwordx4 v[14:17], v[2:3], off nt
	global_load_dwordx2 v[74:75], v234, s[24:25] offset:2560
	global_load_dwordx4 v[10:13], v[2:3], off offset:1024 nt
	global_load_dwordx2 v[70:71], v234, s[24:25] offset:3072
	global_load_dwordx4 v[6:9], v[2:3], off offset:2048 nt
	global_load_dwordx2 v[72:73], v234, s[24:25] offset:3584
	s_nop 0
	global_load_dwordx4 v[2:5], v[2:3], off offset:3072 nt
	ds_read_b128 v[34:37], v233
	v_mul_f32_e32 v87, 0x45800000, v86
	v_cndmask_b32_e32 v86, v86, v87, vcc
	v_pk_mul_f32 v[88:89], v[86:87], v[130:131] op_sel_hi:[0,1]
	v_pk_mul_f32 v[90:91], v[86:87], v[132:133] op_sel_hi:[0,1]
	s_waitcnt lgkmcnt(0)
	v_pk_fma_f32 v[132:133], v[34:35], v[88:89], v[38:39]
	v_pk_fma_f32 v[130:131], v[36:37], v[90:91], v[40:41]
	v_and_b32_sdwa v39, v132, v235 dst_sel:DWORD dst_unused:UNUSED_PAD src0_sel:WORD_1 src1_sel:DWORD
	v_add3_u32 v40, v132, v39, s44
	v_and_b32_sdwa v39, v131, v235 dst_sel:DWORD dst_unused:UNUSED_PAD src0_sel:WORD_1 src1_sel:DWORD
	v_and_b32_sdwa v41, v133, v235 dst_sel:DWORD dst_unused:UNUSED_PAD src0_sel:WORD_1 src1_sel:DWORD
	v_and_b32_sdwa v38, v130, v235 dst_sel:DWORD dst_unused:UNUSED_PAD src0_sel:WORD_1 src1_sel:DWORD
	v_add3_u32 v39, v131, v39, s44
	v_add3_u32 v41, v133, v41, s44
	v_add3_u32 v38, v130, v38, s44
	v_and_b32_e32 v39, 0xffff0000, v39
	v_and_b32_e32 v41, 0xffff0000, v41
	v_or_b32_sdwa v39, v39, v38 dst_sel:DWORD dst_unused:UNUSED_PAD src0_sel:DWORD src1_sel:WORD_1
	v_or_b32_sdwa v38, v41, v40 dst_sel:DWORD dst_unused:UNUSED_PAD src0_sel:DWORD src1_sel:WORD_1
	global_store_dwordx2 v234, v[38:39], s[22:23] nt
	ds_read_b128 v[38:41], v233 offset:1024
	v_mov_b32_e32 v88, v126
	v_mov_b32_e32 v89, v128
	v_pk_mul_f32 v[88:89], v[86:87], v[88:89] op_sel_hi:[0,1]
	v_mov_b32_e32 v128, v127
	v_pk_mul_f32 v[90:91], v[86:87], v[128:129] op_sel_hi:[0,1]
	s_waitcnt lgkmcnt(0)
	v_pk_fma_f32 v[136:137], v[38:39], v[88:89], v[46:47]
	v_pk_fma_f32 v[134:135], v[40:41], v[90:91], v[48:49]
	v_and_b32_sdwa v47, v136, v235 dst_sel:DWORD dst_unused:UNUSED_PAD src0_sel:WORD_1 src1_sel:DWORD
	v_add3_u32 v48, v136, v47, s44
	v_and_b32_sdwa v47, v135, v235 dst_sel:DWORD dst_unused:UNUSED_PAD src0_sel:WORD_1 src1_sel:DWORD
	v_and_b32_sdwa v49, v137, v235 dst_sel:DWORD dst_unused:UNUSED_PAD src0_sel:WORD_1 src1_sel:DWORD
	v_and_b32_sdwa v46, v134, v235 dst_sel:DWORD dst_unused:UNUSED_PAD src0_sel:WORD_1 src1_sel:DWORD
	v_add3_u32 v47, v135, v47, s44
	v_add3_u32 v49, v137, v49, s44
	v_add3_u32 v46, v134, v46, s44
	v_and_b32_e32 v47, 0xffff0000, v47
	v_and_b32_e32 v49, 0xffff0000, v49
	v_or_b32_sdwa v47, v47, v46 dst_sel:DWORD dst_unused:UNUSED_PAD src0_sel:DWORD src1_sel:WORD_1
	v_or_b32_sdwa v46, v49, v48 dst_sel:DWORD dst_unused:UNUSED_PAD src0_sel:DWORD src1_sel:WORD_1
	v_mov_b32_e32 v48, v133
	v_mov_b32_e32 v49, v137
	global_store_dwordx2 v234, v[46:47], s[22:23] offset:512 nt
	v_mov_b32_e32 v46, v132
	v_mov_b32_e32 v47, v136
	v_pk_mul_f32 v[48:49], v[48:49], v[48:49]
	v_pk_mul_f32 v[92:93], v[86:87], v[124:125] op_sel_hi:[0,1]
	v_pk_fma_f32 v[88:89], v[46:47], v[46:47], v[48:49]
	v_mov_b32_e32 v46, v130
	v_mov_b32_e32 v47, v134
	v_pk_mul_f32 v[46:47], v[46:47], v[46:47]
	v_mov_b32_e32 v48, v131
	v_mov_b32_e32 v49, v135
	v_pk_fma_f32 v[90:91], v[48:49], v[48:49], v[46:47]
	ds_read_b128 v[46:49], v233 offset:2048
	v_pk_add_f32 v[88:89], v[88:89], v[90:91]
	v_pk_mul_f32 v[90:91], v[86:87], v[122:123] op_sel_hi:[0,1]
	v_pk_mul_f32 v[94:95], v[116:117], v[86:87] op_sel_hi:[1,0]
	v_mov_b32_e32 v96, v112
	s_waitcnt lgkmcnt(0)
	v_pk_fma_f32 v[140:141], v[46:47], v[90:91], v[54:55]
	v_pk_fma_f32 v[138:139], v[48:49], v[92:93], v[56:57]
	v_and_b32_sdwa v55, v140, v235 dst_sel:DWORD dst_unused:UNUSED_PAD src0_sel:WORD_1 src1_sel:DWORD
	v_add3_u32 v56, v140, v55, s44
	v_and_b32_sdwa v55, v139, v235 dst_sel:DWORD dst_unused:UNUSED_PAD src0_sel:WORD_1 src1_sel:DWORD
	v_and_b32_sdwa v57, v141, v235 dst_sel:DWORD dst_unused:UNUSED_PAD src0_sel:WORD_1 src1_sel:DWORD
	v_and_b32_sdwa v54, v138, v235 dst_sel:DWORD dst_unused:UNUSED_PAD src0_sel:WORD_1 src1_sel:DWORD
	v_add3_u32 v55, v139, v55, s44
	v_add3_u32 v57, v141, v57, s44
	v_add3_u32 v54, v138, v54, s44
	v_and_b32_e32 v55, 0xffff0000, v55
	v_and_b32_e32 v57, 0xffff0000, v57
	v_or_b32_sdwa v55, v55, v54 dst_sel:DWORD dst_unused:UNUSED_PAD src0_sel:DWORD src1_sel:WORD_1
	v_or_b32_sdwa v54, v57, v56 dst_sel:DWORD dst_unused:UNUSED_PAD src0_sel:DWORD src1_sel:WORD_1
	global_store_dwordx2 v234, v[54:55], s[22:23] offset:1024 nt
	v_pk_mul_f32 v[54:55], v[140:141], v[140:141]
	v_pk_mul_f32 v[56:57], v[138:139], v[138:139]
	v_pk_mul_f32 v[92:93], v[118:119], v[86:87] op_sel_hi:[1,0]
	v_pk_mov_b32 v[90:91], v[54:55], v[56:57] op_sel:[1,0]
	v_mov_b32_e32 v55, v57
	v_pk_add_f32 v[90:91], v[54:55], v[90:91]
	ds_read_b128 v[54:57], v233 offset:3072
	v_mov_b32_e32 v97, v114
	v_pk_mul_f32 v[96:97], v[86:87], v[96:97] op_sel_hi:[0,1]
	v_mov_b32_e32 v114, v113
	v_pk_mul_f32 v[112:113], v[86:87], v[114:115] op_sel_hi:[0,1]
	s_waitcnt lgkmcnt(0)
	v_pk_fma_f32 v[144:145], v[54:55], v[92:93], v[58:59]
	v_pk_fma_f32 v[142:143], v[56:57], v[94:95], v[60:61]
	v_and_b32_sdwa v59, v144, v235 dst_sel:DWORD dst_unused:UNUSED_PAD src0_sel:WORD_1 src1_sel:DWORD
	v_add3_u32 v60, v144, v59, s44
	v_and_b32_sdwa v59, v143, v235 dst_sel:DWORD dst_unused:UNUSED_PAD src0_sel:WORD_1 src1_sel:DWORD
	v_and_b32_sdwa v61, v145, v235 dst_sel:DWORD dst_unused:UNUSED_PAD src0_sel:WORD_1 src1_sel:DWORD
	v_and_b32_sdwa v58, v142, v235 dst_sel:DWORD dst_unused:UNUSED_PAD src0_sel:WORD_1 src1_sel:DWORD
	v_add3_u32 v59, v143, v59, s44
	v_add3_u32 v61, v145, v61, s44
	v_add3_u32 v58, v142, v58, s44
	v_and_b32_e32 v59, 0xffff0000, v59
	v_and_b32_e32 v61, 0xffff0000, v61
	v_or_b32_sdwa v59, v59, v58 dst_sel:DWORD dst_unused:UNUSED_PAD src0_sel:DWORD src1_sel:WORD_1
	v_or_b32_sdwa v58, v61, v60 dst_sel:DWORD dst_unused:UNUSED_PAD src0_sel:DWORD src1_sel:WORD_1
	global_store_dwordx2 v234, v[58:59], s[22:23] offset:1536 nt
	v_mul_f32_e32 v58, v144, v144
	v_pk_fma_f32 v[92:93], v[144:145], v[144:145], v[58:59] op_sel_hi:[1,1,0]
	v_mul_f32_e32 v58, v142, v142
	v_pk_fma_f32 v[94:95], v[142:143], v[142:143], v[58:59] op_sel_hi:[1,1,0]
	ds_read_b128 v[58:61], v233 offset:4096
	v_pk_add_f32 v[88:89], v[88:89], v[88:89] op_sel_hi:[0,1]
	v_pk_add_f32 v[90:91], v[90:91], v[90:91] op_sel_hi:[0,1]
	v_mov_b32_e32 v100, v103
	s_waitcnt vmcnt(19)
	v_and_b32_e32 v207, 0xffff0000, v84
	s_waitcnt lgkmcnt(0)
	v_pk_fma_f32 v[148:149], v[58:59], v[96:97], v[66:67]
	v_pk_fma_f32 v[146:147], v[60:61], v[112:113], v[68:69]
	v_and_b32_sdwa v67, v148, v235 dst_sel:DWORD dst_unused:UNUSED_PAD src0_sel:WORD_1 src1_sel:DWORD
	v_add3_u32 v68, v148, v67, s44
	v_and_b32_sdwa v67, v147, v235 dst_sel:DWORD dst_unused:UNUSED_PAD src0_sel:WORD_1 src1_sel:DWORD
	v_and_b32_sdwa v69, v149, v235 dst_sel:DWORD dst_unused:UNUSED_PAD src0_sel:WORD_1 src1_sel:DWORD
	v_and_b32_sdwa v66, v146, v235 dst_sel:DWORD dst_unused:UNUSED_PAD src0_sel:WORD_1 src1_sel:DWORD
	v_add3_u32 v67, v147, v67, s44
	v_add3_u32 v69, v149, v69, s44
	v_add3_u32 v66, v146, v66, s44
	v_and_b32_e32 v67, 0xffff0000, v67
	v_and_b32_e32 v69, 0xffff0000, v69
	v_or_b32_sdwa v67, v67, v66 dst_sel:DWORD dst_unused:UNUSED_PAD src0_sel:DWORD src1_sel:WORD_1
	v_or_b32_sdwa v66, v69, v68 dst_sel:DWORD dst_unused:UNUSED_PAD src0_sel:DWORD src1_sel:WORD_1
	v_mul_f32_e32 v92, v148, v148
	v_mul_f32_e32 v94, v149, v149
	v_mul_f32_e32 v88, v146, v146
	v_mul_f32_e32 v90, v147, v147
	global_store_dwordx2 v234, v[66:67], s[22:23] offset:2048 nt
	v_pk_add_f32 v[66:67], v[92:93], v[94:95]
	v_pk_add_f32 v[68:69], v[90:91], v[88:89]
	v_mov_b32_e32 v90, v108
	v_pk_add_f32 v[66:67], v[66:67], v[68:69]
	v_mov_b32_e32 v91, v110
	v_pk_add_f32 v[88:89], v[66:67], v[66:67] op_sel_hi:[0,1]
	ds_read_b128 v[66:69], v233 offset:5120
	v_pk_mul_f32 v[90:91], v[86:87], v[90:91] op_sel_hi:[0,1]
	v_mov_b32_e32 v110, v109
	v_pk_mul_f32 v[92:93], v[86:87], v[110:111] op_sel_hi:[0,1]
	v_pk_mul_f32 v[94:95], v[86:87], v[106:107] op_sel_hi:[0,1]
	s_waitcnt lgkmcnt(0)
	v_pk_fma_f32 v[152:153], v[66:67], v[90:91], v[62:63]
	v_pk_fma_f32 v[150:151], v[68:69], v[92:93], v[64:65]
	v_and_b32_sdwa v63, v152, v235 dst_sel:DWORD dst_unused:UNUSED_PAD src0_sel:WORD_1 src1_sel:DWORD
	v_add3_u32 v64, v152, v63, s44
	v_and_b32_sdwa v63, v151, v235 dst_sel:DWORD dst_unused:UNUSED_PAD src0_sel:WORD_1 src1_sel:DWORD
	v_and_b32_sdwa v65, v153, v235 dst_sel:DWORD dst_unused:UNUSED_PAD src0_sel:WORD_1 src1_sel:DWORD
	v_and_b32_sdwa v62, v150, v235 dst_sel:DWORD dst_unused:UNUSED_PAD src0_sel:WORD_1 src1_sel:DWORD
	v_add3_u32 v63, v151, v63, s44
	v_add3_u32 v65, v153, v65, s44
	v_add3_u32 v62, v150, v62, s44
	v_and_b32_e32 v63, 0xffff0000, v63
	v_and_b32_e32 v65, 0xffff0000, v65
	v_or_b32_sdwa v63, v63, v62 dst_sel:DWORD dst_unused:UNUSED_PAD src0_sel:DWORD src1_sel:WORD_1
	v_or_b32_sdwa v62, v65, v64 dst_sel:DWORD dst_unused:UNUSED_PAD src0_sel:DWORD src1_sel:WORD_1
	global_store_dwordx2 v234, v[62:63], s[22:23] offset:2560 nt
	v_pk_mul_f32 v[90:91], v[152:153], v[152:153]
	v_pk_mul_f32 v[62:63], v[150:151], v[150:151]
	v_pk_mul_f32 v[96:97], v[100:101], v[86:87] op_sel_hi:[1,0]
	v_pk_mov_b32 v[92:93], v[90:91], v[62:63] op_sel:[1,0]
	v_mov_b32_e32 v91, v63
	ds_read_b128 v[62:65], v233 offset:6144
	v_pk_add_f32 v[90:91], v[90:91], v[92:93]
	v_pk_mul_f32 v[92:93], v[86:87], v[104:105] op_sel_hi:[0,1]
	v_pk_mul_f32 v[86:87], v[98:99], v[86:87] op_sel_hi:[1,0]
	v_and_b32_e32 v209, 0xffff0000, v85
	s_waitcnt lgkmcnt(0)
	v_pk_fma_f32 v[156:157], v[92:93], v[62:63], v[50:51]
	v_pk_fma_f32 v[154:155], v[94:95], v[64:65], v[52:53]
	v_and_b32_sdwa v51, v156, v235 dst_sel:DWORD dst_unused:UNUSED_PAD src0_sel:WORD_1 src1_sel:DWORD
	v_add3_u32 v52, v156, v51, s44
	v_and_b32_sdwa v51, v155, v235 dst_sel:DWORD dst_unused:UNUSED_PAD src0_sel:WORD_1 src1_sel:DWORD
	v_and_b32_sdwa v53, v157, v235 dst_sel:DWORD dst_unused:UNUSED_PAD src0_sel:WORD_1 src1_sel:DWORD
	v_and_b32_sdwa v50, v154, v235 dst_sel:DWORD dst_unused:UNUSED_PAD src0_sel:WORD_1 src1_sel:DWORD
	v_add3_u32 v51, v155, v51, s44
	v_add3_u32 v53, v157, v53, s44
	v_add3_u32 v50, v154, v50, s44
	v_and_b32_e32 v51, 0xffff0000, v51
	v_and_b32_e32 v53, 0xffff0000, v53
	v_or_b32_sdwa v51, v51, v50 dst_sel:DWORD dst_unused:UNUSED_PAD src0_sel:DWORD src1_sel:WORD_1
	v_or_b32_sdwa v50, v53, v52 dst_sel:DWORD dst_unused:UNUSED_PAD src0_sel:DWORD src1_sel:WORD_1
	global_store_dwordx2 v234, v[50:51], s[22:23] offset:3072 nt
	v_mul_f32_e32 v50, v156, v156
	v_pk_fma_f32 v[92:93], v[156:157], v[156:157], v[50:51] op_sel_hi:[1,1,0]
	ds_read_b128 v[50:53], v233 offset:7168
	v_lshlrev_b32_e32 v206, 16, v84
	v_lshlrev_b32_e32 v208, 16, v85
	v_mul_f32_e32 v84, v209, v209
	s_waitcnt vmcnt(16)
	v_lshlrev_b32_e32 v195, 16, v78
	s_waitcnt lgkmcnt(0)
	v_pk_fma_f32 v[160:161], v[96:97], v[50:51], v[42:43]
	v_pk_fma_f32 v[158:159], v[86:87], v[52:53], v[44:45]
	v_and_b32_sdwa v43, v160, v235 dst_sel:DWORD dst_unused:UNUSED_PAD src0_sel:WORD_1 src1_sel:DWORD
	v_and_b32_e32 v193, 0xffff0000, v78
	v_mul_f32_e32 v78, v207, v207
	v_add3_u32 v44, v160, v43, s44
	v_and_b32_sdwa v43, v159, v235 dst_sel:DWORD dst_unused:UNUSED_PAD src0_sel:WORD_1 src1_sel:DWORD
	v_and_b32_sdwa v45, v161, v235 dst_sel:DWORD dst_unused:UNUSED_PAD src0_sel:WORD_1 src1_sel:DWORD
	v_pk_fma_f32 v[84:85], v[208:209], v[208:209], v[84:85] op_sel_hi:[1,1,0]
	v_and_b32_e32 v205, 0xffff0000, v83
	v_and_b32_e32 v204, 0xffff0000, v82
	v_lshlrev_b32_e32 v196, 16, v79
	v_and_b32_e32 v197, 0xffff0000, v79
	v_pk_fma_f32 v[78:79], v[206:207], v[206:207], v[78:79] op_sel_hi:[1,1,0]
	v_pk_add_f32 v[90:91], v[90:91], v[90:91] op_sel_hi:[0,1]
	v_mul_f32_e32 v88, v154, v154
	v_and_b32_sdwa v42, v158, v235 dst_sel:DWORD dst_unused:UNUSED_PAD src0_sel:WORD_1 src1_sel:DWORD
	v_add3_u32 v43, v159, v43, s44
	v_add3_u32 v45, v161, v45, s44
	v_lshlrev_b32_e32 v203, 16, v83
	v_lshlrev_b32_e32 v202, 16, v82
	v_pk_mul_f32 v[82:83], v[204:205], v[204:205]
	v_lshlrev_b32_e32 v198, 16, v80
	v_and_b32_e32 v199, 0xffff0000, v80
	v_lshlrev_b32_e32 v200, 16, v81
	v_and_b32_e32 v201, 0xffff0000, v81
	v_mov_b32_e32 v194, v78
	v_mov_b32_e32 v80, v84
	v_mov_b32_e32 v81, v195
	v_pk_fma_f32 v[94:95], v[154:155], v[154:155], v[88:89] op_sel_hi:[1,1,0]
	v_add3_u32 v42, v158, v42, s44
	v_and_b32_e32 v43, 0xffff0000, v43
	v_and_b32_e32 v45, 0xffff0000, v45
	v_mul_f32_e32 v88, v158, v158
	v_mul_f32_e32 v90, v159, v159
	v_pk_fma_f32 v[82:83], v[202:203], v[202:203], v[82:83]
	v_pk_add_f32 v[78:79], v[78:79], v[84:85]
	v_pk_mul_f32 v[80:81], v[194:195], v[80:81]
	v_or_b32_sdwa v43, v43, v42 dst_sel:DWORD dst_unused:UNUSED_PAD src0_sel:DWORD src1_sel:WORD_1
	v_or_b32_sdwa v42, v45, v44 dst_sel:DWORD dst_unused:UNUSED_PAD src0_sel:DWORD src1_sel:WORD_1
	v_pk_add_f32 v[44:45], v[90:91], v[88:89]
	v_mul_f32_e32 v88, v193, v193
	v_mov_b32_e32 v79, v81
	v_pk_add_f32 v[80:81], v[82:83], v[82:83] op_sel:[0,1] op_sel_hi:[1,0]
	v_mul_f32_e32 v82, v201, v201
	v_mov_b32_e32 v81, v88
	v_pk_add_f32 v[78:79], v[78:79], v[80:81]
	v_mul_f32_e32 v80, v199, v199
	v_mul_f32_e32 v89, v196, v196
	v_mul_f32_e32 v90, v197, v197
	v_pk_fma_f32 v[80:81], v[198:199], v[198:199], v[80:81] op_sel_hi:[1,1,0]
	v_pk_fma_f32 v[82:83], v[200:201], v[200:201], v[82:83] op_sel_hi:[1,1,0]
	v_mov_b32_e32 v81, v89
	v_mov_b32_e32 v83, v90
	s_waitcnt vmcnt(14)
	v_and_b32_e32 v189, 0xffff0000, v77
	v_and_b32_e32 v188, 0xffff0000, v76
	v_pk_add_f32 v[80:81], v[80:81], v[82:83]
	v_lshlrev_b32_e32 v191, 16, v77
	v_lshlrev_b32_e32 v190, 16, v76
	v_pk_mul_f32 v[76:77], v[188:189], v[188:189]
	v_pk_add_f32 v[78:79], v[78:79], v[80:81]
	v_pk_fma_f32 v[76:77], v[190:191], v[190:191], v[76:77]
	s_waitcnt vmcnt(12)
	v_and_b32_e32 v187, 0xffff0000, v75
	v_pk_add_f32 v[76:77], v[76:77], v[76:77] op_sel:[0,1] op_sel_hi:[1,0]
	v_and_b32_e32 v186, 0xffff0000, v74
	s_waitcnt vmcnt(10)
	v_lshlrev_b32_e32 v168, 16, v70
	v_and_b32_e32 v169, 0xffff0000, v70
	v_lshlrev_b32_e32 v182, 16, v71
	v_and_b32_e32 v183, 0xffff0000, v71
	s_waitcnt vmcnt(8)
	v_lshlrev_b32_e32 v167, 16, v72
	v_pk_add_f32 v[70:71], v[78:79], v[78:79] op_sel:[0,1] op_sel_hi:[1,0]
	v_lshlrev_b32_e32 v185, 16, v75
	v_lshlrev_b32_e32 v184, 16, v74
	v_pk_mul_f32 v[74:75], v[186:187], v[186:187]
	v_and_b32_e32 v165, 0xffff0000, v72
	v_lshlrev_b32_e32 v162, 16, v73
	v_and_b32_e32 v163, 0xffff0000, v73
	v_mov_b32_e32 v166, v70
	v_mov_b32_e32 v72, v76
	v_mov_b32_e32 v73, v167
	v_pk_fma_f32 v[74:75], v[184:185], v[184:185], v[74:75]
	v_pk_add_f32 v[70:71], v[70:71], v[76:77]
	v_pk_mul_f32 v[72:73], v[166:167], v[72:73]
	v_mul_f32_e32 v80, v165, v165
	v_mov_b32_e32 v71, v73
	v_pk_add_f32 v[72:73], v[74:75], v[74:75] op_sel:[0,1] op_sel_hi:[1,0]
	v_mul_f32_e32 v74, v183, v183
	v_mov_b32_e32 v73, v80
	v_pk_add_f32 v[70:71], v[70:71], v[72:73]
	v_mul_f32_e32 v72, v169, v169
	v_mul_f32_e32 v81, v162, v162
	v_mul_f32_e32 v82, v163, v163
	v_pk_fma_f32 v[72:73], v[168:169], v[168:169], v[72:73] op_sel_hi:[1,1,0]
	v_pk_fma_f32 v[74:75], v[182:183], v[182:183], v[74:75] op_sel_hi:[1,1,0]
	v_mul_f32_e32 v92, v160, v160
	v_mul_f32_e32 v94, v161, v161
	v_mov_b32_e32 v73, v81
	v_mov_b32_e32 v75, v82
	global_store_dwordx2 v234, v[42:43], s[22:23] offset:3584 nt
	v_pk_add_f32 v[42:43], v[92:93], v[94:95]
	v_pk_add_f32 v[72:73], v[72:73], v[74:75]
	v_pk_add_f32 v[86:87], v[42:43], v[44:45]
	v_pk_add_f32 v[70:71], v[70:71], v[72:73]
	v_mov_b32_e32 v73, v86
	v_mov_b32_e32 v72, v70
	v_mov_b32_e32 v86, v71
	v_pk_add_f32 v[70:71], v[72:73], v[86:87]
	ds_bpermute_b32 v73, v171, v71
	ds_bpermute_b32 v72, v171, v70
	s_lshl_b64 s[22:23], s[8:9], 11
	s_lshl_b64 s[24:25], s[8:9], 12
	s_add_u32 s28, s96, s24
	s_addc_u32 s29, s97, s25
	s_waitcnt lgkmcnt(0)
	v_pk_add_f32 v[74:75], v[70:71], v[72:73]
	ds_bpermute_b32 v77, v226, v75
	ds_bpermute_b32 v76, v226, v74
	s_lshl_b64 s[4:5], s[8:9], 13
	s_add_u32 s30, s6, s4
	s_addc_u32 s31, s7, s5
	ds_read_b128 v[42:45], v233 offset:8192
	s_waitcnt lgkmcnt(1)
	v_pk_add_f32 v[114:115], v[74:75], v[76:77]
	ds_bpermute_b32 v117, v228, v115
	ds_bpermute_b32 v116, v228, v114
	ds_read_b128 v[126:129], v233 offset:16384
	ds_read_b128 v[106:109], v233 offset:9216
	ds_read_b128 v[110:113], v233 offset:17408
	ds_read_b128 v[86:89], v233 offset:10240
	ds_read_b128 v[102:105], v233 offset:18432
	ds_read_b128 v[78:81], v233 offset:11264
	ds_read_b128 v[82:85], v233 offset:19456
	ds_read_b128 v[70:73], v233 offset:12288
	ds_read_b128 v[74:77], v233 offset:20480
	ds_read_b128 v[90:93], v233 offset:13312
	ds_read_b128 v[98:101], v233 offset:21504
	ds_read_b128 v[94:97], v233 offset:14336
	s_add_u32 s26, s35, s16
	s_waitcnt lgkmcnt(12)
	v_pk_add_f32 v[210:211], v[114:115], v[116:117]
	ds_bpermute_b32 v213, v229, v211
	ds_bpermute_b32 v212, v229, v210
	ds_read_b128 v[118:121], v233 offset:22528
	ds_read_b128 v[114:117], v233 offset:15360
	ds_read_b128 v[122:125], v233 offset:23552
	s_addc_u32 s27, s36, s17
	s_add_u32 s16, s11, s16
	s_addc_u32 s17, s13, s17
	s_waitcnt lgkmcnt(3)
	v_pk_add_f32 v[210:211], v[210:211], v[212:213]
	ds_bpermute_b32 v213, v230, v211
	ds_bpermute_b32 v212, v230, v210
	s_waitcnt lgkmcnt(0)
	v_pk_add_f32 v[212:213], v[210:211], v[212:213]
	ds_bpermute_b32 v215, v231, v213
	ds_bpermute_b32 v214, v231, v212
	v_lshl_add_u64 v[210:211], s[30:31], 0, v[178:179]
	s_waitcnt lgkmcnt(0)
	v_pk_add_f32 v[212:213], v[212:213], v[214:215]
	s_nop 0
	v_pk_fma_f32 v[214:215], v[212:213], s[10:11], v[180:181] op_sel_hi:[1,0,0]
	s_nop 0
	v_mul_f32_e32 v164, 0x4b800000, v215
	v_cmp_gt_f32_e64 s[4:5], s43, v215
	v_cmp_gt_f32_e32 vcc, s43, v214
	s_nop 0
	v_cndmask_b32_e64 v164, v215, v164, s[4:5]
	v_rsq_f32_e32 v164, v164
	s_nop 0
	v_mul_f32_e32 v166, 0x45800000, v164
	v_cndmask_b32_e64 v164, v164, v166, s[4:5]
	v_pk_mul_f32 v[132:133], v[132:133], v[164:165] op_sel_hi:[1,0]
	v_pk_mul_f32 v[130:131], v[130:131], v[164:165] op_sel_hi:[1,0]
	v_pk_fma_f32 v[132:133], v[42:43], v[132:133], v[126:127]
	v_pk_fma_f32 v[130:131], v[44:45], v[130:131], v[128:129]
	v_bfe_u32 v166, v132, 16, 1
	v_add3_u32 v166, v132, v166, s44
	v_bfe_u32 v192, v133, 16, 1
	v_lshrrev_b32_e32 v166, 16, v166
	v_add3_u32 v192, v133, v192, s44
	v_and_or_b32 v212, v192, s42, v166
	v_med3_f32 v132, v132, s45, v236
	v_med3_f32 v133, v133, s45, v236
	v_mov_b32_e32 v192, 0
	v_cvt_pk_fp8_f32 v192, v132, v133
	v_bfe_u32 v166, v130, 16, 1
	v_add3_u32 v166, v130, v166, s44
	v_bfe_u32 v132, v131, 16, 1
	v_med3_f32 v130, v130, s45, v236
	v_med3_f32 v133, v131, s45, v236
	v_lshrrev_b32_e32 v166, 16, v166
	v_cvt_pk_fp8_f32 v192, v130, v133 op_sel:[0,0,1]
	v_add3_u32 v130, v131, v132, s44
	v_and_or_b32 v213, v130, s42, v166
	v_pk_mul_f32 v[130:131], v[136:137], v[164:165] op_sel_hi:[1,0]
	v_pk_mul_f32 v[132:133], v[134:135], v[164:165] op_sel_hi:[1,0]
	v_pk_fma_f32 v[130:131], v[106:107], v[130:131], v[110:111]
	v_mov_b32_e32 v136, 0
	v_bfe_u32 v134, v130, 16, 1
	v_bfe_u32 v135, v131, 16, 1
	v_add3_u32 v134, v130, v134, s44
	v_add3_u32 v135, v131, v135, s44
	v_med3_f32 v130, v130, s45, v236
	v_med3_f32 v131, v131, s45, v236
	v_cvt_pk_fp8_f32 v136, v130, v131
	v_pk_fma_f32 v[132:133], v[108:109], v[132:133], v[112:113]
	v_lshrrev_b32_e32 v134, 16, v134
	v_and_or_b32 v134, v135, s42, v134
	v_bfe_u32 v135, v132, 16, 1
	v_add3_u32 v135, v132, v135, s44
	v_bfe_u32 v130, v133, 16, 1
	v_med3_f32 v131, v132, s45, v236
	v_med3_f32 v132, v133, s45, v236
	v_lshrrev_b32_e32 v135, 16, v135
	v_cvt_pk_fp8_f32 v136, v131, v132 op_sel:[0,0,1]
	v_add3_u32 v130, v133, v130, s44
	v_and_or_b32 v135, v130, s42, v135
	v_pk_mul_f32 v[130:131], v[140:141], v[164:165] op_sel_hi:[1,0]
	global_store_dwordx2 v234, v[212:213], s[20:21]
	global_store_dword v237, v192, s[18:19]
	v_pk_fma_f32 v[130:131], v[86:87], v[130:131], v[102:103]
	global_store_dwordx2 v234, v[134:135], s[20:21] offset:512
	global_store_dword v237, v136, s[18:19] offset:256
	v_bfe_u32 v134, v130, 16, 1
	v_bfe_u32 v135, v131, 16, 1
	v_add3_u32 v134, v130, v134, s44
	v_add3_u32 v135, v131, v135, s44
	v_med3_f32 v130, v130, s45, v236
	v_med3_f32 v131, v131, s45, v236
	v_mov_b32_e32 v136, 0
	v_pk_mul_f32 v[132:133], v[138:139], v[164:165] op_sel_hi:[1,0]
	v_cvt_pk_fp8_f32 v136, v130, v131
	v_pk_fma_f32 v[132:133], v[88:89], v[132:133], v[104:105]
	v_lshrrev_b32_e32 v134, 16, v134
	v_and_or_b32 v134, v135, s42, v134
	v_bfe_u32 v135, v132, 16, 1
	v_add3_u32 v135, v132, v135, s44
	v_bfe_u32 v130, v133, 16, 1
	v_med3_f32 v131, v132, s45, v236
	v_med3_f32 v132, v133, s45, v236
	v_lshrrev_b32_e32 v135, 16, v135
	v_cvt_pk_fp8_f32 v136, v131, v132 op_sel:[0,0,1]
	v_add3_u32 v130, v133, v130, s44
	v_and_or_b32 v135, v130, s42, v135
	v_pk_mul_f32 v[130:131], v[144:145], v[164:165] op_sel_hi:[1,0]
	global_store_dwordx2 v234, v[134:135], s[20:21] offset:1024
	global_store_dword v237, v136, s[18:19] offset:512
	v_pk_fma_f32 v[130:131], v[130:131], v[78:79], v[82:83]
	v_mov_b32_e32 v136, 0
	v_bfe_u32 v134, v130, 16, 1
	v_bfe_u32 v135, v131, 16, 1
	v_add3_u32 v134, v130, v134, s44
	v_add3_u32 v135, v131, v135, s44
	v_med3_f32 v130, v130, s45, v236
	v_med3_f32 v131, v131, s45, v236
	v_pk_mul_f32 v[132:133], v[142:143], v[164:165] op_sel_hi:[1,0]
	v_cvt_pk_fp8_f32 v136, v130, v131
	v_pk_fma_f32 v[132:133], v[132:133], v[80:81], v[84:85]
	v_lshrrev_b32_e32 v134, 16, v134
	v_and_or_b32 v134, v135, s42, v134
	v_bfe_u32 v135, v132, 16, 1
	v_add3_u32 v135, v132, v135, s44
	v_bfe_u32 v130, v133, 16, 1
	v_med3_f32 v131, v132, s45, v236
	v_med3_f32 v132, v133, s45, v236
	v_lshrrev_b32_e32 v135, 16, v135
	v_cvt_pk_fp8_f32 v136, v131, v132 op_sel:[0,0,1]
	v_add3_u32 v130, v133, v130, s44
	v_and_or_b32 v135, v130, s42, v135
	v_pk_mul_f32 v[130:131], v[148:149], v[164:165] op_sel_hi:[1,0]
	global_store_dwordx2 v234, v[134:135], s[20:21] offset:1536
	global_store_dword v237, v136, s[18:19] offset:768
	v_pk_fma_f32 v[130:131], v[130:131], v[70:71], v[74:75]
	v_mov_b32_e32 v136, 0
	v_bfe_u32 v134, v130, 16, 1
	v_bfe_u32 v135, v131, 16, 1
	v_add3_u32 v134, v130, v134, s44
	v_add3_u32 v135, v131, v135, s44
	v_med3_f32 v130, v130, s45, v236
	v_med3_f32 v131, v131, s45, v236
	v_pk_mul_f32 v[132:133], v[146:147], v[164:165] op_sel_hi:[1,0]
	v_cvt_pk_fp8_f32 v136, v130, v131
	v_pk_fma_f32 v[132:133], v[132:133], v[72:73], v[76:77]
	v_lshrrev_b32_e32 v134, 16, v134
	v_and_or_b32 v134, v135, s42, v134
	v_bfe_u32 v135, v132, 16, 1
	v_add3_u32 v135, v132, v135, s44
	v_bfe_u32 v130, v133, 16, 1
	v_med3_f32 v131, v132, s45, v236
	v_med3_f32 v132, v133, s45, v236
	v_lshrrev_b32_e32 v135, 16, v135
	v_cvt_pk_fp8_f32 v136, v131, v132 op_sel:[0,0,1]
	v_add3_u32 v130, v133, v130, s44
	v_and_or_b32 v135, v130, s42, v135
	v_pk_mul_f32 v[130:131], v[152:153], v[164:165] op_sel_hi:[1,0]
	global_store_dwordx2 v234, v[134:135], s[20:21] offset:2048
	global_store_dword v237, v136, s[18:19] offset:1024
	v_pk_fma_f32 v[130:131], v[130:131], v[90:91], v[98:99]
	v_mov_b32_e32 v136, 0
	v_bfe_u32 v134, v130, 16, 1
	v_bfe_u32 v135, v131, 16, 1
	v_add3_u32 v134, v130, v134, s44
	v_add3_u32 v135, v131, v135, s44
	v_med3_f32 v130, v130, s45, v236
	v_med3_f32 v131, v131, s45, v236
	v_pk_mul_f32 v[132:133], v[150:151], v[164:165] op_sel_hi:[1,0]
	v_cvt_pk_fp8_f32 v136, v130, v131
	v_pk_fma_f32 v[132:133], v[132:133], v[92:93], v[100:101]
	v_lshrrev_b32_e32 v134, 16, v134
	v_and_or_b32 v134, v135, s42, v134
	v_bfe_u32 v135, v132, 16, 1
	v_add3_u32 v135, v132, v135, s44
	v_bfe_u32 v130, v133, 16, 1
	v_med3_f32 v131, v132, s45, v236
	v_med3_f32 v132, v133, s45, v236
	v_lshrrev_b32_e32 v135, 16, v135
	v_cvt_pk_fp8_f32 v136, v131, v132 op_sel:[0,0,1]
	v_add3_u32 v130, v133, v130, s44
	v_and_or_b32 v135, v130, s42, v135
	v_pk_mul_f32 v[130:131], v[156:157], v[164:165] op_sel_hi:[1,0]
	global_store_dwordx2 v234, v[134:135], s[20:21] offset:2560
	global_store_dword v237, v136, s[18:19] offset:1280
	v_pk_fma_f32 v[130:131], v[130:131], v[94:95], v[118:119]
	v_mov_b32_e32 v136, 0
	v_bfe_u32 v134, v130, 16, 1
	v_bfe_u32 v135, v131, 16, 1
	v_add3_u32 v134, v130, v134, s44
	v_add3_u32 v135, v131, v135, s44
	v_med3_f32 v130, v130, s45, v236
	v_med3_f32 v131, v131, s45, v236
	v_pk_mul_f32 v[132:133], v[154:155], v[164:165] op_sel_hi:[1,0]
	v_cvt_pk_fp8_f32 v136, v130, v131
	v_pk_fma_f32 v[132:133], v[132:133], v[96:97], v[120:121]
	v_lshrrev_b32_e32 v134, 16, v134
	v_and_or_b32 v134, v135, s42, v134
	v_bfe_u32 v135, v132, 16, 1
	v_add3_u32 v135, v132, v135, s44
	v_bfe_u32 v130, v133, 16, 1
	v_med3_f32 v131, v132, s45, v236
	v_med3_f32 v132, v133, s45, v236
	v_lshrrev_b32_e32 v135, 16, v135
	v_cvt_pk_fp8_f32 v136, v131, v132 op_sel:[0,0,1]
	v_add3_u32 v130, v133, v130, s44
	v_and_or_b32 v135, v130, s42, v135
	v_pk_mul_f32 v[130:131], v[160:161], v[164:165] op_sel_hi:[1,0]
	global_store_dwordx2 v234, v[134:135], s[20:21] offset:3072
	global_store_dword v237, v136, s[18:19] offset:1536
	v_pk_fma_f32 v[130:131], v[130:131], v[114:115], v[122:123]
	v_mov_b32_e32 v136, 0
	v_bfe_u32 v134, v130, 16, 1
	v_bfe_u32 v135, v131, 16, 1
	v_add3_u32 v134, v130, v134, s44
	v_add3_u32 v135, v131, v135, s44
	v_med3_f32 v130, v130, s45, v236
	v_med3_f32 v131, v131, s45, v236
	v_pk_mul_f32 v[132:133], v[158:159], v[164:165] op_sel_hi:[1,0]
	v_cvt_pk_fp8_f32 v136, v130, v131
	v_pk_fma_f32 v[132:133], v[132:133], v[116:117], v[124:125]
	v_lshrrev_b32_e32 v134, 16, v134
	v_and_or_b32 v134, v135, s42, v134
	v_bfe_u32 v135, v132, 16, 1
	v_add3_u32 v135, v132, v135, s44
	v_med3_f32 v131, v132, s45, v236
	v_med3_f32 v132, v133, s45, v236
	v_bfe_u32 v130, v133, 16, 1
	v_cvt_pk_fp8_f32 v136, v131, v132 op_sel:[0,0,1]
	v_lshrrev_b32_e32 v135, 16, v135
	v_add3_u32 v130, v133, v130, s44
	v_and_or_b32 v135, v130, s42, v135
	global_store_dwordx2 v234, v[134:135], s[20:21] offset:3584
	global_store_dword v237, v136, s[18:19] offset:1792
	global_load_dwordx2 v[224:225], v234, s[28:29]
	global_load_dwordx4 v[158:161], v178, s[30:31] nt
	global_load_dwordx2 v[222:223], v234, s[28:29] offset:512
	global_load_dwordx4 v[154:157], v178, s[30:31] offset:1024 nt
	global_load_dwordx2 v[220:221], v234, s[28:29] offset:1024
	global_load_dwordx4 v[150:153], v178, s[30:31] offset:2048 nt
	global_load_dwordx2 v[218:219], v234, s[28:29] offset:1536
	global_load_dwordx4 v[146:149], v178, s[30:31] offset:3072 nt
	global_load_dwordx2 v[216:217], v234, s[28:29] offset:2048
	v_add_co_u32_e64 v130, s[4:5], s41, v210
	v_mul_f32_e32 v132, 0x4b800000, v214
	s_nop 0
	v_addc_co_u32_e64 v131, s[4:5], 0, v211, s[4:5]
	global_load_dwordx4 v[142:145], v[130:131], off nt
	global_load_dwordx2 v[212:213], v234, s[28:29] offset:2560
	global_load_dwordx4 v[138:141], v[130:131], off offset:1024 nt
	global_load_dwordx2 v[210:211], v234, s[28:29] offset:3072
	v_cndmask_b32_e32 v132, v214, v132, vcc
	v_rsq_f32_e32 v164, v132
	global_load_dwordx4 v[134:137], v[130:131], off offset:2048 nt
	global_load_dwordx2 v[214:215], v234, s[28:29] offset:3584
	s_nop 0
	global_load_dwordx4 v[130:133], v[130:131], off offset:3072 nt
	v_mov_b32_e32 v192, v195
	s_add_u32 s18, s33, s14
	v_mul_f32_e32 v166, 0x45800000, v164
	v_cndmask_b32_e32 v166, v164, v166, vcc
	v_pk_mul_f32 v[206:207], v[166:167], v[206:207] op_sel_hi:[0,1]
	v_pk_mul_f32 v[208:209], v[166:167], v[208:209] op_sel_hi:[0,1]
	v_pk_fma_f32 v[206:207], v[34:35], v[206:207], v[30:31]
	v_pk_fma_f32 v[208:209], v[36:37], v[208:209], v[32:33]
	v_and_b32_sdwa v31, v206, v235 dst_sel:DWORD dst_unused:UNUSED_PAD src0_sel:WORD_1 src1_sel:DWORD
	v_add3_u32 v32, v206, v31, s44
	v_and_b32_sdwa v31, v209, v235 dst_sel:DWORD dst_unused:UNUSED_PAD src0_sel:WORD_1 src1_sel:DWORD
	v_and_b32_sdwa v33, v207, v235 dst_sel:DWORD dst_unused:UNUSED_PAD src0_sel:WORD_1 src1_sel:DWORD
	v_and_b32_sdwa v30, v208, v235 dst_sel:DWORD dst_unused:UNUSED_PAD src0_sel:WORD_1 src1_sel:DWORD
	v_add3_u32 v31, v209, v31, s44
	v_add3_u32 v33, v207, v33, s44
	v_add3_u32 v30, v208, v30, s44
	v_and_b32_e32 v31, 0xffff0000, v31
	v_and_b32_e32 v33, 0xffff0000, v33
	v_or_b32_sdwa v31, v31, v30 dst_sel:DWORD dst_unused:UNUSED_PAD src0_sel:DWORD src1_sel:WORD_1
	v_or_b32_sdwa v30, v33, v32 dst_sel:DWORD dst_unused:UNUSED_PAD src0_sel:DWORD src1_sel:WORD_1
	global_store_dwordx2 v234, v[30:31], s[26:27] nt
	v_mov_b32_e32 v30, v203
	v_mov_b32_e32 v203, v204
	v_mov_b32_e32 v31, v205
	v_pk_mul_f32 v[32:33], v[166:167], v[202:203] op_sel_hi:[0,1]
	v_pk_mul_f32 v[30:31], v[166:167], v[30:31] op_sel_hi:[0,1]
	v_pk_fma_f32 v[202:203], v[38:39], v[32:33], v[26:27]
	v_pk_fma_f32 v[204:205], v[40:41], v[30:31], v[28:29]
	v_and_b32_sdwa v27, v202, v235 dst_sel:DWORD dst_unused:UNUSED_PAD src0_sel:WORD_1 src1_sel:DWORD
	v_add3_u32 v28, v202, v27, s44
	v_and_b32_sdwa v27, v205, v235 dst_sel:DWORD dst_unused:UNUSED_PAD src0_sel:WORD_1 src1_sel:DWORD
	v_and_b32_sdwa v29, v203, v235 dst_sel:DWORD dst_unused:UNUSED_PAD src0_sel:WORD_1 src1_sel:DWORD
	v_and_b32_sdwa v26, v204, v235 dst_sel:DWORD dst_unused:UNUSED_PAD src0_sel:WORD_1 src1_sel:DWORD
	v_add3_u32 v27, v205, v27, s44
	v_add3_u32 v29, v203, v29, s44
	v_add3_u32 v26, v204, v26, s44
	v_and_b32_e32 v27, 0xffff0000, v27
	v_and_b32_e32 v29, 0xffff0000, v29
	v_or_b32_sdwa v27, v27, v26 dst_sel:DWORD dst_unused:UNUSED_PAD src0_sel:DWORD src1_sel:WORD_1
	v_or_b32_sdwa v26, v29, v28 dst_sel:DWORD dst_unused:UNUSED_PAD src0_sel:DWORD src1_sel:WORD_1
	v_mov_b32_e32 v28, v207
	v_mov_b32_e32 v29, v203
	global_store_dwordx2 v234, v[26:27], s[26:27] offset:512 nt
	v_mov_b32_e32 v26, v206
	v_mov_b32_e32 v27, v202
	v_pk_mul_f32 v[28:29], v[28:29], v[28:29]
	v_mov_b32_e32 v30, v209
	v_pk_fma_f32 v[26:27], v[26:27], v[26:27], v[28:29]
	v_mov_b32_e32 v28, v208
	v_mov_b32_e32 v29, v204
	v_pk_mul_f32 v[28:29], v[28:29], v[28:29]
	v_mov_b32_e32 v31, v205
	v_pk_fma_f32 v[28:29], v[30:31], v[30:31], v[28:29]
	v_pk_mul_f32 v[30:31], v[166:167], v[198:199] op_sel_hi:[0,1]
	v_pk_add_f32 v[26:27], v[26:27], v[28:29]
	v_pk_mul_f32 v[28:29], v[166:167], v[200:201] op_sel_hi:[0,1]
	v_pk_fma_f32 v[198:199], v[46:47], v[30:31], v[22:23]
	v_pk_fma_f32 v[200:201], v[48:49], v[28:29], v[24:25]
	v_and_b32_sdwa v23, v198, v235 dst_sel:DWORD dst_unused:UNUSED_PAD src0_sel:WORD_1 src1_sel:DWORD
	v_add3_u32 v24, v198, v23, s44
	v_and_b32_sdwa v23, v201, v235 dst_sel:DWORD dst_unused:UNUSED_PAD src0_sel:WORD_1 src1_sel:DWORD
	v_and_b32_sdwa v25, v199, v235 dst_sel:DWORD dst_unused:UNUSED_PAD src0_sel:WORD_1 src1_sel:DWORD
	v_and_b32_sdwa v22, v200, v235 dst_sel:DWORD dst_unused:UNUSED_PAD src0_sel:WORD_1 src1_sel:DWORD
	v_add3_u32 v23, v201, v23, s44
	v_add3_u32 v25, v199, v25, s44
	v_add3_u32 v22, v200, v22, s44
	v_and_b32_e32 v23, 0xffff0000, v23
	v_and_b32_e32 v25, 0xffff0000, v25
	v_or_b32_sdwa v23, v23, v22 dst_sel:DWORD dst_unused:UNUSED_PAD src0_sel:DWORD src1_sel:WORD_1
	v_or_b32_sdwa v22, v25, v24 dst_sel:DWORD dst_unused:UNUSED_PAD src0_sel:DWORD src1_sel:WORD_1
	global_store_dwordx2 v234, v[22:23], s[26:27] offset:1024 nt
	v_pk_mul_f32 v[22:23], v[200:201], v[200:201]
	v_pk_mul_f32 v[24:25], v[198:199], v[198:199]
	v_pk_add_f32 v[26:27], v[26:27], v[26:27] op_sel_hi:[0,1]
	v_pk_mov_b32 v[28:29], v[24:25], v[22:23] op_sel:[1,0]
	v_mov_b32_e32 v25, v23
	v_pk_add_f32 v[22:23], v[24:25], v[28:29]
	v_pk_mul_f32 v[28:29], v[192:193], v[166:167] op_sel_hi:[1,0]
	v_pk_mul_f32 v[24:25], v[196:197], v[166:167] op_sel_hi:[1,0]
	v_pk_fma_f32 v[192:193], v[54:55], v[28:29], v[18:19]
	v_pk_fma_f32 v[196:197], v[56:57], v[24:25], v[20:21]
	v_and_b32_sdwa v19, v192, v235 dst_sel:DWORD dst_unused:UNUSED_PAD src0_sel:WORD_1 src1_sel:DWORD
	v_add3_u32 v20, v192, v19, s44
	v_and_b32_sdwa v19, v197, v235 dst_sel:DWORD dst_unused:UNUSED_PAD src0_sel:WORD_1 src1_sel:DWORD
	v_and_b32_sdwa v21, v193, v235 dst_sel:DWORD dst_unused:UNUSED_PAD src0_sel:WORD_1 src1_sel:DWORD
	v_and_b32_sdwa v18, v196, v235 dst_sel:DWORD dst_unused:UNUSED_PAD src0_sel:WORD_1 src1_sel:DWORD
	v_add3_u32 v19, v197, v19, s44
	v_add3_u32 v21, v193, v21, s44
	v_mov_b32_e32 v24, v190
	v_mov_b32_e32 v25, v188
	v_add3_u32 v18, v196, v18, s44
	v_and_b32_e32 v19, 0xffff0000, v19
	v_and_b32_e32 v21, 0xffff0000, v21
	v_pk_mul_f32 v[24:25], v[166:167], v[24:25] op_sel_hi:[0,1]
	v_mov_b32_e32 v188, v191
	v_or_b32_sdwa v19, v19, v18 dst_sel:DWORD dst_unused:UNUSED_PAD src0_sel:DWORD src1_sel:WORD_1
	v_or_b32_sdwa v18, v21, v20 dst_sel:DWORD dst_unused:UNUSED_PAD src0_sel:DWORD src1_sel:WORD_1
	v_pk_mul_f32 v[28:29], v[166:167], v[188:189] op_sel_hi:[0,1]
	v_pk_fma_f32 v[190:191], v[58:59], v[24:25], v[14:15]
	global_store_dwordx2 v234, v[18:19], s[26:27] offset:1536 nt
	v_mul_f32_e32 v18, v192, v192
	v_pk_fma_f32 v[188:189], v[60:61], v[28:29], v[16:17]
	v_and_b32_sdwa v15, v190, v235 dst_sel:DWORD dst_unused:UNUSED_PAD src0_sel:WORD_1 src1_sel:DWORD
	v_pk_fma_f32 v[18:19], v[192:193], v[192:193], v[18:19] op_sel_hi:[1,1,0]
	v_add3_u32 v16, v190, v15, s44
	v_and_b32_sdwa v15, v189, v235 dst_sel:DWORD dst_unused:UNUSED_PAD src0_sel:WORD_1 src1_sel:DWORD
	v_and_b32_sdwa v17, v191, v235 dst_sel:DWORD dst_unused:UNUSED_PAD src0_sel:WORD_1 src1_sel:DWORD
	v_mul_f32_e32 v18, v196, v196
	v_and_b32_sdwa v14, v188, v235 dst_sel:DWORD dst_unused:UNUSED_PAD src0_sel:WORD_1 src1_sel:DWORD
	v_add3_u32 v15, v189, v15, s44
	v_add3_u32 v17, v191, v17, s44
	v_pk_add_f32 v[22:23], v[22:23], v[22:23] op_sel_hi:[0,1]
	v_pk_fma_f32 v[20:21], v[196:197], v[196:197], v[18:19] op_sel_hi:[1,1,0]
	v_add3_u32 v14, v188, v14, s44
	v_and_b32_e32 v15, 0xffff0000, v15
	v_and_b32_e32 v17, 0xffff0000, v17
	v_or_b32_sdwa v15, v15, v14 dst_sel:DWORD dst_unused:UNUSED_PAD src0_sel:DWORD src1_sel:WORD_1
	v_or_b32_sdwa v14, v17, v16 dst_sel:DWORD dst_unused:UNUSED_PAD src0_sel:DWORD src1_sel:WORD_1
	v_mul_f32_e32 v18, v190, v190
	v_mul_f32_e32 v20, v191, v191
	v_mul_f32_e32 v26, v188, v188
	v_mul_f32_e32 v22, v189, v189
	global_store_dwordx2 v234, v[14:15], s[26:27] offset:2048 nt
	v_pk_add_f32 v[14:15], v[18:19], v[20:21]
	v_pk_add_f32 v[16:17], v[22:23], v[26:27]
	v_mov_b32_e32 v164, v167
	v_pk_add_f32 v[14:15], v[14:15], v[16:17]
	v_mov_b32_e32 v16, v185
	v_mov_b32_e32 v185, v186
	v_mov_b32_e32 v17, v187
	v_pk_mul_f32 v[18:19], v[166:167], v[184:185] op_sel_hi:[0,1]
	v_pk_mul_f32 v[16:17], v[166:167], v[16:17] op_sel_hi:[0,1]
	v_pk_fma_f32 v[184:185], v[66:67], v[18:19], v[10:11]
	v_pk_fma_f32 v[186:187], v[68:69], v[16:17], v[12:13]
	v_and_b32_sdwa v11, v184, v235 dst_sel:DWORD dst_unused:UNUSED_PAD src0_sel:WORD_1 src1_sel:DWORD
	v_add3_u32 v12, v184, v11, s44
	v_and_b32_sdwa v11, v187, v235 dst_sel:DWORD dst_unused:UNUSED_PAD src0_sel:WORD_1 src1_sel:DWORD
	v_and_b32_sdwa v13, v185, v235 dst_sel:DWORD dst_unused:UNUSED_PAD src0_sel:WORD_1 src1_sel:DWORD
	v_and_b32_sdwa v10, v186, v235 dst_sel:DWORD dst_unused:UNUSED_PAD src0_sel:WORD_1 src1_sel:DWORD
	v_add3_u32 v11, v187, v11, s44
	v_add3_u32 v13, v185, v13, s44
	v_add3_u32 v10, v186, v10, s44
	v_and_b32_e32 v11, 0xffff0000, v11
	v_and_b32_e32 v13, 0xffff0000, v13
	v_or_b32_sdwa v11, v11, v10 dst_sel:DWORD dst_unused:UNUSED_PAD src0_sel:DWORD src1_sel:WORD_1
	v_or_b32_sdwa v10, v13, v12 dst_sel:DWORD dst_unused:UNUSED_PAD src0_sel:DWORD src1_sel:WORD_1
	global_store_dwordx2 v234, v[10:11], s[26:27] offset:2560 nt
	v_pk_mul_f32 v[10:11], v[186:187], v[186:187]
	v_pk_mul_f32 v[12:13], v[184:185], v[184:185]
	v_pk_add_f32 v[14:15], v[14:15], v[14:15] op_sel_hi:[0,1]
	v_pk_mov_b32 v[16:17], v[12:13], v[10:11] op_sel:[1,0]
	v_mov_b32_e32 v13, v11
	v_pk_add_f32 v[10:11], v[12:13], v[16:17]
	v_pk_mul_f32 v[12:13], v[166:167], v[182:183] op_sel_hi:[0,1]
	v_pk_mul_f32 v[16:17], v[166:167], v[168:169] op_sel_hi:[0,1]
	v_pk_fma_f32 v[168:169], v[64:65], v[12:13], v[8:9]
	v_pk_fma_f32 v[30:31], v[62:63], v[16:17], v[6:7]
	v_and_b32_sdwa v6, v168, v235 dst_sel:DWORD dst_unused:UNUSED_PAD src0_sel:WORD_1 src1_sel:DWORD
	v_and_b32_sdwa v7, v30, v235 dst_sel:DWORD dst_unused:UNUSED_PAD src0_sel:WORD_1 src1_sel:DWORD
	v_add3_u32 v241, v168, v6, s44
	v_mul_f32_e32 v6, v30, v30
	v_add3_u32 v240, v30, v7, s44
	v_pk_fma_f32 v[6:7], v[30:31], v[30:31], v[6:7] op_sel_hi:[1,1,0]
	v_pk_mul_f32 v[12:13], v[164:165], v[166:167] op_sel_hi:[1,0]
	v_mul_f32_e32 v6, v168, v168
	v_pk_mul_f32 v[16:17], v[162:163], v[166:167] op_sel_hi:[1,0]
	v_pk_add_f32 v[10:11], v[10:11], v[10:11] op_sel_hi:[0,1]
	v_pk_fma_f32 v[8:9], v[168:169], v[168:169], v[6:7] op_sel_hi:[1,1,0]
	s_waitcnt vmcnt(46)
	v_pk_fma_f32 v[162:163], v[52:53], v[16:17], v[4:5]
	v_pk_fma_f32 v[164:165], v[50:51], v[12:13], v[2:3]
	v_mul_f32_e32 v14, v162, v162
	v_mul_f32_e32 v6, v164, v164
	v_mul_f32_e32 v8, v165, v165
	v_mul_f32_e32 v10, v163, v163
	v_pk_add_f32 v[2:3], v[6:7], v[8:9]
	v_pk_add_f32 v[4:5], v[10:11], v[14:15]
	s_waitcnt vmcnt(21)
	v_and_b32_e32 v183, 0xffff0000, v224
	v_and_b32_e32 v195, 0xffff0000, v225
	v_pk_add_f32 v[238:239], v[2:3], v[4:5]
	v_lshlrev_b32_e32 v182, 16, v224
	v_lshlrev_b32_e32 v194, 16, v225
	v_mul_f32_e32 v2, v195, v195
	s_waitcnt vmcnt(19)
	v_and_b32_e32 v167, 0xffff0000, v223
	v_and_b32_e32 v166, 0xffff0000, v222
	v_mul_f32_e32 v6, v183, v183
	v_pk_fma_f32 v[2:3], v[194:195], v[194:195], v[2:3] op_sel_hi:[1,1,0]
	v_lshlrev_b32_e32 v33, 16, v223
	v_lshlrev_b32_e32 v32, 16, v222
	v_pk_mul_f32 v[4:5], v[166:167], v[166:167]
	s_waitcnt vmcnt(15)
	v_lshlrev_b32_e32 v19, 16, v218
	v_pk_fma_f32 v[6:7], v[182:183], v[182:183], v[6:7] op_sel_hi:[1,1,0]
	v_pk_fma_f32 v[4:5], v[32:33], v[32:33], v[4:5]
	v_and_b32_e32 v17, 0xffff0000, v218
	v_mov_b32_e32 v18, v6
	v_mov_b32_e32 v8, v2
	v_mov_b32_e32 v9, v19
	v_mul_f32_e32 v10, v17, v17
	v_pk_add_f32 v[2:3], v[6:7], v[2:3]
	v_pk_mul_f32 v[6:7], v[18:19], v[8:9]
	v_pk_add_f32 v[4:5], v[4:5], v[4:5] op_sel:[0,1] op_sel_hi:[1,0]
	v_and_b32_e32 v27, 0xffff0000, v220
	v_and_b32_e32 v29, 0xffff0000, v221
	v_mov_b32_e32 v3, v7
	v_mov_b32_e32 v5, v10
	v_lshlrev_b32_e32 v26, 16, v220
	v_lshlrev_b32_e32 v28, 16, v221
	v_lshlrev_b32_e32 v20, 16, v219
	v_and_b32_e32 v21, 0xffff0000, v219
	v_pk_add_f32 v[2:3], v[2:3], v[4:5]
	v_mul_f32_e32 v4, v27, v27
	v_mul_f32_e32 v6, v29, v29
	v_mul_f32_e32 v11, v20, v20
	v_mul_f32_e32 v12, v21, v21
	v_pk_fma_f32 v[4:5], v[26:27], v[26:27], v[4:5] op_sel_hi:[1,1,0]
	v_pk_fma_f32 v[6:7], v[28:29], v[28:29], v[6:7] op_sel_hi:[1,1,0]
	v_mov_b32_e32 v5, v11
	v_mov_b32_e32 v7, v12
	v_pk_add_f32 v[4:5], v[4:5], v[6:7]
	s_waitcnt vmcnt(13)
	v_and_b32_e32 v25, 0xffff0000, v217
	v_and_b32_e32 v24, 0xffff0000, v216
	v_pk_add_f32 v[218:219], v[2:3], v[4:5]
	v_lshlrev_b32_e32 v23, 16, v217
	v_lshlrev_b32_e32 v22, 16, v216
	v_pk_mul_f32 v[2:3], v[24:25], v[24:25]
	s_waitcnt vmcnt(11)
	v_and_b32_e32 v15, 0xffff0000, v213
	v_pk_fma_f32 v[2:3], v[22:23], v[22:23], v[2:3]
	v_and_b32_e32 v14, 0xffff0000, v212
	v_pk_add_f32 v[216:217], v[2:3], v[2:3] op_sel:[0,1] op_sel_hi:[1,0]
	v_lshlrev_b32_e32 v13, 16, v213
	v_lshlrev_b32_e32 v12, 16, v212
	v_pk_mul_f32 v[2:3], v[14:15], v[14:15]
	s_waitcnt vmcnt(9)
	v_lshlrev_b32_e32 v8, 16, v210
	v_and_b32_e32 v9, 0xffff0000, v210
	v_lshlrev_b32_e32 v10, 16, v211
	v_and_b32_e32 v11, 0xffff0000, v211
	s_waitcnt vmcnt(7)
	v_lshlrev_b32_e32 v7, 16, v214
	v_pk_add_f32 v[210:211], v[218:219], v[218:219] op_sel:[0,1] op_sel_hi:[1,0]
	v_pk_fma_f32 v[212:213], v[12:13], v[12:13], v[2:3]
	v_and_b32_e32 v5, 0xffff0000, v214
	v_lshlrev_b32_e32 v2, 16, v215
	v_and_b32_e32 v3, 0xffff0000, v215
	v_mov_b32_e32 v6, v210
	v_mov_b32_e32 v214, v216
	v_mov_b32_e32 v215, v7
	v_mul_f32_e32 v4, v5, v5
	v_pk_add_f32 v[210:211], v[210:211], v[216:217]
	v_pk_mul_f32 v[214:215], v[6:7], v[214:215]
	v_pk_add_f32 v[212:213], v[212:213], v[212:213] op_sel:[0,1] op_sel_hi:[1,0]
	v_mov_b32_e32 v211, v215
	v_mov_b32_e32 v213, v4
	v_mul_f32_e32 v4, v9, v9
	v_pk_add_f32 v[210:211], v[210:211], v[212:213]
	v_pk_fma_f32 v[212:213], v[8:9], v[8:9], v[4:5] op_sel_hi:[1,1,0]
	v_mul_f32_e32 v4, v11, v11
	v_mul_f32_e32 v16, v2, v2
	v_mul_f32_e32 v18, v3, v3
	v_pk_fma_f32 v[214:215], v[10:11], v[10:11], v[4:5] op_sel_hi:[1,1,0]
	v_mov_b32_e32 v213, v16
	v_mov_b32_e32 v215, v18
	v_pk_add_f32 v[212:213], v[212:213], v[214:215]
	v_and_b32_sdwa v242, v169, v235 dst_sel:DWORD dst_unused:UNUSED_PAD src0_sel:WORD_1 src1_sel:DWORD
	v_pk_add_f32 v[210:211], v[210:211], v[212:213]
	v_mov_b32_e32 v213, v238
	v_mov_b32_e32 v212, v210
	v_mov_b32_e32 v238, v211
	v_pk_add_f32 v[210:211], v[212:213], v[238:239]
	ds_bpermute_b32 v213, v171, v211
	ds_bpermute_b32 v212, v171, v210
	v_and_b32_sdwa v243, v31, v235 dst_sel:DWORD dst_unused:UNUSED_PAD src0_sel:WORD_1 src1_sel:DWORD
	v_add3_u32 v4, v169, v242, s44
	v_add3_u32 v6, v31, v243, s44
	v_and_b32_e32 v4, 0xffff0000, v4
	s_waitcnt lgkmcnt(0)
	v_pk_add_f32 v[210:211], v[210:211], v[212:213]
	ds_bpermute_b32 v213, v226, v211
	ds_bpermute_b32 v212, v226, v210
	v_and_b32_sdwa v16, v163, v235 dst_sel:DWORD dst_unused:UNUSED_PAD src0_sel:WORD_1 src1_sel:DWORD
	v_and_b32_e32 v6, 0xffff0000, v6
	v_or_b32_sdwa v215, v4, v241 dst_sel:DWORD dst_unused:UNUSED_PAD src0_sel:DWORD src1_sel:WORD_1
	v_and_b32_sdwa v4, v162, v235 dst_sel:DWORD dst_unused:UNUSED_PAD src0_sel:WORD_1 src1_sel:DWORD
	s_waitcnt lgkmcnt(0)
	v_pk_add_f32 v[210:211], v[210:211], v[212:213]
	ds_bpermute_b32 v213, v228, v211
	ds_bpermute_b32 v212, v228, v210
	v_add3_u32 v16, v163, v16, s44
	v_or_b32_sdwa v214, v6, v240 dst_sel:DWORD dst_unused:UNUSED_PAD src0_sel:DWORD src1_sel:WORD_1
	v_add3_u32 v4, v162, v4, s44
	v_and_b32_e32 v16, 0xffff0000, v16
	s_waitcnt lgkmcnt(0)
	v_pk_add_f32 v[210:211], v[210:211], v[212:213]
	ds_bpermute_b32 v213, v229, v211
	ds_bpermute_b32 v212, v229, v210
	global_store_dwordx2 v234, v[214:215], s[26:27] offset:3072 nt
	v_or_b32_sdwa v215, v16, v4 dst_sel:DWORD dst_unused:UNUSED_PAD src0_sel:DWORD src1_sel:WORD_1
	v_and_b32_sdwa v18, v165, v235 dst_sel:DWORD dst_unused:UNUSED_PAD src0_sel:WORD_1 src1_sel:DWORD
	v_and_b32_sdwa v6, v164, v235 dst_sel:DWORD dst_unused:UNUSED_PAD src0_sel:WORD_1 src1_sel:DWORD
	s_waitcnt lgkmcnt(0)
	v_pk_add_f32 v[210:211], v[210:211], v[212:213]
	ds_bpermute_b32 v213, v230, v211
	ds_bpermute_b32 v212, v230, v210
	v_add3_u32 v18, v165, v18, s44
	v_add3_u32 v6, v164, v6, s44
	v_and_b32_e32 v18, 0xffff0000, v18
	v_or_b32_sdwa v214, v18, v6 dst_sel:DWORD dst_unused:UNUSED_PAD src0_sel:DWORD src1_sel:WORD_1
	s_waitcnt lgkmcnt(0)
	v_pk_add_f32 v[210:211], v[210:211], v[212:213]
	ds_bpermute_b32 v213, v231, v211
	ds_bpermute_b32 v212, v231, v210
	global_store_dwordx2 v234, v[214:215], s[26:27] offset:3584 nt
	s_addc_u32 s19, s34, s15
	s_add_u32 s14, s35, s24
	s_addc_u32 s15, s36, s25
	s_waitcnt lgkmcnt(0)
	v_pk_add_f32 v[210:211], v[210:211], v[212:213]
	s_nop 0
	v_pk_fma_f32 v[180:181], v[210:211], s[10:11], v[180:181] op_sel_hi:[1,0,0]
	s_nop 0
	v_mul_f32_e32 v4, 0x4b800000, v181
	v_cmp_gt_f32_e64 s[4:5], s43, v181
	v_cmp_gt_f32_e32 vcc, s43, v180
	s_nop 0
	v_cndmask_b32_e64 v4, v181, v4, s[4:5]
	v_rsq_f32_e32 v4, v4
	v_mov_b32_e32 v181, 0
	v_mul_f32_e32 v6, 0x45800000, v4
	v_cndmask_b32_e64 v4, v4, v6, s[4:5]
	v_pk_mul_f32 v[206:207], v[206:207], v[4:5] op_sel_hi:[1,0]
	v_pk_mul_f32 v[208:209], v[208:209], v[4:5] op_sel_hi:[1,0]
	v_pk_fma_f32 v[206:207], v[42:43], v[206:207], v[126:127]
	v_pk_fma_f32 v[208:209], v[44:45], v[208:209], v[128:129]
	v_bfe_u32 v6, v206, 16, 1
	v_add3_u32 v6, v206, v6, s44
	v_bfe_u32 v16, v207, 16, 1
	v_lshrrev_b32_e32 v6, 16, v6
	v_add3_u32 v16, v207, v16, s44
	v_and_or_b32 v210, v16, s42, v6
	v_med3_f32 v16, v206, s45, v236
	v_med3_f32 v18, v207, s45, v236
	v_cvt_pk_fp8_f32 v181, v16, v18
	v_bfe_u32 v6, v208, 16, 1
	v_add3_u32 v6, v208, v6, s44
	v_bfe_u32 v16, v209, 16, 1
	v_pk_mul_f32 v[202:203], v[202:203], v[4:5] op_sel_hi:[1,0]
	v_lshrrev_b32_e32 v6, 16, v6
	v_med3_f32 v18, v208, s45, v236
	v_med3_f32 v206, v209, s45, v236
	v_add3_u32 v16, v209, v16, s44
	v_pk_fma_f32 v[202:203], v[106:107], v[202:203], v[110:111]
	v_cvt_pk_fp8_f32 v181, v18, v206 op_sel:[0,0,1]
	v_and_or_b32 v211, v16, s42, v6
	v_bfe_u32 v6, v202, 16, 1
	v_add3_u32 v6, v202, v6, s44
	v_bfe_u32 v16, v203, 16, 1
	v_lshrrev_b32_e32 v6, 16, v6
	v_add3_u32 v16, v203, v16, s44
	global_store_dwordx2 v234, v[210:211], s[16:17]
	global_store_dword v237, v181, s[18:19]
	v_pk_mul_f32 v[204:205], v[204:205], v[4:5] op_sel_hi:[1,0]
	v_and_or_b32 v206, v16, s42, v6
	v_med3_f32 v16, v202, s45, v236
	v_med3_f32 v18, v203, s45, v236
	v_mov_b32_e32 v181, 0
	v_pk_fma_f32 v[204:205], v[108:109], v[204:205], v[112:113]
	v_cvt_pk_fp8_f32 v181, v16, v18
	v_bfe_u32 v6, v204, 16, 1
	v_add3_u32 v6, v204, v6, s44
	v_bfe_u32 v16, v205, 16, 1
	v_pk_mul_f32 v[198:199], v[198:199], v[4:5] op_sel_hi:[1,0]
	v_lshrrev_b32_e32 v6, 16, v6
	v_med3_f32 v18, v204, s45, v236
	v_med3_f32 v202, v205, s45, v236
	v_add3_u32 v16, v205, v16, s44
	v_pk_fma_f32 v[198:199], v[86:87], v[198:199], v[102:103]
	v_cvt_pk_fp8_f32 v181, v18, v202 op_sel:[0,0,1]
	v_and_or_b32 v207, v16, s42, v6
	v_bfe_u32 v6, v198, 16, 1
	v_add3_u32 v6, v198, v6, s44
	v_bfe_u32 v16, v199, 16, 1
	v_lshrrev_b32_e32 v6, 16, v6
	v_add3_u32 v16, v199, v16, s44
	global_store_dwordx2 v234, v[206:207], s[16:17] offset:512
	global_store_dword v237, v181, s[18:19] offset:256
	v_pk_mul_f32 v[200:201], v[200:201], v[4:5] op_sel_hi:[1,0]
	v_and_or_b32 v202, v16, s42, v6
	v_med3_f32 v16, v198, s45, v236
	v_med3_f32 v18, v199, s45, v236
	v_mov_b32_e32 v181, 0
	v_pk_fma_f32 v[200:201], v[88:89], v[200:201], v[104:105]
	v_cvt_pk_fp8_f32 v181, v16, v18
	v_bfe_u32 v6, v200, 16, 1
	v_add3_u32 v6, v200, v6, s44
	v_bfe_u32 v16, v201, 16, 1
	v_pk_mul_f32 v[192:193], v[192:193], v[4:5] op_sel_hi:[1,0]
	v_lshrrev_b32_e32 v6, 16, v6
	v_med3_f32 v18, v200, s45, v236
	v_med3_f32 v198, v201, s45, v236
	v_add3_u32 v16, v201, v16, s44
	v_pk_fma_f32 v[192:193], v[78:79], v[192:193], v[82:83]
	v_cvt_pk_fp8_f32 v181, v18, v198 op_sel:[0,0,1]
	v_and_or_b32 v203, v16, s42, v6
	v_bfe_u32 v6, v192, 16, 1
	v_add3_u32 v6, v192, v6, s44
	v_bfe_u32 v16, v193, 16, 1
	v_lshrrev_b32_e32 v6, 16, v6
	v_add3_u32 v16, v193, v16, s44
	global_store_dwordx2 v234, v[202:203], s[16:17] offset:1024
	global_store_dword v237, v181, s[18:19] offset:512
	v_pk_mul_f32 v[196:197], v[196:197], v[4:5] op_sel_hi:[1,0]
	v_and_or_b32 v198, v16, s42, v6
	v_med3_f32 v16, v192, s45, v236
	v_med3_f32 v18, v193, s45, v236
	v_mov_b32_e32 v181, 0
	v_pk_fma_f32 v[196:197], v[80:81], v[196:197], v[84:85]
	v_cvt_pk_fp8_f32 v181, v16, v18
	v_bfe_u32 v6, v196, 16, 1
	v_add3_u32 v6, v196, v6, s44
	v_bfe_u32 v16, v197, 16, 1
	v_pk_mul_f32 v[190:191], v[190:191], v[4:5] op_sel_hi:[1,0]
	v_lshrrev_b32_e32 v6, 16, v6
	v_med3_f32 v18, v196, s45, v236
	v_med3_f32 v192, v197, s45, v236
	v_add3_u32 v16, v197, v16, s44
	v_pk_fma_f32 v[190:191], v[70:71], v[190:191], v[74:75]
	v_cvt_pk_fp8_f32 v181, v18, v192 op_sel:[0,0,1]
	v_and_or_b32 v199, v16, s42, v6
	v_bfe_u32 v6, v190, 16, 1
	v_add3_u32 v6, v190, v6, s44
	v_bfe_u32 v16, v191, 16, 1
	v_lshrrev_b32_e32 v6, 16, v6
	v_add3_u32 v16, v191, v16, s44
	global_store_dwordx2 v234, v[198:199], s[16:17] offset:1536
	global_store_dword v237, v181, s[18:19] offset:768
	v_pk_mul_f32 v[188:189], v[188:189], v[4:5] op_sel_hi:[1,0]
	v_and_or_b32 v192, v16, s42, v6
	v_med3_f32 v16, v190, s45, v236
	v_med3_f32 v18, v191, s45, v236
	v_mov_b32_e32 v181, 0
	v_pk_fma_f32 v[188:189], v[72:73], v[188:189], v[76:77]
	v_cvt_pk_fp8_f32 v181, v16, v18
	v_bfe_u32 v6, v188, 16, 1
	v_add3_u32 v6, v188, v6, s44
	v_bfe_u32 v16, v189, 16, 1
	v_pk_mul_f32 v[184:185], v[184:185], v[4:5] op_sel_hi:[1,0]
	v_lshrrev_b32_e32 v6, 16, v6
	v_med3_f32 v18, v188, s45, v236
	v_med3_f32 v188, v189, s45, v236
	v_add3_u32 v16, v189, v16, s44
	v_pk_fma_f32 v[184:185], v[90:91], v[184:185], v[98:99]
	v_cvt_pk_fp8_f32 v181, v18, v188 op_sel:[0,0,1]
	v_and_or_b32 v193, v16, s42, v6
	v_bfe_u32 v6, v184, 16, 1
	v_pk_mul_f32 v[186:187], v[186:187], v[4:5] op_sel_hi:[1,0]
	v_add3_u32 v6, v184, v6, s44
	v_bfe_u32 v16, v185, 16, 1
	v_pk_fma_f32 v[186:187], v[92:93], v[186:187], v[100:101]
	v_lshrrev_b32_e32 v6, 16, v6
	v_add3_u32 v16, v185, v16, s44
	global_store_dwordx2 v234, v[192:193], s[16:17] offset:2048
	global_store_dword v237, v181, s[18:19] offset:1024
	v_and_or_b32 v188, v16, s42, v6
	v_bfe_u32 v6, v186, 16, 1
	v_med3_f32 v16, v184, s45, v236
	v_med3_f32 v18, v185, s45, v236
	v_mov_b32_e32 v181, 0
	v_add3_u32 v6, v186, v6, s44
	v_cvt_pk_fp8_f32 v181, v16, v18
	v_bfe_u32 v16, v187, 16, 1
	v_pk_mul_f32 v[30:31], v[30:31], v[4:5] op_sel_hi:[1,0]
	v_lshrrev_b32_e32 v6, 16, v6
	v_add3_u32 v16, v187, v16, s44
	v_pk_fma_f32 v[30:31], v[94:95], v[30:31], v[118:119]
	v_and_or_b32 v189, v16, s42, v6
	v_bfe_u32 v6, v30, 16, 1
	v_add3_u32 v6, v30, v6, s44
	v_bfe_u32 v16, v31, 16, 1
	v_med3_f32 v18, v186, s45, v236
	v_med3_f32 v184, v187, s45, v236
	v_lshrrev_b32_e32 v6, 16, v6
	v_add3_u32 v16, v31, v16, s44
	v_cvt_pk_fp8_f32 v181, v18, v184 op_sel:[0,0,1]
	v_and_or_b32 v184, v16, s42, v6
	v_med3_f32 v16, v30, s45, v236
	v_med3_f32 v18, v31, s45, v236
	v_mov_b32_e32 v30, 0
	v_cvt_pk_fp8_f32 v30, v16, v18
	v_pk_mul_f32 v[168:169], v[168:169], v[4:5] op_sel_hi:[1,0]
	global_store_dwordx2 v234, v[188:189], s[16:17] offset:2560
	global_store_dword v237, v181, s[18:19] offset:1280
	v_pk_fma_f32 v[168:169], v[96:97], v[168:169], v[120:121]
	v_pk_mul_f32 v[162:163], v[162:163], v[4:5] op_sel_hi:[1,0]
	v_bfe_u32 v6, v168, 16, 1
	v_med3_f32 v18, v168, s45, v236
	v_med3_f32 v31, v169, s45, v236
	v_add3_u32 v6, v168, v6, s44
	v_bfe_u32 v16, v169, 16, 1
	v_cvt_pk_fp8_f32 v30, v18, v31 op_sel:[0,0,1]
	v_lshrrev_b32_e32 v6, 16, v6
	v_add3_u32 v16, v169, v16, s44
	v_and_or_b32 v185, v16, s42, v6
	global_store_dwordx2 v234, v[184:185], s[16:17] offset:3072
	global_store_dword v237, v30, s[18:19] offset:1536
	v_pk_mul_f32 v[30:31], v[164:165], v[4:5] op_sel_hi:[1,0]
	v_pk_fma_f32 v[162:163], v[116:117], v[162:163], v[124:125]
	v_pk_fma_f32 v[30:31], v[114:115], v[30:31], v[122:123]
	s_nop 0
	v_bfe_u32 v4, v30, 16, 1
	v_add3_u32 v4, v30, v4, s44
	v_med3_f32 v16, v30, s45, v236
	v_med3_f32 v18, v31, s45, v236
	v_mov_b32_e32 v30, 0
	v_cvt_pk_fp8_f32 v30, v16, v18
	v_med3_f32 v16, v162, s45, v236
	v_med3_f32 v18, v163, s45, v236
	v_bfe_u32 v6, v31, 16, 1
	v_cvt_pk_fp8_f32 v30, v16, v18 op_sel:[0,0,1]
	v_mul_f32_e32 v16, 0x4b800000, v180
	v_cndmask_b32_e32 v16, v180, v16, vcc
	v_lshrrev_b32_e32 v4, 16, v4
	v_add3_u32 v6, v31, v6, s44
	v_rsq_f32_e32 v16, v16
	v_and_or_b32 v164, v6, s42, v4
	v_bfe_u32 v4, v162, 16, 1
	v_add3_u32 v4, v162, v4, s44
	v_bfe_u32 v6, v163, 16, 1
	v_lshrrev_b32_e32 v4, 16, v4
	v_add3_u32 v6, v163, v6, s44
	v_and_or_b32 v165, v6, s42, v4
	v_mul_f32_e32 v4, 0x45800000, v16
	v_cndmask_b32_e32 v6, v16, v4, vcc
	global_store_dwordx2 v234, v[164:165], s[16:17] offset:3584
	global_store_dword v237, v30, s[18:19] offset:1792
	v_pk_mul_f32 v[30:31], v[6:7], v[194:195] op_sel_hi:[0,1]
	v_pk_mul_f32 v[162:163], v[6:7], v[182:183] op_sel_hi:[0,1]
	v_pk_fma_f32 v[158:159], v[34:35], v[162:163], v[158:159]
	v_pk_fma_f32 v[36:37], v[36:37], v[30:31], v[160:161]
	v_and_b32_sdwa v30, v159, v235 dst_sel:DWORD dst_unused:UNUSED_PAD src0_sel:WORD_1 src1_sel:DWORD
	v_and_b32_sdwa v18, v37, v235 dst_sel:DWORD dst_unused:UNUSED_PAD src0_sel:WORD_1 src1_sel:DWORD
	v_and_b32_sdwa v4, v36, v235 dst_sel:DWORD dst_unused:UNUSED_PAD src0_sel:WORD_1 src1_sel:DWORD
	v_and_b32_sdwa v16, v158, v235 dst_sel:DWORD dst_unused:UNUSED_PAD src0_sel:WORD_1 src1_sel:DWORD
	v_add3_u32 v18, v37, v18, s44
	v_add3_u32 v30, v159, v30, s44
	v_add3_u32 v16, v158, v16, s44
	v_add3_u32 v4, v36, v4, s44
	v_and_b32_e32 v18, 0xffff0000, v18
	v_and_b32_e32 v30, 0xffff0000, v30
	v_or_b32_sdwa v31, v18, v4 dst_sel:DWORD dst_unused:UNUSED_PAD src0_sel:DWORD src1_sel:WORD_1
	v_or_b32_sdwa v30, v30, v16 dst_sel:DWORD dst_unused:UNUSED_PAD src0_sel:DWORD src1_sel:WORD_1
	global_store_dwordx2 v234, v[30:31], s[14:15] nt
	v_mov_b32_e32 v30, v33
	v_mov_b32_e32 v31, v167
	v_mov_b32_e32 v33, v166
	v_pk_mul_f32 v[30:31], v[6:7], v[30:31] op_sel_hi:[0,1]
	v_pk_mul_f32 v[32:33], v[6:7], v[32:33] op_sel_hi:[0,1]
	v_pk_fma_f32 v[32:33], v[38:39], v[32:33], v[154:155]
	v_pk_fma_f32 v[34:35], v[40:41], v[30:31], v[156:157]
	v_and_b32_sdwa v30, v33, v235 dst_sel:DWORD dst_unused:UNUSED_PAD src0_sel:WORD_1 src1_sel:DWORD
	v_and_b32_sdwa v18, v35, v235 dst_sel:DWORD dst_unused:UNUSED_PAD src0_sel:WORD_1 src1_sel:DWORD
	v_and_b32_sdwa v4, v34, v235 dst_sel:DWORD dst_unused:UNUSED_PAD src0_sel:WORD_1 src1_sel:DWORD
	v_and_b32_sdwa v16, v32, v235 dst_sel:DWORD dst_unused:UNUSED_PAD src0_sel:WORD_1 src1_sel:DWORD
	v_add3_u32 v18, v35, v18, s44
	v_add3_u32 v30, v33, v30, s44
	v_add3_u32 v16, v32, v16, s44
	v_add3_u32 v4, v34, v4, s44
	v_and_b32_e32 v18, 0xffff0000, v18
	v_and_b32_e32 v30, 0xffff0000, v30
	v_or_b32_sdwa v31, v18, v4 dst_sel:DWORD dst_unused:UNUSED_PAD src0_sel:DWORD src1_sel:WORD_1
	v_or_b32_sdwa v30, v30, v16 dst_sel:DWORD dst_unused:UNUSED_PAD src0_sel:DWORD src1_sel:WORD_1
	v_mov_b32_e32 v38, v159
	v_mov_b32_e32 v39, v33
	global_store_dwordx2 v234, v[30:31], s[14:15] offset:512 nt
	v_mov_b32_e32 v30, v158
	v_mov_b32_e32 v31, v32
	v_pk_mul_f32 v[38:39], v[38:39], v[38:39]
	v_mov_b32_e32 v40, v37
	v_pk_fma_f32 v[30:31], v[30:31], v[30:31], v[38:39]
	v_mov_b32_e32 v38, v36
	v_mov_b32_e32 v39, v34
	v_pk_mul_f32 v[38:39], v[38:39], v[38:39]
	v_mov_b32_e32 v41, v35
	v_pk_fma_f32 v[38:39], v[40:41], v[40:41], v[38:39]
	v_pk_mul_f32 v[26:27], v[6:7], v[26:27] op_sel_hi:[0,1]
	v_pk_add_f32 v[30:31], v[30:31], v[38:39]
	v_pk_mul_f32 v[8:9], v[6:7], v[8:9] op_sel_hi:[0,1]
	v_pk_add_f32 v[38:39], v[30:31], v[30:31] op_sel_hi:[0,1]
	v_pk_mul_f32 v[30:31], v[6:7], v[28:29] op_sel_hi:[0,1]
	v_pk_fma_f32 v[28:29], v[46:47], v[26:27], v[150:151]
	v_pk_fma_f32 v[30:31], v[48:49], v[30:31], v[152:153]
	v_and_b32_sdwa v26, v29, v235 dst_sel:DWORD dst_unused:UNUSED_PAD src0_sel:WORD_1 src1_sel:DWORD
	v_and_b32_sdwa v18, v31, v235 dst_sel:DWORD dst_unused:UNUSED_PAD src0_sel:WORD_1 src1_sel:DWORD
	v_and_b32_sdwa v4, v30, v235 dst_sel:DWORD dst_unused:UNUSED_PAD src0_sel:WORD_1 src1_sel:DWORD
	v_and_b32_sdwa v16, v28, v235 dst_sel:DWORD dst_unused:UNUSED_PAD src0_sel:WORD_1 src1_sel:DWORD
	v_add3_u32 v18, v31, v18, s44
	v_add3_u32 v26, v29, v26, s44
	v_add3_u32 v16, v28, v16, s44
	v_add3_u32 v4, v30, v4, s44
	v_and_b32_e32 v18, 0xffff0000, v18
	v_and_b32_e32 v26, 0xffff0000, v26
	v_or_b32_sdwa v27, v18, v4 dst_sel:DWORD dst_unused:UNUSED_PAD src0_sel:DWORD src1_sel:WORD_1
	v_or_b32_sdwa v26, v26, v16 dst_sel:DWORD dst_unused:UNUSED_PAD src0_sel:DWORD src1_sel:WORD_1
	global_store_dwordx2 v234, v[26:27], s[14:15] offset:1024 nt
	v_pk_mul_f32 v[26:27], v[30:31], v[30:31]
	v_pk_mul_f32 v[40:41], v[28:29], v[28:29]
	v_mov_b32_e32 v16, v19
	v_pk_mov_b32 v[46:47], v[40:41], v[26:27] op_sel:[1,0]
	v_mov_b32_e32 v41, v27
	v_pk_add_f32 v[26:27], v[40:41], v[46:47]
	v_pk_mul_f32 v[16:17], v[16:17], v[6:7] op_sel_hi:[1,0]
	v_pk_add_f32 v[40:41], v[26:27], v[26:27] op_sel_hi:[0,1]
	v_pk_mul_f32 v[26:27], v[20:21], v[6:7] op_sel_hi:[1,0]
	v_pk_fma_f32 v[20:21], v[54:55], v[16:17], v[146:147]
	v_pk_fma_f32 v[26:27], v[56:57], v[26:27], v[148:149]
	v_and_b32_sdwa v18, v21, v235 dst_sel:DWORD dst_unused:UNUSED_PAD src0_sel:WORD_1 src1_sel:DWORD
	v_and_b32_sdwa v17, v27, v235 dst_sel:DWORD dst_unused:UNUSED_PAD src0_sel:WORD_1 src1_sel:DWORD
	v_and_b32_sdwa v4, v26, v235 dst_sel:DWORD dst_unused:UNUSED_PAD src0_sel:WORD_1 src1_sel:DWORD
	v_and_b32_sdwa v16, v20, v235 dst_sel:DWORD dst_unused:UNUSED_PAD src0_sel:WORD_1 src1_sel:DWORD
	v_add3_u32 v17, v27, v17, s44
	v_add3_u32 v18, v21, v18, s44
	v_add3_u32 v16, v20, v16, s44
	v_add3_u32 v4, v26, v4, s44
	v_and_b32_e32 v17, 0xffff0000, v17
	v_and_b32_e32 v18, 0xffff0000, v18
	v_or_b32_sdwa v17, v17, v4 dst_sel:DWORD dst_unused:UNUSED_PAD src0_sel:DWORD src1_sel:WORD_1
	v_or_b32_sdwa v16, v18, v16 dst_sel:DWORD dst_unused:UNUSED_PAD src0_sel:DWORD src1_sel:WORD_1
	global_store_dwordx2 v234, v[16:17], s[14:15] offset:1536 nt
	v_mov_b32_e32 v16, v22
	v_mov_b32_e32 v17, v24
	v_mov_b32_e32 v24, v23
	v_pk_mul_f32 v[18:19], v[6:7], v[16:17] op_sel_hi:[0,1]
	v_pk_mul_f32 v[16:17], v[6:7], v[24:25] op_sel_hi:[0,1]
	v_mul_f32_e32 v4, v20, v20
	v_pk_fma_f32 v[16:17], v[60:61], v[16:17], v[144:145]
	v_pk_fma_f32 v[18:19], v[58:59], v[18:19], v[142:143]
	v_pk_fma_f32 v[46:47], v[20:21], v[20:21], v[4:5] op_sel_hi:[1,1,0]
	v_mul_f32_e32 v4, v26, v26
	v_and_b32_sdwa v23, v17, v235 dst_sel:DWORD dst_unused:UNUSED_PAD src0_sel:WORD_1 src1_sel:DWORD
	v_and_b32_sdwa v24, v19, v235 dst_sel:DWORD dst_unused:UNUSED_PAD src0_sel:WORD_1 src1_sel:DWORD
	v_pk_fma_f32 v[48:49], v[26:27], v[26:27], v[4:5] op_sel_hi:[1,1,0]
	v_and_b32_sdwa v4, v16, v235 dst_sel:DWORD dst_unused:UNUSED_PAD src0_sel:WORD_1 src1_sel:DWORD
	v_and_b32_sdwa v22, v18, v235 dst_sel:DWORD dst_unused:UNUSED_PAD src0_sel:WORD_1 src1_sel:DWORD
	v_add3_u32 v23, v17, v23, s44
	v_add3_u32 v24, v19, v24, s44
	v_add3_u32 v22, v18, v22, s44
	v_add3_u32 v4, v16, v4, s44
	v_and_b32_e32 v23, 0xffff0000, v23
	v_and_b32_e32 v24, 0xffff0000, v24
	v_or_b32_sdwa v23, v23, v4 dst_sel:DWORD dst_unused:UNUSED_PAD src0_sel:DWORD src1_sel:WORD_1
	v_or_b32_sdwa v22, v24, v22 dst_sel:DWORD dst_unused:UNUSED_PAD src0_sel:DWORD src1_sel:WORD_1
	v_mul_f32_e32 v46, v18, v18
	v_mul_f32_e32 v48, v19, v19
	v_mul_f32_e32 v38, v16, v16
	v_mul_f32_e32 v40, v17, v17
	global_store_dwordx2 v234, v[22:23], s[14:15] offset:2048 nt
	v_pk_add_f32 v[22:23], v[46:47], v[48:49]
	v_pk_add_f32 v[24:25], v[40:41], v[38:39]
	v_pk_mul_f32 v[10:11], v[6:7], v[10:11] op_sel_hi:[0,1]
	v_pk_add_f32 v[22:23], v[22:23], v[24:25]
	v_mov_b32_e32 v24, v13
	v_mov_b32_e32 v25, v15
	v_mov_b32_e32 v13, v14
	v_pk_mul_f32 v[24:25], v[6:7], v[24:25] op_sel_hi:[0,1]
	v_pk_mul_f32 v[12:13], v[6:7], v[12:13] op_sel_hi:[0,1]
	v_pk_fma_f32 v[12:13], v[66:67], v[12:13], v[138:139]
	v_pk_fma_f32 v[14:15], v[68:69], v[24:25], v[140:141]
	v_pk_add_f32 v[22:23], v[22:23], v[22:23] op_sel_hi:[0,1]
	v_and_b32_sdwa v24, v15, v235 dst_sel:DWORD dst_unused:UNUSED_PAD src0_sel:WORD_1 src1_sel:DWORD
	v_and_b32_sdwa v25, v13, v235 dst_sel:DWORD dst_unused:UNUSED_PAD src0_sel:WORD_1 src1_sel:DWORD
	v_and_b32_sdwa v4, v14, v235 dst_sel:DWORD dst_unused:UNUSED_PAD src0_sel:WORD_1 src1_sel:DWORD
	v_and_b32_sdwa v22, v12, v235 dst_sel:DWORD dst_unused:UNUSED_PAD src0_sel:WORD_1 src1_sel:DWORD
	v_add3_u32 v24, v15, v24, s44
	v_add3_u32 v25, v13, v25, s44
	v_add3_u32 v22, v12, v22, s44
	v_add3_u32 v4, v14, v4, s44
	v_and_b32_e32 v24, 0xffff0000, v24
	v_and_b32_e32 v38, 0xffff0000, v25
	v_or_b32_sdwa v25, v24, v4 dst_sel:DWORD dst_unused:UNUSED_PAD src0_sel:DWORD src1_sel:WORD_1
	v_or_b32_sdwa v24, v38, v22 dst_sel:DWORD dst_unused:UNUSED_PAD src0_sel:DWORD src1_sel:WORD_1
	v_pk_mul_f32 v[38:39], v[14:15], v[14:15]
	v_pk_mul_f32 v[40:41], v[12:13], v[12:13]
	v_pk_fma_f32 v[8:9], v[62:63], v[8:9], v[134:135]
	v_pk_mov_b32 v[46:47], v[40:41], v[38:39] op_sel:[1,0]
	v_mov_b32_e32 v41, v39
	v_pk_fma_f32 v[10:11], v[64:65], v[10:11], v[136:137]
	v_mul_f32_e32 v4, v8, v8
	v_pk_add_f32 v[38:39], v[40:41], v[46:47]
	v_pk_fma_f32 v[40:41], v[8:9], v[8:9], v[4:5] op_sel_hi:[1,1,0]
	v_mul_f32_e32 v4, v10, v10
	v_pk_fma_f32 v[46:47], v[10:11], v[10:11], v[4:5] op_sel_hi:[1,1,0]
	v_mov_b32_e32 v4, v7
	v_pk_mul_f32 v[4:5], v[4:5], v[6:7] op_sel_hi:[1,0]
	v_pk_mul_f32 v[2:3], v[2:3], v[6:7] op_sel_hi:[1,0]
	v_pk_add_f32 v[38:39], v[38:39], v[38:39] op_sel_hi:[0,1]
	s_waitcnt vmcnt(29)
	v_pk_fma_f32 v[2:3], v[52:53], v[2:3], v[132:133]
	v_pk_fma_f32 v[4:5], v[50:51], v[4:5], v[130:131]
	v_mul_f32_e32 v22, v2, v2
	v_mul_f32_e32 v40, v4, v4
	v_mul_f32_e32 v46, v5, v5
	v_mul_f32_e32 v38, v3, v3
	v_pk_add_f32 v[6:7], v[40:41], v[46:47]
	v_pk_add_f32 v[22:23], v[38:39], v[22:23]
	global_store_dwordx2 v234, v[24:25], s[14:15] offset:2560 nt
	v_pk_add_f32 v[6:7], v[6:7], v[22:23]
	v_and_b32_sdwa v24, v11, v235 dst_sel:DWORD dst_unused:UNUSED_PAD src0_sel:WORD_1 src1_sel:DWORD
	v_add_f32_e32 v6, v6, v7
	ds_bpermute_b32 v7, v171, v6
	v_and_b32_sdwa v22, v10, v235 dst_sel:DWORD dst_unused:UNUSED_PAD src0_sel:WORD_1 src1_sel:DWORD
	v_and_b32_sdwa v25, v9, v235 dst_sel:DWORD dst_unused:UNUSED_PAD src0_sel:WORD_1 src1_sel:DWORD
	v_add3_u32 v24, v11, v24, s44
	v_add3_u32 v22, v10, v22, s44
	s_waitcnt lgkmcnt(0)
	v_add_f32_e32 v6, v6, v7
	ds_bpermute_b32 v7, v226, v6
	v_and_b32_e32 v24, 0xffff0000, v24
	v_and_b32_sdwa v23, v8, v235 dst_sel:DWORD dst_unused:UNUSED_PAD src0_sel:WORD_1 src1_sel:DWORD
	v_add3_u32 v23, v8, v23, s44
	s_waitcnt lgkmcnt(0)
	v_add_f32_e32 v6, v6, v7
	ds_bpermute_b32 v38, v228, v6
	v_add3_u32 v7, v9, v25, s44
	v_and_b32_e32 v25, 0xffff0000, v7
	v_or_b32_sdwa v7, v24, v22 dst_sel:DWORD dst_unused:UNUSED_PAD src0_sel:DWORD src1_sel:WORD_1
	s_waitcnt lgkmcnt(0)
	v_add_f32_e32 v22, v6, v38
	ds_bpermute_b32 v24, v229, v22
	v_or_b32_sdwa v6, v25, v23 dst_sel:DWORD dst_unused:UNUSED_PAD src0_sel:DWORD src1_sel:WORD_1
	global_store_dwordx2 v234, v[6:7], s[14:15] offset:3072 nt
	v_and_b32_sdwa v7, v4, v235 dst_sel:DWORD dst_unused:UNUSED_PAD src0_sel:WORD_1 src1_sel:DWORD
	v_and_b32_sdwa v25, v5, v235 dst_sel:DWORD dst_unused:UNUSED_PAD src0_sel:WORD_1 src1_sel:DWORD
	s_waitcnt lgkmcnt(0)
	v_add_f32_e32 v22, v22, v24
	ds_bpermute_b32 v23, v230, v22
	v_add3_u32 v24, v4, v7, s44
	v_and_b32_sdwa v7, v3, v235 dst_sel:DWORD dst_unused:UNUSED_PAD src0_sel:WORD_1 src1_sel:DWORD
	v_and_b32_sdwa v6, v2, v235 dst_sel:DWORD dst_unused:UNUSED_PAD src0_sel:WORD_1 src1_sel:DWORD
	v_add3_u32 v7, v3, v7, s44
	s_waitcnt lgkmcnt(0)
	v_add_f32_e32 v22, v22, v23
	ds_bpermute_b32 v23, v231, v22
	v_add3_u32 v25, v5, v25, s44
	v_add3_u32 v6, v2, v6, s44
	v_and_b32_e32 v7, 0xffff0000, v7
	v_and_b32_e32 v25, 0xffff0000, v25
	s_waitcnt lgkmcnt(0)
	v_add_f32_e32 v22, v22, v23
	v_fmamk_f32 v22, v22, 0x3a000000, v232
	v_cmp_gt_f32_e32 vcc, s43, v22
	v_mul_f32_e32 v23, 0x4b800000, v22
	v_or_b32_sdwa v7, v7, v6 dst_sel:DWORD dst_unused:UNUSED_PAD src0_sel:DWORD src1_sel:WORD_1
	v_cndmask_b32_e32 v22, v22, v23, vcc
	v_rsq_f32_e32 v22, v22
	v_or_b32_sdwa v6, v25, v24 dst_sel:DWORD dst_unused:UNUSED_PAD src0_sel:DWORD src1_sel:WORD_1
	global_store_dwordx2 v234, v[6:7], s[14:15] offset:3584 nt
	v_mov_b32_e32 v38, 0
	v_mul_f32_e32 v6, 0x45800000, v22
	v_cndmask_b32_e32 v6, v22, v6, vcc
	v_pk_mul_f32 v[22:23], v[158:159], v[6:7] op_sel_hi:[1,0]
	v_pk_mul_f32 v[24:25], v[36:37], v[6:7] op_sel_hi:[1,0]
	v_pk_fma_f32 v[22:23], v[42:43], v[22:23], v[126:127]
	v_pk_fma_f32 v[24:25], v[44:45], v[24:25], v[128:129]
	v_bfe_u32 v7, v22, 16, 1
	v_bfe_u32 v36, v23, 16, 1
	v_add3_u32 v7, v22, v7, s44
	v_add3_u32 v36, v23, v36, s44
	v_med3_f32 v22, v22, s45, v236
	v_med3_f32 v23, v23, s45, v236
	v_lshrrev_b32_e32 v7, 16, v7
	v_cvt_pk_fp8_f32 v38, v22, v23
	v_and_or_b32 v36, v36, s42, v7
	v_bfe_u32 v7, v24, 16, 1
	v_add3_u32 v7, v24, v7, s44
	v_bfe_u32 v22, v25, 16, 1
	v_lshrrev_b32_e32 v7, 16, v7
	v_med3_f32 v23, v24, s45, v236
	v_med3_f32 v24, v25, s45, v236
	v_add3_u32 v22, v25, v22, s44
	v_cvt_pk_fp8_f32 v38, v23, v24 op_sel:[0,0,1]
	v_and_or_b32 v37, v22, s42, v7
	v_pk_mul_f32 v[22:23], v[32:33], v[6:7] op_sel_hi:[1,0]
	v_pk_mul_f32 v[24:25], v[34:35], v[6:7] op_sel_hi:[1,0]
	v_pk_fma_f32 v[22:23], v[106:107], v[22:23], v[110:111]
	v_mov_b32_e32 v34, 0
	v_bfe_u32 v7, v22, 16, 1
	v_bfe_u32 v32, v23, 16, 1
	v_add3_u32 v7, v22, v7, s44
	v_add3_u32 v32, v23, v32, s44
	v_med3_f32 v22, v22, s45, v236
	v_med3_f32 v23, v23, s45, v236
	v_pk_fma_f32 v[24:25], v[108:109], v[24:25], v[112:113]
	v_lshrrev_b32_e32 v7, 16, v7
	v_cvt_pk_fp8_f32 v34, v22, v23
	v_and_or_b32 v32, v32, s42, v7
	v_bfe_u32 v7, v24, 16, 1
	v_add3_u32 v7, v24, v7, s44
	v_bfe_u32 v22, v25, 16, 1
	v_lshrrev_b32_e32 v7, 16, v7
	v_med3_f32 v23, v24, s45, v236
	v_med3_f32 v24, v25, s45, v236
	v_add3_u32 v22, v25, v22, s44
	v_cvt_pk_fp8_f32 v34, v23, v24 op_sel:[0,0,1]
	v_and_or_b32 v33, v22, s42, v7
	v_pk_mul_f32 v[22:23], v[28:29], v[6:7] op_sel_hi:[1,0]
	v_pk_mul_f32 v[24:25], v[30:31], v[6:7] op_sel_hi:[1,0]
	v_pk_fma_f32 v[22:23], v[86:87], v[22:23], v[102:103]
	v_pk_fma_f32 v[24:25], v[88:89], v[24:25], v[104:105]
	v_bfe_u32 v7, v22, 16, 1
	v_add3_u32 v7, v22, v7, s44
	v_bfe_u32 v28, v23, 16, 1
	v_lshrrev_b32_e32 v7, 16, v7
	v_add3_u32 v28, v23, v28, s44
	v_and_or_b32 v28, v28, s42, v7
	v_bfe_u32 v7, v24, 16, 1
	v_med3_f32 v22, v22, s45, v236
	v_med3_f32 v23, v23, s45, v236
	v_mov_b32_e32 v30, 0
	v_add3_u32 v7, v24, v7, s44
	v_cvt_pk_fp8_f32 v30, v22, v23
	v_lshrrev_b32_e32 v7, 16, v7
	v_bfe_u32 v22, v25, 16, 1
	v_pk_mul_f32 v[20:21], v[20:21], v[6:7] op_sel_hi:[1,0]
	v_med3_f32 v23, v24, s45, v236
	v_med3_f32 v24, v25, s45, v236
	v_add3_u32 v22, v25, v22, s44
	v_pk_fma_f32 v[20:21], v[78:79], v[20:21], v[82:83]
	v_cvt_pk_fp8_f32 v30, v23, v24 op_sel:[0,0,1]
	v_and_or_b32 v29, v22, s42, v7
	v_pk_mul_f32 v[22:23], v[26:27], v[6:7] op_sel_hi:[1,0]
	v_bfe_u32 v7, v20, 16, 1
	v_add3_u32 v7, v20, v7, s44
	v_bfe_u32 v24, v21, 16, 1
	v_pk_fma_f32 v[22:23], v[80:81], v[22:23], v[84:85]
	v_lshrrev_b32_e32 v7, 16, v7
	v_add3_u32 v24, v21, v24, s44
	v_and_or_b32 v24, v24, s42, v7
	v_bfe_u32 v7, v22, 16, 1
	v_add3_u32 v7, v22, v7, s44
	v_lshrrev_b32_e32 v7, 16, v7
	v_med3_f32 v20, v20, s45, v236
	v_med3_f32 v21, v21, s45, v236
	v_mov_b32_e32 v26, 0
	v_cvt_pk_fp8_f32 v26, v20, v21
	v_bfe_u32 v20, v23, 16, 1
	v_pk_mul_f32 v[18:19], v[18:19], v[6:7] op_sel_hi:[1,0]
	v_add3_u32 v20, v23, v20, s44
	v_pk_fma_f32 v[18:19], v[70:71], v[18:19], v[74:75]
	v_and_or_b32 v25, v20, s42, v7
	v_pk_mul_f32 v[16:17], v[16:17], v[6:7] op_sel_hi:[1,0]
	v_bfe_u32 v7, v18, 16, 1
	v_med3_f32 v21, v22, s45, v236
	v_med3_f32 v22, v23, s45, v236
	v_add3_u32 v7, v18, v7, s44
	v_bfe_u32 v20, v19, 16, 1
	v_cvt_pk_fp8_f32 v26, v21, v22 op_sel:[0,0,1]
	v_pk_fma_f32 v[16:17], v[72:73], v[16:17], v[76:77]
	v_lshrrev_b32_e32 v7, 16, v7
	v_add3_u32 v20, v19, v20, s44
	v_med3_f32 v18, v18, s45, v236
	v_med3_f32 v19, v19, s45, v236
	v_mov_b32_e32 v22, 0
	v_and_or_b32 v20, v20, s42, v7
	v_bfe_u32 v7, v16, 16, 1
	v_cvt_pk_fp8_f32 v22, v18, v19
	v_add3_u32 v7, v16, v7, s44
	v_lshrrev_b32_e32 v7, 16, v7
	v_bfe_u32 v18, v17, 16, 1
	v_med3_f32 v16, v16, s45, v236
	v_med3_f32 v19, v17, s45, v236
	v_pk_mul_f32 v[12:13], v[12:13], v[6:7] op_sel_hi:[1,0]
	v_cvt_pk_fp8_f32 v22, v16, v19 op_sel:[0,0,1]
	v_add3_u32 v16, v17, v18, s44
	v_pk_fma_f32 v[12:13], v[90:91], v[12:13], v[98:99]
	v_and_or_b32 v21, v16, s42, v7
	v_pk_mul_f32 v[14:15], v[14:15], v[6:7] op_sel_hi:[1,0]
	v_bfe_u32 v7, v12, 16, 1
	v_add3_u32 v7, v12, v7, s44
	v_bfe_u32 v16, v13, 16, 1
	v_pk_fma_f32 v[14:15], v[92:93], v[14:15], v[100:101]
	v_lshrrev_b32_e32 v7, 16, v7
	v_add3_u32 v16, v13, v16, s44
	v_and_or_b32 v16, v16, s42, v7
	v_bfe_u32 v7, v14, 16, 1
	v_add3_u32 v7, v14, v7, s44
	v_lshrrev_b32_e32 v7, 16, v7
	v_med3_f32 v12, v12, s45, v236
	v_med3_f32 v13, v13, s45, v236
	v_mov_b32_e32 v18, 0
	v_cvt_pk_fp8_f32 v18, v12, v13
	v_bfe_u32 v12, v15, 16, 1
	v_pk_mul_f32 v[8:9], v[8:9], v[6:7] op_sel_hi:[1,0]
	v_add3_u32 v12, v15, v12, s44
	v_pk_fma_f32 v[8:9], v[94:95], v[8:9], v[118:119]
	v_and_or_b32 v17, v12, s42, v7
	v_pk_mul_f32 v[10:11], v[10:11], v[6:7] op_sel_hi:[1,0]
	v_bfe_u32 v7, v8, 16, 1
	v_add3_u32 v7, v8, v7, s44
	v_bfe_u32 v12, v9, 16, 1
	v_pk_fma_f32 v[10:11], v[96:97], v[10:11], v[120:121]
	v_lshrrev_b32_e32 v7, 16, v7
	v_add3_u32 v12, v9, v12, s44
	v_and_or_b32 v12, v12, s42, v7
	v_bfe_u32 v7, v10, 16, 1
	v_add3_u32 v7, v10, v7, s44
	v_med3_f32 v13, v14, s45, v236
	v_med3_f32 v14, v15, s45, v236
	v_lshrrev_b32_e32 v7, 16, v7
	v_cvt_pk_fp8_f32 v18, v13, v14 op_sel:[0,0,1]
	v_med3_f32 v8, v8, s45, v236
	v_med3_f32 v9, v9, s45, v236
	v_mov_b32_e32 v14, 0
	v_pk_mul_f32 v[4:5], v[4:5], v[6:7] op_sel_hi:[1,0]
	v_cvt_pk_fp8_f32 v14, v8, v9
	v_bfe_u32 v8, v11, 16, 1
	v_pk_fma_f32 v[4:5], v[114:115], v[4:5], v[122:123]
	v_add3_u32 v8, v11, v8, s44
	v_pk_mul_f32 v[2:3], v[2:3], v[6:7] op_sel_hi:[1,0]
	v_bfe_u32 v6, v4, 16, 1
	v_and_or_b32 v13, v8, s42, v7
	v_add3_u32 v6, v4, v6, s44
	v_bfe_u32 v7, v5, 16, 1
	v_pk_fma_f32 v[2:3], v[116:117], v[2:3], v[124:125]
	v_lshrrev_b32_e32 v6, 16, v6
	v_add3_u32 v7, v5, v7, s44
	v_and_or_b32 v6, v7, s42, v6
	v_bfe_u32 v7, v2, 16, 1
	v_add3_u32 v7, v2, v7, s44
	v_bfe_u32 v8, v3, 16, 1
	v_lshrrev_b32_e32 v7, 16, v7
	v_add3_u32 v8, v3, v8, s44
	v_and_or_b32 v7, v8, s42, v7
	v_med3_f32 v4, v4, s45, v236
	v_med3_f32 v5, v5, s45, v236
	v_mov_b32_e32 v8, 0
	v_cvt_pk_fp8_f32 v8, v4, v5
	s_add_u32 s14, s11, s24
	v_med3_f32 v2, v2, s45, v236
	v_med3_f32 v3, v3, s45, v236
	s_addc_u32 s15, s13, s25
	v_med3_f32 v9, v10, s45, v236
	v_med3_f32 v10, v11, s45, v236
	v_cvt_pk_fp8_f32 v8, v2, v3 op_sel:[0,0,1]
	s_add_u32 s4, s33, s22
	v_cvt_pk_fp8_f32 v14, v9, v10 op_sel:[0,0,1]
	s_addc_u32 s5, s34, s23
	s_add_i32 s46, s46, s81
	s_add_i32 s8, s8, s37
	s_cmpk_lt_i32 s46, 0x100
	global_store_dwordx2 v234, v[36:37], s[14:15]
	global_store_dword v237, v38, s[4:5]
	global_store_dwordx2 v234, v[32:33], s[14:15] offset:512
	global_store_dword v237, v34, s[4:5] offset:256
	global_store_dwordx2 v234, v[28:29], s[14:15] offset:1024
	global_store_dword v237, v30, s[4:5] offset:512
	global_store_dwordx2 v234, v[24:25], s[14:15] offset:1536
	global_store_dword v237, v26, s[4:5] offset:768
	global_store_dwordx2 v234, v[20:21], s[14:15] offset:2048
	global_store_dword v237, v22, s[4:5] offset:1024
	global_store_dwordx2 v234, v[16:17], s[14:15] offset:2560
	global_store_dword v237, v18, s[4:5] offset:1280
	global_store_dwordx2 v234, v[12:13], s[14:15] offset:3072
	global_store_dword v237, v14, s[4:5] offset:1536
	global_store_dwordx2 v234, v[6:7], s[14:15] offset:3584
	global_store_dword v237, v8, s[4:5] offset:1792
	s_cbranch_scc0 .LBB0_3481
.LBB0_3479:
	s_ashr_i32 s4, s46, 5
	s_cmp_eq_u32 s4, s47
	s_cbranch_scc1 .LBB0_3478
	s_mul_i32 s14, s4, 0x3000
	s_ashr_i32 s15, s14, 31
	s_lshl_b64 s[14:15], s[14:15], 2
	s_add_u32 s14, s2, s14
	s_addc_u32 s15, s3, s15
	v_lshl_add_u64 v[18:19], v[172:173], 2, s[14:15]
	v_add_co_u32_e32 v10, vcc, s38, v18
	s_waitcnt vmcnt(0)
	s_nop 0
	v_addc_co_u32_e32 v11, vcc, 0, v19, vcc
	v_add_co_u32_e32 v14, vcc, s39, v18
	s_barrier
	s_nop 0
	v_addc_co_u32_e32 v15, vcc, 0, v19, vcc
	global_load_dwordx4 v[2:5], v[174:175], off nt
	v_add_co_u32_e32 v18, vcc, s40, v18
	global_load_dwordx4 v[6:9], v[176:177], off nt
	s_nop 0
	global_load_dwordx4 v[10:13], v[10:11], off nt
	s_nop 0
	global_load_dwordx4 v[14:17], v[14:15], off nt
	v_addc_co_u32_e32 v19, vcc, 0, v19, vcc
	global_load_dwordx4 v[18:21], v[18:19], off nt
	s_mov_b32 s47, s4
	s_waitcnt vmcnt(2)
	v_pk_mul_f32 v[4:5], v[4:5], v[12:13]
	v_pk_mul_f32 v[2:3], v[2:3], v[10:11]
	ds_write_b128 v1, v[2:5]
	s_waitcnt vmcnt(1)
	v_pk_add_f32 v[2:3], v[16:17], 1.0 op_sel_hi:[1,0]
	v_pk_add_f32 v[10:11], v[14:15], 1.0 op_sel_hi:[1,0]
	v_pk_mul_f32 v[4:5], v[8:9], v[2:3]
	v_pk_mul_f32 v[2:3], v[6:7], v[10:11]
	s_waitcnt vmcnt(0)
	ds_write_b128 v1, v[18:21] offset:16384
	ds_write_b128 v1, v[2:5] offset:8192
	s_waitcnt lgkmcnt(0)
	s_barrier
	s_branch .LBB0_3478

.LBB0_4363:
	s_ashr_i32 s9, s8, 31
	s_lshl_b64 s[0:1], s[8:9], 12
	s_add_u32 s0, s20, s0
	s_addc_u32 s1, s21, s1
	v_lshlrev_b32_e32 v8, 3, v2
	global_load_dwordx2 v[22:23], v8, s[0:1] nt
	global_load_dwordx2 v[20:21], v8, s[0:1] offset:512 nt
	global_load_dwordx2 v[18:19], v8, s[0:1] offset:1024 nt
	global_load_dwordx2 v[16:17], v8, s[0:1] offset:1536 nt
	global_load_dwordx2 v[14:15], v8, s[0:1] offset:2048 nt
	global_load_dwordx2 v[12:13], v8, s[0:1] offset:2560 nt
	global_load_dwordx2 v[10:11], v8, s[0:1] offset:3072 nt
	s_nop 0
	global_load_dwordx2 v[8:9], v8, s[0:1] offset:3584 nt
	s_cmpk_lg_i32 s12, 0x47
	s_cselect_b64 s[10:11], -1, 0
	s_cmpk_eq_i32 s12, 0x47
	s_cbranch_scc1 .LBB0_4365
	s_add_i32 s0, s12, -7
	v_readlane_b32 s0, v41, s0
	s_ashr_i32 s1, s0, 31
	s_lshl_b64 s[0:1], s[0:1], 11
	s_add_u32 s0, s2, s0
	s_addc_u32 s1, s3, s1
	s_nop 0
	global_load_dword v49, v39, s[0:1]
	global_load_dword v48, v39, s[0:1] offset:256
	global_load_dword v47, v39, s[0:1] offset:512
	global_load_dword v46, v39, s[0:1] offset:768
	global_load_dword v45, v39, s[0:1] offset:1024
	global_load_dword v44, v39, s[0:1] offset:1280
	global_load_dword v43, v39, s[0:1] offset:1536
	global_load_dword v42, v39, s[0:1] offset:1792
	s_add_i32 s0, s12, -6
	v_readlane_b32 s0, v41, s0
	s_ashr_i32 s1, s0, 31
	s_lshl_b64 s[0:1], s[0:1], 11
	s_add_u32 s0, s2, s0
	s_addc_u32 s1, s3, s1
	s_nop 0
	global_load_dword v57, v39, s[0:1]
	global_load_dword v56, v39, s[0:1] offset:256
	global_load_dword v55, v39, s[0:1] offset:512
	global_load_dword v54, v39, s[0:1] offset:768
	global_load_dword v53, v39, s[0:1] offset:1024
	global_load_dword v52, v39, s[0:1] offset:1280
	global_load_dword v51, v39, s[0:1] offset:1536
	global_load_dword v50, v39, s[0:1] offset:1792
	s_add_i32 s0, s12, -5
	v_readlane_b32 s0, v41, s0
	s_ashr_i32 s1, s0, 31
	s_lshl_b64 s[0:1], s[0:1], 11
	s_add_u32 s0, s2, s0
	s_addc_u32 s1, s3, s1
	s_nop 0
	global_load_dword v65, v39, s[0:1]
	global_load_dword v64, v39, s[0:1] offset:256
	global_load_dword v63, v39, s[0:1] offset:512
	global_load_dword v62, v39, s[0:1] offset:768
	global_load_dword v61, v39, s[0:1] offset:1024
	global_load_dword v60, v39, s[0:1] offset:1280
	global_load_dword v59, v39, s[0:1] offset:1536
	global_load_dword v58, v39, s[0:1] offset:1792
